# compute segments of all GEMM K-loops: removed the already-satisfied lgkmcnt waits and the mid-segment setprio 0/1 pairs (on top of m0 save/restore removal)
# speedup vs baseline: 1.0027x; 1.0027x over previous
.LBB0_260:
	s_ashr_i32 s41, s40, 31
	s_lshl_b64 s[42:43], s[40:41], 19
	s_add_u32 s42, s54, s42
	s_addc_u32 s43, s55, s43
	s_and_b64 s[44:45], s[4:5], exec
	ds_read_b128 v[0:3], v219
	ds_read_b128 v[4:7], v219 offset:1024
	ds_read_b128 v[8:11], v219 offset:2048
	s_waitcnt vmcnt(2)
	ds_read_b128 v[12:15], v219 offset:3072
	s_waitcnt vmcnt(1)
	ds_read_b128 v[16:19], v220
	s_waitcnt vmcnt(0)
	ds_read_b128 v[20:23], v220 offset:1024
	ds_read_b128 v[24:27], v220 offset:2048
	ds_read_b128 v[28:31], v220 offset:3072
	s_cselect_b32 s7, s43, s13
	s_cselect_b32 s11, s42, s12
	s_ashr_i32 s39, s38, 31
	s_lshl_b64 s[44:45], s[38:39], 19
	s_add_u32 s44, s56, s44
	s_addc_u32 s45, s57, s45
	s_and_b64 s[46:47], s[4:5], exec
	s_cselect_b32 s39, s45, s9
	s_cselect_b32 s41, s44, s8
	s_add_u32 s46, s12, 0x100
	s_addc_u32 s47, s13, 0
	s_add_u32 s52, s8, 0x100
	s_addc_u32 s53, s9, 0
	s_add_u32 s48, s12, 0x180
	s_addc_u32 s49, s13, 0
	ds_read_b128 v[32:35], v221
	ds_read_b128 v[36:39], v221 offset:1024
	ds_read_b128 v[40:43], v221 offset:2048
	ds_read_b128 v[44:47], v221 offset:3072
	ds_read_b128 v[48:51], v221 offset:4096
	ds_read_b128 v[52:55], v221 offset:5120
	ds_read_b128 v[56:59], v221 offset:6144
	ds_read_b128 v[60:63], v221 offset:7168
	s_add_u32 s50, s8, 0x180
	s_addc_u32 s51, s9, 0
	s_add_u32 s76, s12, 0x40080
	s_addc_u32 s77, s13, 0
	s_add_i32 m0, s59, 0xc000
	s_nop 0
	global_load_lds_dwordx4 v215, s[76:77]
	s_nop 0
	s_add_i32 m0, s59, 0xe000
	s_nop 0
	global_load_lds_dwordx4 v217, s[76:77]
	s_waitcnt vmcnt(8)
	s_waitcnt lgkmcnt(0)
	s_barrier
	s_setprio 1
	s_waitcnt lgkmcnt(7)
	v_mfma_i32_16x16x64_i8 v[64:67], v[0:3], v[32:35], 0
	s_mov_b32 s76, 0
	v_mfma_i32_16x16x64_i8 v[68:71], v[8:11], v[32:35], 0
	s_waitcnt lgkmcnt(5)
	v_mfma_i32_16x16x64_i8 v[72:75], v[0:3], v[40:43], 0
	v_mfma_i32_16x16x64_i8 v[76:79], v[8:11], v[40:43], 0
	s_waitcnt lgkmcnt(3)
	v_mfma_i32_16x16x64_i8 v[84:87], v[8:11], v[48:51], 0
	s_waitcnt lgkmcnt(1)
	v_mfma_i32_16x16x64_i8 v[88:91], v[0:3], v[56:59], 0
	v_mfma_i32_16x16x64_i8 v[140:143], v[4:7], v[36:39], v[64:67]
	v_mfma_i32_16x16x64_i8 v[144:147], v[12:15], v[36:39], v[68:71]
	v_mfma_i32_16x16x64_i8 v[152:155], v[4:7], v[44:47], v[72:75]
	v_mfma_i32_16x16x64_i8 v[156:159], v[12:15], v[44:47], v[76:79]
	v_mfma_i32_16x16x64_i8 v[80:83], v[0:3], v[48:51], 0
	v_mfma_i32_16x16x64_i8 v[84:87], v[12:15], v[52:55], v[84:87]
	s_waitcnt lgkmcnt(0)
	v_mfma_i32_16x16x64_i8 v[88:91], v[4:7], v[60:63], v[88:91]
	v_mfma_i32_16x16x64_i8 v[92:95], v[8:11], v[56:59], 0
	v_mfma_i32_16x16x64_i8 v[80:83], v[4:7], v[52:55], v[80:83]
	v_mfma_i32_16x16x64_i8 v[92:95], v[12:15], v[60:63], v[92:95]
	s_setprio 0
	s_setprio 1
	v_mfma_i32_16x16x64_i8 v[96:99], v[16:19], v[32:35], 0
	v_mfma_i32_16x16x64_i8 v[32:35], v[24:27], v[32:35], 0
	v_mfma_i32_16x16x64_i8 v[96:99], v[20:23], v[36:39], v[96:99]
	v_mfma_i32_16x16x64_i8 v[32:35], v[28:31], v[36:39], v[32:35]
	v_mfma_i32_16x16x64_i8 v[36:39], v[16:19], v[40:43], 0
	v_mfma_i32_16x16x64_i8 v[40:43], v[24:27], v[40:43], 0
	v_mfma_i32_16x16x64_i8 v[36:39], v[20:23], v[44:47], v[36:39]
	v_mfma_i32_16x16x64_i8 v[40:43], v[28:31], v[44:47], v[40:43]
	v_mfma_i32_16x16x64_i8 v[44:47], v[16:19], v[48:51], 0
	v_mfma_i32_16x16x64_i8 v[48:51], v[24:27], v[48:51], 0
	v_mfma_i32_16x16x64_i8 v[44:47], v[20:23], v[52:55], v[44:47]
	v_mfma_i32_16x16x64_i8 v[48:51], v[28:31], v[52:55], v[48:51]
	v_mfma_i32_16x16x64_i8 v[52:55], v[16:19], v[56:59], 0
	v_mfma_i32_16x16x64_i8 v[56:59], v[24:27], v[56:59], 0
	v_mfma_i32_16x16x64_i8 v[52:55], v[20:23], v[60:63], v[52:55]
	v_mfma_i32_16x16x64_i8 v[56:59], v[28:31], v[60:63], v[56:59]
	s_setprio 0
	s_barrier
	ds_read_b128 v[60:63], v221 offset:16384
	ds_read_b128 v[100:103], v221 offset:17408
	ds_read_b128 v[104:107], v221 offset:18432
	ds_read_b128 v[108:111], v221 offset:19456
	ds_read_b128 v[112:115], v221 offset:20480
	ds_read_b128 v[116:119], v221 offset:21504
	ds_read_b128 v[120:123], v221 offset:22528
	ds_read_b128 v[124:127], v221 offset:23552
	s_add_i32 m0, s59, 0x10000
	s_nop 0
	global_load_lds_dwordx4 v216, s[52:53]
	s_nop 0
	s_add_i32 m0, s59, 0x12000
	s_nop 0
	global_load_lds_dwordx4 v218, s[52:53]
	s_add_u32 s52, s8, 0x40100
	s_addc_u32 s53, s9, 0
	s_add_i32 m0, s59, 0x14000
	s_nop 0
	global_load_lds_dwordx4 v216, s[52:53]
	s_nop 0
	s_add_i32 m0, s59, 0x16000
	s_nop 0
	global_load_lds_dwordx4 v218, s[52:53]
	s_nop 0
	s_add_i32 m0, s59, 0
	s_nop 0
	global_load_lds_dwordx4 v215, s[46:47]
	s_nop 0
	s_add_i32 m0, s59, 0x2000
	s_nop 0
	global_load_lds_dwordx4 v217, s[46:47]
	s_waitcnt vmcnt(8)
	s_waitcnt lgkmcnt(0)
	s_barrier
	s_setprio 1
	v_mfma_i32_16x16x64_i8 v[136:139], v[0:3], v[104:107], 0
	v_mfma_i32_16x16x64_i8 v[228:231], v[4:7], v[108:111], v[136:139]
	v_mfma_i32_16x16x64_i8 v[136:139], v[8:11], v[104:107], 0
	v_mfma_i32_16x16x64_i8 v[128:131], v[0:3], v[60:63], 0
	v_mfma_i32_16x16x64_i8 v[132:135], v[8:11], v[60:63], 0
	v_mfma_i32_16x16x64_i8 v[232:235], v[12:15], v[108:111], v[136:139]
	v_mfma_i32_16x16x64_i8 v[136:139], v[0:3], v[112:115], 0
	v_mfma_i32_16x16x64_i8 v[0:3], v[0:3], v[120:123], 0
	v_mfma_i32_16x16x64_i8 v[128:131], v[4:7], v[100:103], v[128:131]
	v_mfma_i32_16x16x64_i8 v[132:135], v[12:15], v[100:103], v[132:135]
	v_mfma_i32_16x16x64_i8 v[236:239], v[4:7], v[116:119], v[136:139]
	v_mfma_i32_16x16x64_i8 v[136:139], v[8:11], v[112:115], 0
	v_mfma_i32_16x16x64_i8 v[0:3], v[4:7], v[124:127], v[0:3]
	v_mfma_i32_16x16x64_i8 v[4:7], v[8:11], v[120:123], 0
	v_mfma_i32_16x16x64_i8 v[240:243], v[12:15], v[116:119], v[136:139]
	v_mfma_i32_16x16x64_i8 v[4:7], v[12:15], v[124:127], v[4:7]
	v_mfma_i32_16x16x64_i8 v[8:11], v[16:19], v[60:63], 0
	v_mfma_i32_16x16x64_i8 v[12:15], v[24:27], v[60:63], 0
	v_mfma_i32_16x16x64_i8 v[8:11], v[20:23], v[100:103], v[8:11]
	v_mfma_i32_16x16x64_i8 v[12:15], v[28:31], v[100:103], v[12:15]
	v_mfma_i32_16x16x64_i8 v[60:63], v[16:19], v[104:107], 0
	v_mfma_i32_16x16x64_i8 v[100:103], v[24:27], v[104:107], 0
	v_mfma_i32_16x16x64_i8 v[104:107], v[16:19], v[112:115], 0
	v_mfma_i32_16x16x64_i8 v[16:19], v[16:19], v[120:123], 0
	v_mfma_i32_16x16x64_i8 v[60:63], v[20:23], v[108:111], v[60:63]
	v_mfma_i32_16x16x64_i8 v[100:103], v[28:31], v[108:111], v[100:103]
	v_mfma_i32_16x16x64_i8 v[244:247], v[20:23], v[116:119], v[104:107]
	v_mfma_i32_16x16x64_i8 v[104:107], v[24:27], v[112:115], 0
	v_mfma_i32_16x16x64_i8 v[16:19], v[20:23], v[124:127], v[16:19]
	v_mfma_i32_16x16x64_i8 v[20:23], v[24:27], v[120:123], 0
	v_mfma_i32_16x16x64_i8 v[248:251], v[28:31], v[116:119], v[104:107]
	v_mfma_i32_16x16x64_i8 v[20:23], v[28:31], v[124:127], v[20:23]
	s_setprio 0
	s_barrier
	ds_read_b128 v[24:27], v222
	ds_read_b128 v[28:31], v222 offset:1024
	ds_read_b128 v[112:115], v222 offset:2048
	ds_read_b128 v[116:119], v222 offset:3072
	ds_read_b128 v[208:211], v223
	ds_read_b128 v[224:227], v223 offset:1024
	ds_read_b128 v[64:67], v223 offset:2048
	ds_read_b128 v[68:71], v223 offset:3072
	ds_read_b128 v[104:107], v221 offset:32768
	ds_read_b128 v[108:111], v221 offset:33792
	ds_read_b128 v[120:123], v221 offset:34816
	ds_read_b128 v[124:127], v221 offset:35840
	ds_read_b128 v[136:139], v221 offset:36864
	ds_read_b128 v[148:151], v221 offset:37888
	ds_read_b128 v[72:75], v221 offset:38912
	ds_read_b128 v[76:79], v221 offset:39936
	s_add_u32 s12, s12, 0x40100
	s_addc_u32 s13, s13, 0
	s_add_i32 m0, s59, 0x4000
	s_nop 0
	global_load_lds_dwordx4 v215, s[12:13]
	s_nop 0
	s_add_i32 m0, s59, 0x6000
	s_nop 0
	global_load_lds_dwordx4 v217, s[12:13]
	s_waitcnt vmcnt(8)
	s_waitcnt lgkmcnt(0)
	s_barrier
	s_setprio 1
	v_mfma_i32_16x16x64_i8 v[140:143], v[24:27], v[104:107], v[140:143]
	v_mfma_i32_16x16x64_i8 v[80:83], v[24:27], v[136:139], v[80:83]
	v_mfma_i32_16x16x64_i8 v[204:207], v[28:31], v[108:111], v[140:143]
	v_mfma_i32_16x16x64_i8 v[140:143], v[112:115], v[104:107], v[144:147]
	v_mfma_i32_16x16x64_i8 v[172:175], v[28:31], v[148:151], v[80:83]
	v_mfma_i32_16x16x64_i8 v[80:83], v[112:115], v[136:139], v[84:87]
	v_mfma_i32_16x16x64_i8 v[200:203], v[116:119], v[108:111], v[140:143]
	v_mfma_i32_16x16x64_i8 v[140:143], v[24:27], v[120:123], v[152:155]
	v_mfma_i32_16x16x64_i8 v[168:171], v[116:119], v[148:151], v[80:83]
	v_mfma_i32_16x16x64_i8 v[80:83], v[24:27], v[72:75], v[88:91]
	v_mfma_i32_16x16x64_i8 v[188:191], v[28:31], v[124:127], v[140:143]
	v_mfma_i32_16x16x64_i8 v[140:143], v[112:115], v[120:123], v[156:159]
	v_mfma_i32_16x16x64_i8 v[156:159], v[28:31], v[76:79], v[80:83]
	v_mfma_i32_16x16x64_i8 v[80:83], v[112:115], v[72:75], v[92:95]
	v_mfma_i32_16x16x64_i8 v[184:187], v[116:119], v[124:127], v[140:143]
	v_mfma_i32_16x16x64_i8 v[152:155], v[116:119], v[76:79], v[80:83]
	v_mfma_i32_16x16x64_i8 v[32:35], v[64:67], v[104:107], v[32:35]
	v_mfma_i32_16x16x64_i8 v[192:195], v[68:71], v[108:111], v[32:35]
	v_mfma_i32_16x16x64_i8 v[32:35], v[208:211], v[120:123], v[36:39]
	v_mfma_i32_16x16x64_i8 v[180:183], v[224:227], v[124:127], v[32:35]
	v_mfma_i32_16x16x64_i8 v[32:35], v[64:67], v[120:123], v[40:43]
	v_mfma_i32_16x16x64_i8 v[176:179], v[68:71], v[124:127], v[32:35]
	v_mfma_i32_16x16x64_i8 v[32:35], v[208:211], v[136:139], v[44:47]
	v_mfma_i32_16x16x64_i8 v[164:167], v[224:227], v[148:151], v[32:35]
	v_mfma_i32_16x16x64_i8 v[32:35], v[64:67], v[136:139], v[48:51]
	v_mfma_i32_16x16x64_i8 v[160:163], v[68:71], v[148:151], v[32:35]
	v_mfma_i32_16x16x64_i8 v[32:35], v[208:211], v[72:75], v[52:55]
	v_mfma_i32_16x16x64_i8 v[80:83], v[208:211], v[104:107], v[96:99]
	v_mfma_i32_16x16x64_i8 v[148:151], v[224:227], v[76:79], v[32:35]
	v_mfma_i32_16x16x64_i8 v[32:35], v[64:67], v[72:75], v[56:59]
	v_mfma_i32_16x16x64_i8 v[196:199], v[224:227], v[108:111], v[80:83]
	v_mfma_i32_16x16x64_i8 v[144:147], v[68:71], v[76:79], v[32:35]
	s_setprio 0
	s_barrier
	s_nop 3
	ds_read_b128 v[32:35], v221 offset:49152
	ds_read_b128 v[36:39], v221 offset:50176
	ds_read_b128 v[40:43], v221 offset:51200
	ds_read_b128 v[44:47], v221 offset:52224
	ds_read_b128 v[48:51], v221 offset:53248
	ds_read_b128 v[52:55], v221 offset:54272
	ds_read_b128 v[56:59], v221 offset:55296
	ds_read_b128 v[76:79], v221 offset:56320
	s_add_i32 m0, s59, 0x18000
	s_nop 0
	global_load_lds_dwordx4 v216, s[50:51]
	s_nop 0
	s_add_i32 m0, s59, 0x1a000
	s_nop 0
	global_load_lds_dwordx4 v218, s[50:51]
	s_add_u32 s12, s8, 0x40180
	s_addc_u32 s13, s9, 0
	s_add_i32 m0, s59, 0x1c000
	s_nop 0
	global_load_lds_dwordx4 v216, s[12:13]
	s_nop 0
	s_add_i32 m0, s59, 0x1e000
	s_nop 0
	global_load_lds_dwordx4 v218, s[12:13]
	s_nop 0
	s_add_i32 m0, s59, 0x8000
	s_nop 0
	global_load_lds_dwordx4 v215, s[48:49]
	s_nop 0
	s_add_i32 m0, s59, 0xa000
	s_nop 0
	global_load_lds_dwordx4 v217, s[48:49]
	s_waitcnt vmcnt(8)
	s_waitcnt lgkmcnt(0)
	s_barrier
	s_setprio 1
	v_mfma_i32_16x16x64_i8 v[72:75], v[24:27], v[32:35], v[128:131]
	v_mfma_i32_16x16x64_i8 v[140:143], v[28:31], v[36:39], v[72:75]
	v_mfma_i32_16x16x64_i8 v[72:75], v[112:115], v[32:35], v[132:135]
	v_mfma_i32_16x16x64_i8 v[136:139], v[116:119], v[36:39], v[72:75]
	v_mfma_i32_16x16x64_i8 v[72:75], v[24:27], v[40:43], v[228:231]
	v_mfma_i32_16x16x64_i8 v[124:127], v[28:31], v[44:47], v[72:75]
	v_mfma_i32_16x16x64_i8 v[72:75], v[112:115], v[40:43], v[232:235]
	v_mfma_i32_16x16x64_i8 v[120:123], v[116:119], v[44:47], v[72:75]
	v_mfma_i32_16x16x64_i8 v[72:75], v[24:27], v[48:51], v[236:239]
	v_mfma_i32_16x16x64_i8 v[0:3], v[24:27], v[56:59], v[0:3]
	v_mfma_i32_16x16x64_i8 v[108:111], v[28:31], v[52:55], v[72:75]
	v_mfma_i32_16x16x64_i8 v[72:75], v[112:115], v[48:51], v[240:243]
	v_mfma_i32_16x16x64_i8 v[88:91], v[28:31], v[76:79], v[0:3]
	v_mfma_i32_16x16x64_i8 v[0:3], v[112:115], v[56:59], v[4:7]
	v_mfma_i32_16x16x64_i8 v[104:107], v[116:119], v[52:55], v[72:75]
	v_mfma_i32_16x16x64_i8 v[84:87], v[116:119], v[76:79], v[0:3]
	v_mfma_i32_16x16x64_i8 v[0:3], v[208:211], v[32:35], v[8:11]
	v_mfma_i32_16x16x64_i8 v[132:135], v[224:227], v[36:39], v[0:3]
	v_mfma_i32_16x16x64_i8 v[0:3], v[64:67], v[32:35], v[12:15]
	v_mfma_i32_16x16x64_i8 v[128:131], v[68:71], v[36:39], v[0:3]
	v_mfma_i32_16x16x64_i8 v[0:3], v[208:211], v[40:43], v[60:63]
	v_mfma_i32_16x16x64_i8 v[116:119], v[224:227], v[44:47], v[0:3]
	v_mfma_i32_16x16x64_i8 v[0:3], v[64:67], v[40:43], v[100:103]
	v_mfma_i32_16x16x64_i8 v[112:115], v[68:71], v[44:47], v[0:3]
	v_mfma_i32_16x16x64_i8 v[0:3], v[208:211], v[48:51], v[244:247]
	v_mfma_i32_16x16x64_i8 v[100:103], v[224:227], v[52:55], v[0:3]
	v_mfma_i32_16x16x64_i8 v[0:3], v[64:67], v[48:51], v[248:251]
	v_mfma_i32_16x16x64_i8 v[96:99], v[68:71], v[52:55], v[0:3]
	v_mfma_i32_16x16x64_i8 v[0:3], v[208:211], v[56:59], v[16:19]
	v_mfma_i32_16x16x64_i8 v[72:75], v[224:227], v[76:79], v[0:3]
	v_mfma_i32_16x16x64_i8 v[0:3], v[64:67], v[56:59], v[20:23]
	v_mfma_i32_16x16x64_i8 v[68:71], v[68:71], v[76:79], v[0:3]
	s_setprio 0
	s_barrier
	s_add_u32 s77, s8, 0x200
	s_addc_u32 s80, s9, 0
.LBB0_261:
	s_nop 2
	ds_read_b128 v[0:3], v219
	ds_read_b128 v[4:7], v219 offset:1024
	ds_read_b128 v[8:11], v219 offset:2048
	ds_read_b128 v[12:15], v219 offset:3072
	ds_read_b128 v[16:19], v220
	ds_read_b128 v[20:23], v220 offset:1024
	ds_read_b128 v[24:27], v220 offset:2048
	ds_read_b128 v[28:31], v220 offset:3072
	s_add_u32 s8, s46, 0x100
	s_addc_u32 s9, s47, 0
	s_cmp_eq_u32 s76, 12
	s_cselect_b32 s52, s11, s8
	s_cselect_b32 s53, s7, s9
	s_cselect_b32 s48, s41, s77
	s_cselect_b32 s49, s39, s80
	s_add_u32 s12, s52, 0x80
	s_addc_u32 s13, s53, 0
	ds_read_b128 v[32:35], v221
	ds_read_b128 v[36:39], v221 offset:1024
	ds_read_b128 v[40:43], v221 offset:2048
	ds_read_b128 v[44:47], v221 offset:3072
	ds_read_b128 v[48:51], v221 offset:4096
	ds_read_b128 v[52:55], v221 offset:5120
	ds_read_b128 v[56:59], v221 offset:6144
	ds_read_b128 v[60:63], v221 offset:7168
	s_add_u32 s50, s48, 0x80
	s_addc_u32 s51, s49, 0
	s_add_u32 s46, s46, 0x40080
	s_addc_u32 s47, s47, 0
	s_add_i32 m0, s59, 0xc000
	s_nop 0
	global_load_lds_dwordx4 v215, s[46:47]
	s_nop 0
	s_add_i32 m0, s59, 0xe000
	s_nop 0
	global_load_lds_dwordx4 v217, s[46:47]
	s_waitcnt vmcnt(8)
	s_waitcnt lgkmcnt(0)
	s_barrier
	s_setprio 1
	v_mfma_i32_16x16x64_i8 v[172:175], v[0:3], v[48:51], v[172:175]
	v_mfma_i32_16x16x64_i8 v[168:171], v[8:11], v[48:51], v[168:171]
	v_mfma_i32_16x16x64_i8 v[156:159], v[0:3], v[56:59], v[156:159]
	v_mfma_i32_16x16x64_i8 v[152:155], v[8:11], v[56:59], v[152:155]
	v_mfma_i32_16x16x64_i8 v[64:67], v[0:3], v[32:35], v[204:207]
	v_mfma_i32_16x16x64_i8 v[76:79], v[8:11], v[32:35], v[200:203]
	v_mfma_i32_16x16x64_i8 v[80:83], v[0:3], v[40:43], v[188:191]
	v_mfma_i32_16x16x64_i8 v[92:95], v[8:11], v[40:43], v[184:187]
	v_mfma_i32_16x16x64_i8 v[172:175], v[4:7], v[52:55], v[172:175]
	v_mfma_i32_16x16x64_i8 v[168:171], v[12:15], v[52:55], v[168:171]
	v_mfma_i32_16x16x64_i8 v[156:159], v[4:7], v[60:63], v[156:159]
	v_mfma_i32_16x16x64_i8 v[152:155], v[12:15], v[60:63], v[152:155]
	v_mfma_i32_16x16x64_i8 v[64:67], v[4:7], v[36:39], v[64:67]
	v_mfma_i32_16x16x64_i8 v[76:79], v[12:15], v[36:39], v[76:79]
	v_mfma_i32_16x16x64_i8 v[80:83], v[4:7], v[44:47], v[80:83]
	v_mfma_i32_16x16x64_i8 v[92:95], v[12:15], v[44:47], v[92:95]
	v_mfma_i32_16x16x64_i8 v[184:187], v[16:19], v[32:35], v[196:199]
	v_mfma_i32_16x16x64_i8 v[32:35], v[24:27], v[32:35], v[192:195]
	v_mfma_i32_16x16x64_i8 v[196:199], v[20:23], v[36:39], v[184:187]
	v_mfma_i32_16x16x64_i8 v[32:35], v[28:31], v[36:39], v[32:35]
	v_mfma_i32_16x16x64_i8 v[36:39], v[16:19], v[40:43], v[180:183]
	v_mfma_i32_16x16x64_i8 v[40:43], v[24:27], v[40:43], v[176:179]
	v_mfma_i32_16x16x64_i8 v[36:39], v[20:23], v[44:47], v[36:39]
	v_mfma_i32_16x16x64_i8 v[40:43], v[28:31], v[44:47], v[40:43]
	v_mfma_i32_16x16x64_i8 v[44:47], v[16:19], v[48:51], v[164:167]
	v_mfma_i32_16x16x64_i8 v[48:51], v[24:27], v[48:51], v[160:163]
	v_mfma_i32_16x16x64_i8 v[44:47], v[20:23], v[52:55], v[44:47]
	v_mfma_i32_16x16x64_i8 v[48:51], v[28:31], v[52:55], v[48:51]
	v_mfma_i32_16x16x64_i8 v[52:55], v[16:19], v[56:59], v[148:151]
	v_mfma_i32_16x16x64_i8 v[56:59], v[24:27], v[56:59], v[144:147]
	v_mfma_i32_16x16x64_i8 v[52:55], v[20:23], v[60:63], v[52:55]
	v_mfma_i32_16x16x64_i8 v[56:59], v[28:31], v[60:63], v[56:59]
	s_setprio 0
	s_barrier
	ds_read_b128 v[60:63], v221 offset:16384
	ds_read_b128 v[144:147], v221 offset:17408
	ds_read_b128 v[148:151], v221 offset:18432
	ds_read_b128 v[160:163], v221 offset:19456
	ds_read_b128 v[164:167], v221 offset:20480
	ds_read_b128 v[176:179], v221 offset:21504
	ds_read_b128 v[180:183], v221 offset:22528
	ds_read_b128 v[184:187], v221 offset:23552
	s_add_i32 m0, s59, 0x10000
	s_nop 0
	global_load_lds_dwordx4 v216, s[48:49]
	s_nop 0
	s_add_i32 m0, s59, 0x12000
	s_nop 0
	global_load_lds_dwordx4 v218, s[48:49]
	s_add_u32 s46, s48, 0x40000
	s_addc_u32 s47, s49, 0
	s_add_i32 m0, s59, 0x14000
	s_nop 0
	global_load_lds_dwordx4 v216, s[46:47]
	s_nop 0
	s_add_i32 m0, s59, 0x16000
	s_nop 0
	global_load_lds_dwordx4 v218, s[46:47]
	s_nop 0
	s_add_i32 m0, s59, 0
	s_nop 0
	global_load_lds_dwordx4 v215, s[52:53]
	s_nop 0
	s_add_i32 m0, s59, 0x2000
	s_nop 0
	global_load_lds_dwordx4 v217, s[52:53]
	s_waitcnt vmcnt(8)
	s_waitcnt lgkmcnt(0)
	s_barrier
	s_setprio 1
	v_mfma_i32_16x16x64_i8 v[140:143], v[0:3], v[60:63], v[140:143]
	v_mfma_i32_16x16x64_i8 v[124:127], v[0:3], v[148:151], v[124:127]
	v_mfma_i32_16x16x64_i8 v[108:111], v[0:3], v[164:167], v[108:111]
	v_mfma_i32_16x16x64_i8 v[0:3], v[0:3], v[180:183], v[88:91]
	v_mfma_i32_16x16x64_i8 v[136:139], v[8:11], v[60:63], v[136:139]
	v_mfma_i32_16x16x64_i8 v[120:123], v[8:11], v[148:151], v[120:123]
	v_mfma_i32_16x16x64_i8 v[104:107], v[8:11], v[164:167], v[104:107]
	v_mfma_i32_16x16x64_i8 v[88:91], v[4:7], v[184:187], v[0:3]
	v_mfma_i32_16x16x64_i8 v[0:3], v[8:11], v[180:183], v[84:87]
	v_mfma_i32_16x16x64_i8 v[140:143], v[4:7], v[144:147], v[140:143]
	v_mfma_i32_16x16x64_i8 v[136:139], v[12:15], v[144:147], v[136:139]
	v_mfma_i32_16x16x64_i8 v[124:127], v[4:7], v[160:163], v[124:127]
	v_mfma_i32_16x16x64_i8 v[120:123], v[12:15], v[160:163], v[120:123]
	v_mfma_i32_16x16x64_i8 v[108:111], v[4:7], v[176:179], v[108:111]
	v_mfma_i32_16x16x64_i8 v[104:107], v[12:15], v[176:179], v[104:107]
	v_mfma_i32_16x16x64_i8 v[84:87], v[12:15], v[184:187], v[0:3]
	v_mfma_i32_16x16x64_i8 v[0:3], v[16:19], v[60:63], v[132:135]
	v_mfma_i32_16x16x64_i8 v[132:135], v[20:23], v[144:147], v[0:3]
	v_mfma_i32_16x16x64_i8 v[0:3], v[24:27], v[60:63], v[128:131]
	v_mfma_i32_16x16x64_i8 v[128:131], v[28:31], v[144:147], v[0:3]
	v_mfma_i32_16x16x64_i8 v[0:3], v[16:19], v[148:151], v[116:119]
	v_mfma_i32_16x16x64_i8 v[116:119], v[20:23], v[160:163], v[0:3]
	v_mfma_i32_16x16x64_i8 v[0:3], v[24:27], v[148:151], v[112:115]
	v_mfma_i32_16x16x64_i8 v[112:115], v[28:31], v[160:163], v[0:3]
	v_mfma_i32_16x16x64_i8 v[0:3], v[16:19], v[164:167], v[100:103]
	v_mfma_i32_16x16x64_i8 v[100:103], v[20:23], v[176:179], v[0:3]
	v_mfma_i32_16x16x64_i8 v[0:3], v[24:27], v[164:167], v[96:99]
	v_mfma_i32_16x16x64_i8 v[96:99], v[28:31], v[176:179], v[0:3]
	v_mfma_i32_16x16x64_i8 v[0:3], v[16:19], v[180:183], v[72:75]
	v_mfma_i32_16x16x64_i8 v[72:75], v[20:23], v[184:187], v[0:3]
	v_mfma_i32_16x16x64_i8 v[0:3], v[24:27], v[180:183], v[68:71]
	v_mfma_i32_16x16x64_i8 v[68:71], v[28:31], v[184:187], v[0:3]
	s_setprio 0
	s_barrier
	ds_read_b128 v[16:19], v222
	ds_read_b128 v[8:11], v222 offset:1024
	ds_read_b128 v[4:7], v222 offset:2048
	s_nop 1
	ds_read_b128 v[0:3], v222 offset:3072
	ds_read_b128 v[28:31], v223
	ds_read_b128 v[24:27], v223 offset:1024
	ds_read_b128 v[20:23], v223 offset:2048
	ds_read_b128 v[12:15], v223 offset:3072
	ds_read_b128 v[60:63], v221 offset:32768
	ds_read_b128 v[144:147], v221 offset:33792
	ds_read_b128 v[148:151], v221 offset:34816
	ds_read_b128 v[160:163], v221 offset:35840
	ds_read_b128 v[208:211], v221 offset:36864
	ds_read_b128 v[224:227], v221 offset:37888
	ds_read_b128 v[228:231], v221 offset:38912
	ds_read_b128 v[232:235], v221 offset:39936
	s_add_u32 s46, s52, 0x40000
	s_addc_u32 s47, s53, 0
	s_add_i32 m0, s59, 0x4000
	s_nop 0
	global_load_lds_dwordx4 v215, s[46:47]
	s_nop 0
	s_add_i32 m0, s59, 0x6000
	s_nop 0
	global_load_lds_dwordx4 v217, s[46:47]
	s_waitcnt vmcnt(8)
	s_waitcnt lgkmcnt(0)
	s_barrier
	s_setprio 1
	v_mfma_i32_16x16x64_i8 v[64:67], v[16:19], v[60:63], v[64:67]
	v_mfma_i32_16x16x64_i8 v[204:207], v[8:11], v[144:147], v[64:67]
	v_mfma_i32_16x16x64_i8 v[64:67], v[4:7], v[60:63], v[76:79]
	v_mfma_i32_16x16x64_i8 v[200:203], v[0:3], v[144:147], v[64:67]
	v_mfma_i32_16x16x64_i8 v[64:67], v[16:19], v[148:151], v[80:83]
	v_mfma_i32_16x16x64_i8 v[188:191], v[8:11], v[160:163], v[64:67]
	v_mfma_i32_16x16x64_i8 v[64:67], v[4:7], v[148:151], v[92:95]
	v_mfma_i32_16x16x64_i8 v[184:187], v[0:3], v[160:163], v[64:67]
	v_mfma_i32_16x16x64_i8 v[64:67], v[16:19], v[208:211], v[172:175]
	v_mfma_i32_16x16x64_i8 v[172:175], v[8:11], v[224:227], v[64:67]
	v_mfma_i32_16x16x64_i8 v[64:67], v[4:7], v[208:211], v[168:171]
	v_mfma_i32_16x16x64_i8 v[168:171], v[0:3], v[224:227], v[64:67]
	v_mfma_i32_16x16x64_i8 v[64:67], v[16:19], v[228:231], v[156:159]
	v_mfma_i32_16x16x64_i8 v[156:159], v[8:11], v[232:235], v[64:67]
	v_mfma_i32_16x16x64_i8 v[64:67], v[4:7], v[228:231], v[152:155]
	v_mfma_i32_16x16x64_i8 v[152:155], v[0:3], v[232:235], v[64:67]
	v_mfma_i32_16x16x64_i8 v[32:35], v[20:23], v[60:63], v[32:35]
	v_mfma_i32_16x16x64_i8 v[192:195], v[12:15], v[144:147], v[32:35]
	v_mfma_i32_16x16x64_i8 v[32:35], v[28:31], v[148:151], v[36:39]
	v_mfma_i32_16x16x64_i8 v[180:183], v[24:27], v[160:163], v[32:35]
	v_mfma_i32_16x16x64_i8 v[32:35], v[20:23], v[148:151], v[40:43]
	v_mfma_i32_16x16x64_i8 v[176:179], v[12:15], v[160:163], v[32:35]
	v_mfma_i32_16x16x64_i8 v[32:35], v[28:31], v[208:211], v[44:47]
	v_mfma_i32_16x16x64_i8 v[164:167], v[24:27], v[224:227], v[32:35]
	v_mfma_i32_16x16x64_i8 v[32:35], v[20:23], v[208:211], v[48:51]
	v_mfma_i32_16x16x64_i8 v[160:163], v[12:15], v[224:227], v[32:35]
	v_mfma_i32_16x16x64_i8 v[32:35], v[28:31], v[228:231], v[52:55]
	v_mfma_i32_16x16x64_i8 v[64:67], v[28:31], v[60:63], v[196:199]
	v_mfma_i32_16x16x64_i8 v[148:151], v[24:27], v[232:235], v[32:35]
	v_mfma_i32_16x16x64_i8 v[32:35], v[20:23], v[228:231], v[56:59]
	v_mfma_i32_16x16x64_i8 v[196:199], v[24:27], v[144:147], v[64:67]
	v_mfma_i32_16x16x64_i8 v[144:147], v[12:15], v[232:235], v[32:35]
	s_setprio 0
	s_barrier
	ds_read_b128 v[60:63], v221 offset:49152
	ds_read_b128 v[56:59], v221 offset:50176
	ds_read_b128 v[52:55], v221 offset:51200
	ds_read_b128 v[48:51], v221 offset:52224
	ds_read_b128 v[44:47], v221 offset:53248
	ds_read_b128 v[40:43], v221 offset:54272
	ds_read_b128 v[36:39], v221 offset:55296
	ds_read_b128 v[32:35], v221 offset:56320
	s_add_i32 m0, s59, 0x18000
	s_nop 0
	global_load_lds_dwordx4 v216, s[50:51]
	s_nop 0
	s_add_i32 m0, s59, 0x1a000
	s_nop 0
	global_load_lds_dwordx4 v218, s[50:51]
	s_add_u32 s46, s48, 0x40080
	s_addc_u32 s47, s49, 0
	s_add_i32 m0, s59, 0x1c000
	s_nop 0
	global_load_lds_dwordx4 v216, s[46:47]
	s_nop 0
	s_add_i32 m0, s59, 0x1e000
	s_nop 0
	global_load_lds_dwordx4 v218, s[46:47]
	s_nop 0
	s_add_i32 m0, s59, 0x8000
	s_nop 0
	global_load_lds_dwordx4 v215, s[12:13]
	s_nop 0
	s_add_i32 m0, s59, 0xa000
	s_nop 0
	global_load_lds_dwordx4 v217, s[12:13]
	s_waitcnt vmcnt(8)
	s_waitcnt lgkmcnt(0)
	s_barrier
	s_setprio 1
	v_mfma_i32_16x16x64_i8 v[64:67], v[16:19], v[60:63], v[140:143]
	v_mfma_i32_16x16x64_i8 v[140:143], v[8:11], v[56:59], v[64:67]
	v_mfma_i32_16x16x64_i8 v[64:67], v[4:7], v[60:63], v[136:139]
	v_mfma_i32_16x16x64_i8 v[136:139], v[0:3], v[56:59], v[64:67]
	v_mfma_i32_16x16x64_i8 v[64:67], v[16:19], v[52:55], v[124:127]
	v_mfma_i32_16x16x64_i8 v[124:127], v[8:11], v[48:51], v[64:67]
	v_mfma_i32_16x16x64_i8 v[64:67], v[4:7], v[52:55], v[120:123]
	v_mfma_i32_16x16x64_i8 v[120:123], v[0:3], v[48:51], v[64:67]
	v_mfma_i32_16x16x64_i8 v[64:67], v[16:19], v[44:47], v[108:111]
	v_mfma_i32_16x16x64_i8 v[108:111], v[8:11], v[40:43], v[64:67]
	v_mfma_i32_16x16x64_i8 v[64:67], v[4:7], v[44:47], v[104:107]
	v_mfma_i32_16x16x64_i8 v[104:107], v[0:3], v[40:43], v[64:67]
	v_mfma_i32_16x16x64_i8 v[64:67], v[16:19], v[36:39], v[88:91]
	v_mfma_i32_16x16x64_i8 v[88:91], v[8:11], v[32:35], v[64:67]
	v_mfma_i32_16x16x64_i8 v[64:67], v[4:7], v[36:39], v[84:87]
	v_mfma_i32_16x16x64_i8 v[84:87], v[0:3], v[32:35], v[64:67]
	v_mfma_i32_16x16x64_i8 v[64:67], v[28:31], v[60:63], v[132:135]
	v_mfma_i32_16x16x64_i8 v[132:135], v[24:27], v[56:59], v[64:67]
	v_mfma_i32_16x16x64_i8 v[64:67], v[20:23], v[60:63], v[128:131]
	v_mfma_i32_16x16x64_i8 v[128:131], v[12:15], v[56:59], v[64:67]
	v_mfma_i32_16x16x64_i8 v[64:67], v[28:31], v[52:55], v[116:119]
	v_mfma_i32_16x16x64_i8 v[116:119], v[24:27], v[48:51], v[64:67]
	v_mfma_i32_16x16x64_i8 v[64:67], v[20:23], v[52:55], v[112:115]
	v_mfma_i32_16x16x64_i8 v[112:115], v[12:15], v[48:51], v[64:67]
	v_mfma_i32_16x16x64_i8 v[64:67], v[28:31], v[44:47], v[100:103]
	v_mfma_i32_16x16x64_i8 v[100:103], v[24:27], v[40:43], v[64:67]
	v_mfma_i32_16x16x64_i8 v[64:67], v[20:23], v[44:47], v[96:99]
	v_mfma_i32_16x16x64_i8 v[96:99], v[12:15], v[40:43], v[64:67]
	v_mfma_i32_16x16x64_i8 v[64:67], v[28:31], v[36:39], v[72:75]
	v_mfma_i32_16x16x64_i8 v[72:75], v[24:27], v[32:35], v[64:67]
	v_mfma_i32_16x16x64_i8 v[64:67], v[20:23], v[36:39], v[68:71]
	v_mfma_i32_16x16x64_i8 v[68:71], v[12:15], v[32:35], v[64:67]
	s_setprio 0
	s_barrier
	s_add_i32 s76, s76, 2
	s_add_u32 s77, s77, 0x100
	s_addc_u32 s80, s80, 0
	s_cmp_gt_u32 s76, 13
	s_mov_b64 s[46:47], s[8:9]
	s_cbranch_scc0 .LBB0_261
	s_and_b64 vcc, exec, s[28:29]
	s_cbranch_vccz .LBB0_264
	s_barrier

.LBB0_602:
	s_ashr_i32 s25, s24, 31
	s_lshl_b64 s[26:27], s[24:25], 20
	s_add_u32 s26, s44, s26
	s_addc_u32 s27, s45, s27
	s_and_b64 s[28:29], s[4:5], exec
	s_waitcnt lgkmcnt(0)
	ds_read_b128 v[0:3], v217
	ds_read_b128 v[4:7], v217 offset:1024
	ds_read_b128 v[8:11], v217 offset:2048
	ds_read_b128 v[12:15], v217 offset:3072
	ds_read_b128 v[16:19], v218
	ds_read_b128 v[20:23], v218 offset:1024
	ds_read_b128 v[24:27], v218 offset:2048
	ds_read_b128 v[28:31], v218 offset:3072
	s_cselect_b32 s7, s27, s35
	s_cselect_b32 s9, s26, s34
	s_ashr_i32 s23, s22, 31
	s_lshl_b64 s[28:29], s[22:23], 20
	s_add_u32 s28, s46, s28
	s_addc_u32 s29, s47, s29
	s_and_b64 s[36:37], s[4:5], exec
	s_cselect_b32 s23, s29, s31
	s_cselect_b32 s25, s28, s30
	s_add_u32 s36, s34, 0x100
	s_addc_u32 s37, s35, 0
	s_add_u32 s42, s30, 0x100
	s_addc_u32 s43, s31, 0
	s_add_u32 s38, s34, 0x180
	s_addc_u32 s39, s35, 0
	ds_read_b128 v[32:35], v219
	ds_read_b128 v[36:39], v219 offset:1024
	ds_read_b128 v[40:43], v219 offset:2048
	ds_read_b128 v[44:47], v219 offset:3072
	ds_read_b128 v[48:51], v219 offset:4096
	ds_read_b128 v[52:55], v219 offset:5120
	ds_read_b128 v[56:59], v219 offset:6144
	ds_read_b128 v[60:63], v219 offset:7168
	s_add_u32 s40, s30, 0x180
	s_addc_u32 s41, s31, 0
	s_add_u32 s60, s34, 0x80080
	s_addc_u32 s61, s35, 0
	s_add_i32 m0, s48, 0xc000
	s_nop 0
	global_load_lds_dwordx4 v213, s[60:61]
	s_nop 0
	s_add_i32 m0, s48, 0xe000
	s_nop 0
	global_load_lds_dwordx4 v214, s[60:61]
	s_waitcnt vmcnt(8)
	s_waitcnt lgkmcnt(0)
	s_barrier
	s_setprio 1
	v_mfma_f32_16x16x32_bf16 v[64:67], v[0:3], v[32:35], 0
	v_mfma_f32_16x16x32_bf16 v[68:71], v[8:11], v[32:35], 0
	v_mfma_f32_16x16x32_bf16 v[72:75], v[0:3], v[40:43], 0
	v_mfma_f32_16x16x32_bf16 v[76:79], v[8:11], v[40:43], 0
	v_mfma_f32_16x16x32_bf16 v[80:83], v[0:3], v[48:51], 0
	v_mfma_f32_16x16x32_bf16 v[84:87], v[8:11], v[48:51], 0
	v_mfma_f32_16x16x32_bf16 v[88:91], v[0:3], v[56:59], 0
	v_mfma_f32_16x16x32_bf16 v[64:67], v[4:7], v[36:39], v[64:67]
	v_mfma_f32_16x16x32_bf16 v[68:71], v[12:15], v[36:39], v[68:71]
	v_mfma_f32_16x16x32_bf16 v[72:75], v[4:7], v[44:47], v[72:75]
	v_mfma_f32_16x16x32_bf16 v[76:79], v[12:15], v[44:47], v[76:79]
	v_mfma_f32_16x16x32_bf16 v[80:83], v[4:7], v[52:55], v[80:83]
	v_mfma_f32_16x16x32_bf16 v[84:87], v[12:15], v[52:55], v[84:87]
	v_mfma_f32_16x16x32_bf16 v[96:99], v[4:7], v[60:63], v[88:91]
	v_mfma_f32_16x16x32_bf16 v[88:91], v[8:11], v[56:59], 0
	v_mfma_f32_16x16x32_bf16 v[100:103], v[12:15], v[60:63], v[88:91]
	v_mfma_f32_16x16x32_bf16 v[88:91], v[16:19], v[32:35], 0
	v_mfma_f32_16x16x32_bf16 v[32:35], v[24:27], v[32:35], 0
	v_mfma_f32_16x16x32_bf16 v[104:107], v[20:23], v[36:39], v[88:91]
	v_mfma_f32_16x16x32_bf16 v[32:35], v[28:31], v[36:39], v[32:35]
	v_mfma_f32_16x16x32_bf16 v[36:39], v[16:19], v[40:43], 0
	v_mfma_f32_16x16x32_bf16 v[40:43], v[24:27], v[40:43], 0
	v_mfma_f32_16x16x32_bf16 v[36:39], v[20:23], v[44:47], v[36:39]
	v_mfma_f32_16x16x32_bf16 v[40:43], v[28:31], v[44:47], v[40:43]
	v_mfma_f32_16x16x32_bf16 v[44:47], v[16:19], v[48:51], 0
	v_mfma_f32_16x16x32_bf16 v[48:51], v[24:27], v[48:51], 0
	v_mfma_f32_16x16x32_bf16 v[44:47], v[20:23], v[52:55], v[44:47]
	v_mfma_f32_16x16x32_bf16 v[48:51], v[28:31], v[52:55], v[48:51]
	v_mfma_f32_16x16x32_bf16 v[52:55], v[16:19], v[56:59], 0
	v_mfma_f32_16x16x32_bf16 v[56:59], v[24:27], v[56:59], 0
	v_mfma_f32_16x16x32_bf16 v[52:55], v[20:23], v[60:63], v[52:55]
	v_mfma_f32_16x16x32_bf16 v[56:59], v[28:31], v[60:63], v[56:59]
	s_setprio 0
	s_barrier
	ds_read_b128 v[60:63], v219 offset:16384
	ds_read_b128 v[88:91], v219 offset:17408
	ds_read_b128 v[92:95], v219 offset:18432
	ds_read_b128 v[108:111], v219 offset:19456
	ds_read_b128 v[112:115], v219 offset:20480
	ds_read_b128 v[116:119], v219 offset:21504
	ds_read_b128 v[120:123], v219 offset:22528
	ds_read_b128 v[124:127], v219 offset:23552
	s_add_i32 m0, s48, 0x10000
	s_nop 0
	global_load_lds_dwordx4 v213, s[42:43]
	s_nop 0
	s_add_i32 m0, s48, 0x12000
	s_nop 0
	global_load_lds_dwordx4 v214, s[42:43]
	s_add_u32 s42, s30, 0x80100
	s_addc_u32 s43, s31, 0
	s_add_i32 m0, s48, 0x14000
	s_nop 0
	global_load_lds_dwordx4 v213, s[42:43]
	s_nop 0
	s_add_i32 m0, s48, 0x16000
	s_nop 0
	global_load_lds_dwordx4 v214, s[42:43]
	s_nop 0
	s_add_i32 m0, s48, 0
	s_nop 0
	global_load_lds_dwordx4 v213, s[36:37]
	s_nop 0
	s_add_i32 m0, s48, 0x2000
	s_nop 0
	global_load_lds_dwordx4 v214, s[36:37]
	s_waitcnt vmcnt(8)
	s_waitcnt lgkmcnt(0)
	s_barrier
	s_setprio 1
	v_mfma_f32_16x16x32_bf16 v[128:131], v[0:3], v[60:63], 0
	v_mfma_f32_16x16x32_bf16 v[132:135], v[4:7], v[88:91], v[128:131]
	v_mfma_f32_16x16x32_bf16 v[128:131], v[8:11], v[60:63], 0
	v_mfma_f32_16x16x32_bf16 v[140:143], v[12:15], v[88:91], v[128:131]
	v_mfma_f32_16x16x32_bf16 v[128:131], v[0:3], v[92:95], 0
	v_mfma_f32_16x16x32_bf16 v[148:151], v[4:7], v[108:111], v[128:131]
	v_mfma_f32_16x16x32_bf16 v[128:131], v[8:11], v[92:95], 0
	v_mfma_f32_16x16x32_bf16 v[156:159], v[12:15], v[108:111], v[128:131]
	v_mfma_f32_16x16x32_bf16 v[128:131], v[0:3], v[112:115], 0
	v_mfma_f32_16x16x32_bf16 v[0:3], v[0:3], v[120:123], 0
	v_mfma_f32_16x16x32_bf16 v[160:163], v[4:7], v[116:119], v[128:131]
	v_mfma_f32_16x16x32_bf16 v[0:3], v[4:7], v[124:127], v[0:3]
	v_mfma_f32_16x16x32_bf16 v[4:7], v[8:11], v[120:123], 0
	v_mfma_f32_16x16x32_bf16 v[128:131], v[8:11], v[112:115], 0
	v_mfma_f32_16x16x32_bf16 v[4:7], v[12:15], v[124:127], v[4:7]
	v_mfma_f32_16x16x32_bf16 v[164:167], v[12:15], v[116:119], v[128:131]
	v_mfma_f32_16x16x32_bf16 v[8:11], v[16:19], v[60:63], 0
	v_mfma_f32_16x16x32_bf16 v[168:171], v[20:23], v[88:91], v[8:11]
	v_mfma_f32_16x16x32_bf16 v[8:11], v[24:27], v[60:63], 0
	v_mfma_f32_16x16x32_bf16 v[172:175], v[28:31], v[88:91], v[8:11]
	v_mfma_f32_16x16x32_bf16 v[8:11], v[16:19], v[92:95], 0
	v_mfma_f32_16x16x32_bf16 v[176:179], v[20:23], v[108:111], v[8:11]
	v_mfma_f32_16x16x32_bf16 v[8:11], v[24:27], v[92:95], 0
	v_mfma_f32_16x16x32_bf16 v[108:111], v[28:31], v[108:111], v[8:11]
	v_mfma_f32_16x16x32_bf16 v[8:11], v[16:19], v[112:115], 0
	v_mfma_f32_16x16x32_bf16 v[180:183], v[20:23], v[116:119], v[8:11]
	v_mfma_f32_16x16x32_bf16 v[8:11], v[24:27], v[112:115], 0
	v_mfma_f32_16x16x32_bf16 v[116:119], v[28:31], v[116:119], v[8:11]
	v_mfma_f32_16x16x32_bf16 v[8:11], v[16:19], v[120:123], 0
	v_mfma_f32_16x16x32_bf16 v[184:187], v[20:23], v[124:127], v[8:11]
	v_mfma_f32_16x16x32_bf16 v[8:11], v[24:27], v[120:123], 0
	v_mfma_f32_16x16x32_bf16 v[124:127], v[28:31], v[124:127], v[8:11]
	s_setprio 0
	s_barrier
	s_nop 4
	ds_read_b128 v[8:11], v220
	ds_read_b128 v[12:15], v220 offset:1024
	ds_read_b128 v[16:19], v220 offset:2048
	ds_read_b128 v[20:23], v220 offset:3072
	ds_read_b128 v[194:197], v221
	ds_read_b128 v[198:201], v221 offset:1024
	ds_read_b128 v[202:205], v221 offset:2048
	ds_read_b128 v[206:209], v221 offset:3072
	ds_read_b128 v[24:27], v219 offset:32768
	ds_read_b128 v[28:31], v219 offset:33792
	ds_read_b128 v[60:63], v219 offset:34816
	ds_read_b128 v[224:227], v219 offset:35840
	ds_read_b128 v[228:231], v219 offset:36864
	ds_read_b128 v[232:235], v219 offset:37888
	ds_read_b128 v[236:239], v219 offset:38912
	ds_read_b128 v[240:243], v219 offset:39936
	s_add_u32 s34, s34, 0x80100
	s_addc_u32 s35, s35, 0
	s_add_i32 m0, s48, 0x4000
	s_nop 0
	global_load_lds_dwordx4 v213, s[34:35]
	s_nop 0
	s_add_i32 m0, s48, 0x6000
	s_nop 0
	global_load_lds_dwordx4 v214, s[34:35]
	s_waitcnt vmcnt(8)
	s_waitcnt lgkmcnt(0)
	s_barrier
	s_setprio 1
	v_mfma_f32_16x16x32_bf16 v[64:67], v[8:11], v[24:27], v[64:67]
	v_mfma_f32_16x16x32_bf16 v[152:155], v[12:15], v[28:31], v[64:67]
	v_mfma_f32_16x16x32_bf16 v[64:67], v[16:19], v[24:27], v[68:71]
	v_mfma_f32_16x16x32_bf16 v[144:147], v[20:23], v[28:31], v[64:67]
	v_mfma_f32_16x16x32_bf16 v[64:67], v[8:11], v[60:63], v[72:75]
	v_mfma_f32_16x16x32_bf16 v[120:123], v[12:15], v[224:227], v[64:67]
	v_mfma_f32_16x16x32_bf16 v[64:67], v[16:19], v[60:63], v[76:79]
	v_mfma_f32_16x16x32_bf16 v[112:115], v[20:23], v[224:227], v[64:67]
	v_mfma_f32_16x16x32_bf16 v[64:67], v[8:11], v[228:231], v[80:83]
	v_mfma_f32_16x16x32_bf16 v[92:95], v[12:15], v[232:235], v[64:67]
	v_mfma_f32_16x16x32_bf16 v[64:67], v[16:19], v[228:231], v[84:87]
	v_mfma_f32_16x16x32_bf16 v[88:91], v[20:23], v[232:235], v[64:67]
	v_mfma_f32_16x16x32_bf16 v[64:67], v[8:11], v[236:239], v[96:99]
	v_mfma_f32_16x16x32_bf16 v[76:79], v[12:15], v[240:243], v[64:67]
	v_mfma_f32_16x16x32_bf16 v[64:67], v[16:19], v[236:239], v[100:103]
	v_mfma_f32_16x16x32_bf16 v[72:75], v[20:23], v[240:243], v[64:67]
	v_mfma_f32_16x16x32_bf16 v[64:67], v[194:197], v[24:27], v[104:107]
	v_mfma_f32_16x16x32_bf16 v[24:27], v[202:205], v[24:27], v[32:35]
	v_mfma_f32_16x16x32_bf16 v[128:131], v[206:209], v[28:31], v[24:27]
	v_mfma_f32_16x16x32_bf16 v[24:27], v[194:197], v[60:63], v[36:39]
	v_mfma_f32_16x16x32_bf16 v[104:107], v[198:201], v[224:227], v[24:27]
	v_mfma_f32_16x16x32_bf16 v[24:27], v[202:205], v[60:63], v[40:43]
	v_mfma_f32_16x16x32_bf16 v[96:99], v[206:209], v[224:227], v[24:27]
	v_mfma_f32_16x16x32_bf16 v[24:27], v[194:197], v[228:231], v[44:47]
	v_mfma_f32_16x16x32_bf16 v[84:87], v[198:201], v[232:235], v[24:27]
	v_mfma_f32_16x16x32_bf16 v[24:27], v[202:205], v[228:231], v[48:51]
	v_mfma_f32_16x16x32_bf16 v[80:83], v[206:209], v[232:235], v[24:27]
	v_mfma_f32_16x16x32_bf16 v[24:27], v[194:197], v[236:239], v[52:55]
	v_mfma_f32_16x16x32_bf16 v[68:71], v[198:201], v[240:243], v[24:27]
	v_mfma_f32_16x16x32_bf16 v[24:27], v[202:205], v[236:239], v[56:59]
	v_mfma_f32_16x16x32_bf16 v[136:139], v[198:201], v[28:31], v[64:67]
	v_mfma_f32_16x16x32_bf16 v[64:67], v[206:209], v[240:243], v[24:27]
	s_setprio 0
	s_barrier
	ds_read_b128 v[32:35], v219 offset:49152
	ds_read_b128 v[36:39], v219 offset:50176
	ds_read_b128 v[100:103], v219 offset:51200
	ds_read_b128 v[224:227], v219 offset:52224
	ds_read_b128 v[228:231], v219 offset:53248
	ds_read_b128 v[232:235], v219 offset:54272
	ds_read_b128 v[236:239], v219 offset:55296
	ds_read_b128 v[240:243], v219 offset:56320
	s_add_i32 m0, s48, 0x18000
	s_nop 0
	global_load_lds_dwordx4 v213, s[40:41]
	s_nop 0
	s_add_i32 m0, s48, 0x1a000
	s_nop 0
	global_load_lds_dwordx4 v214, s[40:41]
	s_add_u32 s34, s30, 0x80180
	s_addc_u32 s35, s31, 0
	s_add_i32 m0, s48, 0x1c000
	s_nop 0
	global_load_lds_dwordx4 v213, s[34:35]
	s_nop 0
	s_add_i32 m0, s48, 0x1e000
	s_nop 0
	global_load_lds_dwordx4 v214, s[34:35]
	s_nop 0
	s_add_i32 m0, s48, 0x8000
	s_nop 0
	global_load_lds_dwordx4 v213, s[38:39]
	s_nop 0
	s_add_i32 m0, s48, 0xa000
	s_nop 0
	global_load_lds_dwordx4 v214, s[38:39]
	s_waitcnt vmcnt(8)
	s_waitcnt lgkmcnt(0)
	s_barrier
	s_setprio 1
	v_mfma_f32_16x16x32_bf16 v[24:27], v[8:11], v[32:35], v[132:135]
	v_mfma_f32_16x16x32_bf16 v[60:63], v[12:15], v[36:39], v[24:27]
	v_mfma_f32_16x16x32_bf16 v[24:27], v[16:19], v[32:35], v[140:143]
	v_mfma_f32_16x16x32_bf16 v[56:59], v[20:23], v[36:39], v[24:27]
	v_mfma_f32_16x16x32_bf16 v[24:27], v[8:11], v[100:103], v[148:151]
	v_mfma_f32_16x16x32_bf16 v[44:47], v[12:15], v[224:227], v[24:27]
	v_mfma_f32_16x16x32_bf16 v[24:27], v[16:19], v[100:103], v[156:159]
	v_mfma_f32_16x16x32_bf16 v[40:43], v[20:23], v[224:227], v[24:27]
	v_mfma_f32_16x16x32_bf16 v[24:27], v[8:11], v[228:231], v[160:163]
	v_mfma_f32_16x16x32_bf16 v[0:3], v[8:11], v[236:239], v[0:3]
	v_mfma_f32_16x16x32_bf16 v[28:31], v[12:15], v[232:235], v[24:27]
	v_mfma_f32_16x16x32_bf16 v[24:27], v[16:19], v[228:231], v[164:167]
	v_mfma_f32_16x16x32_bf16 v[12:15], v[12:15], v[240:243], v[0:3]
	v_mfma_f32_16x16x32_bf16 v[0:3], v[16:19], v[236:239], v[4:7]
	v_mfma_f32_16x16x32_bf16 v[24:27], v[20:23], v[232:235], v[24:27]
	v_mfma_f32_16x16x32_bf16 v[8:11], v[20:23], v[240:243], v[0:3]
	v_mfma_f32_16x16x32_bf16 v[0:3], v[194:197], v[32:35], v[168:171]
	v_mfma_f32_16x16x32_bf16 v[52:55], v[198:201], v[36:39], v[0:3]
	v_mfma_f32_16x16x32_bf16 v[0:3], v[202:205], v[32:35], v[172:175]
	v_mfma_f32_16x16x32_bf16 v[48:51], v[206:209], v[36:39], v[0:3]
	v_mfma_f32_16x16x32_bf16 v[0:3], v[194:197], v[100:103], v[176:179]
	v_mfma_f32_16x16x32_bf16 v[36:39], v[198:201], v[224:227], v[0:3]
	v_mfma_f32_16x16x32_bf16 v[0:3], v[202:205], v[100:103], v[108:111]
	v_mfma_f32_16x16x32_bf16 v[32:35], v[206:209], v[224:227], v[0:3]
	v_mfma_f32_16x16x32_bf16 v[0:3], v[194:197], v[228:231], v[180:183]
	v_mfma_f32_16x16x32_bf16 v[20:23], v[198:201], v[232:235], v[0:3]
	v_mfma_f32_16x16x32_bf16 v[0:3], v[202:205], v[228:231], v[116:119]
	v_mfma_f32_16x16x32_bf16 v[16:19], v[206:209], v[232:235], v[0:3]
	v_mfma_f32_16x16x32_bf16 v[0:3], v[194:197], v[236:239], v[184:187]
	v_mfma_f32_16x16x32_bf16 v[4:7], v[198:201], v[240:243], v[0:3]
	v_mfma_f32_16x16x32_bf16 v[0:3], v[202:205], v[236:239], v[124:127]
	v_mfma_f32_16x16x32_bf16 v[0:3], v[206:209], v[240:243], v[0:3]
	s_setprio 0
	s_barrier
	s_add_u32 s59, s30, 0x200
	s_addc_u32 s60, s31, 0
	s_mov_b32 s61, 0
.LBB0_603:
	ds_read_b128 v[100:103], v217
	ds_read_b128 v[108:111], v217 offset:1024
	ds_read_b128 v[116:119], v217 offset:2048
	ds_read_b128 v[124:127], v217 offset:3072
	ds_read_b128 v[132:135], v218
	ds_read_b128 v[140:143], v218 offset:1024
	ds_read_b128 v[148:151], v218 offset:2048
	ds_read_b128 v[156:159], v218 offset:3072
	s_add_u32 s30, s36, 0x100
	s_addc_u32 s31, s37, 0
	s_cmp_eq_u32 s61, 28
	s_cselect_b32 s42, s9, s30
	s_cselect_b32 s43, s7, s31
	s_cselect_b32 s38, s25, s59
	s_cselect_b32 s39, s23, s60
	s_add_u32 s34, s42, 0x80
	s_addc_u32 s35, s43, 0
	ds_read_b128 v[160:163], v219
	ds_read_b128 v[164:167], v219 offset:1024
	ds_read_b128 v[168:171], v219 offset:2048
	ds_read_b128 v[172:175], v219 offset:3072
	ds_read_b128 v[176:179], v219 offset:4096
	ds_read_b128 v[180:183], v219 offset:5120
	ds_read_b128 v[184:187], v219 offset:6144
	ds_read_b128 v[194:197], v219 offset:7168
	s_add_u32 s40, s38, 0x80
	s_addc_u32 s41, s39, 0
	s_add_u32 s36, s36, 0x80080
	s_addc_u32 s37, s37, 0
	s_add_i32 m0, s48, 0xc000
	s_nop 0
	global_load_lds_dwordx4 v213, s[36:37]
	s_nop 0
	s_add_i32 m0, s48, 0xe000
	s_nop 0
	global_load_lds_dwordx4 v214, s[36:37]
	s_waitcnt vmcnt(8)
	s_waitcnt lgkmcnt(0)
	s_barrier
	s_setprio 1
	v_mfma_f32_16x16x32_bf16 v[152:155], v[100:103], v[160:163], v[152:155]
	v_mfma_f32_16x16x32_bf16 v[144:147], v[116:119], v[160:163], v[144:147]
	v_mfma_f32_16x16x32_bf16 v[120:123], v[100:103], v[168:171], v[120:123]
	v_mfma_f32_16x16x32_bf16 v[112:115], v[116:119], v[168:171], v[112:115]
	v_mfma_f32_16x16x32_bf16 v[92:95], v[100:103], v[176:179], v[92:95]
	v_mfma_f32_16x16x32_bf16 v[88:91], v[116:119], v[176:179], v[88:91]
	v_mfma_f32_16x16x32_bf16 v[76:79], v[100:103], v[184:187], v[76:79]
	v_mfma_f32_16x16x32_bf16 v[72:75], v[116:119], v[184:187], v[72:75]
	v_mfma_f32_16x16x32_bf16 v[152:155], v[108:111], v[164:167], v[152:155]
	v_mfma_f32_16x16x32_bf16 v[144:147], v[124:127], v[164:167], v[144:147]
	v_mfma_f32_16x16x32_bf16 v[120:123], v[108:111], v[172:175], v[120:123]
	v_mfma_f32_16x16x32_bf16 v[112:115], v[124:127], v[172:175], v[112:115]
	v_mfma_f32_16x16x32_bf16 v[92:95], v[108:111], v[180:183], v[92:95]
	v_mfma_f32_16x16x32_bf16 v[88:91], v[124:127], v[180:183], v[88:91]
	v_mfma_f32_16x16x32_bf16 v[76:79], v[108:111], v[194:197], v[76:79]
	v_mfma_f32_16x16x32_bf16 v[72:75], v[124:127], v[194:197], v[72:75]
	v_mfma_f32_16x16x32_bf16 v[136:139], v[132:135], v[160:163], v[136:139]
	v_mfma_f32_16x16x32_bf16 v[128:131], v[148:151], v[160:163], v[128:131]
	v_mfma_f32_16x16x32_bf16 v[104:107], v[132:135], v[168:171], v[104:107]
	v_mfma_f32_16x16x32_bf16 v[96:99], v[148:151], v[168:171], v[96:99]
	v_mfma_f32_16x16x32_bf16 v[84:87], v[132:135], v[176:179], v[84:87]
	v_mfma_f32_16x16x32_bf16 v[80:83], v[148:151], v[176:179], v[80:83]
	v_mfma_f32_16x16x32_bf16 v[68:71], v[132:135], v[184:187], v[68:71]
	v_mfma_f32_16x16x32_bf16 v[64:67], v[148:151], v[184:187], v[64:67]
	v_mfma_f32_16x16x32_bf16 v[136:139], v[140:143], v[164:167], v[136:139]
	v_mfma_f32_16x16x32_bf16 v[128:131], v[156:159], v[164:167], v[128:131]
	v_mfma_f32_16x16x32_bf16 v[104:107], v[140:143], v[172:175], v[104:107]
	v_mfma_f32_16x16x32_bf16 v[96:99], v[156:159], v[172:175], v[96:99]
	v_mfma_f32_16x16x32_bf16 v[84:87], v[140:143], v[180:183], v[84:87]
	v_mfma_f32_16x16x32_bf16 v[80:83], v[156:159], v[180:183], v[80:83]
	v_mfma_f32_16x16x32_bf16 v[68:71], v[140:143], v[194:197], v[68:71]
	v_mfma_f32_16x16x32_bf16 v[64:67], v[156:159], v[194:197], v[64:67]
	s_setprio 0
	s_barrier
	ds_read_b128 v[160:163], v219 offset:16384
	ds_read_b128 v[164:167], v219 offset:17408
	ds_read_b128 v[168:171], v219 offset:18432
	ds_read_b128 v[172:175], v219 offset:19456
	ds_read_b128 v[176:179], v219 offset:20480
	ds_read_b128 v[180:183], v219 offset:21504
	ds_read_b128 v[184:187], v219 offset:22528
	ds_read_b128 v[194:197], v219 offset:23552
	s_add_i32 m0, s48, 0x10000
	s_nop 0
	global_load_lds_dwordx4 v213, s[38:39]
	s_nop 0
	s_add_i32 m0, s48, 0x12000
	s_nop 0
	global_load_lds_dwordx4 v214, s[38:39]
	s_add_u32 s36, s38, 0x80000
	s_addc_u32 s37, s39, 0
	s_add_i32 m0, s48, 0x14000
	s_nop 0
	global_load_lds_dwordx4 v213, s[36:37]
	s_nop 0
	s_add_i32 m0, s48, 0x16000
	s_nop 0
	global_load_lds_dwordx4 v214, s[36:37]
	s_nop 0
	s_add_i32 m0, s48, 0
	s_nop 0
	global_load_lds_dwordx4 v213, s[42:43]
	s_nop 0
	s_add_i32 m0, s48, 0x2000
	s_nop 0
	global_load_lds_dwordx4 v214, s[42:43]
	s_waitcnt vmcnt(8)
	s_waitcnt lgkmcnt(0)
	s_barrier
	s_setprio 1
	v_mfma_f32_16x16x32_bf16 v[60:63], v[100:103], v[160:163], v[60:63]
	v_mfma_f32_16x16x32_bf16 v[56:59], v[116:119], v[160:163], v[56:59]
	v_mfma_f32_16x16x32_bf16 v[44:47], v[100:103], v[168:171], v[44:47]
	v_mfma_f32_16x16x32_bf16 v[40:43], v[116:119], v[168:171], v[40:43]
	v_mfma_f32_16x16x32_bf16 v[28:31], v[100:103], v[176:179], v[28:31]
	v_mfma_f32_16x16x32_bf16 v[24:27], v[116:119], v[176:179], v[24:27]
	v_mfma_f32_16x16x32_bf16 v[12:15], v[100:103], v[184:187], v[12:15]
	v_mfma_f32_16x16x32_bf16 v[8:11], v[116:119], v[184:187], v[8:11]
	v_mfma_f32_16x16x32_bf16 v[60:63], v[108:111], v[164:167], v[60:63]
	v_mfma_f32_16x16x32_bf16 v[56:59], v[124:127], v[164:167], v[56:59]
	v_mfma_f32_16x16x32_bf16 v[44:47], v[108:111], v[172:175], v[44:47]
	v_mfma_f32_16x16x32_bf16 v[40:43], v[124:127], v[172:175], v[40:43]
	v_mfma_f32_16x16x32_bf16 v[28:31], v[108:111], v[180:183], v[28:31]
	v_mfma_f32_16x16x32_bf16 v[24:27], v[124:127], v[180:183], v[24:27]
	v_mfma_f32_16x16x32_bf16 v[12:15], v[108:111], v[194:197], v[12:15]
	v_mfma_f32_16x16x32_bf16 v[8:11], v[124:127], v[194:197], v[8:11]
	v_mfma_f32_16x16x32_bf16 v[52:55], v[132:135], v[160:163], v[52:55]
	v_mfma_f32_16x16x32_bf16 v[48:51], v[148:151], v[160:163], v[48:51]
	v_mfma_f32_16x16x32_bf16 v[36:39], v[132:135], v[168:171], v[36:39]
	v_mfma_f32_16x16x32_bf16 v[32:35], v[148:151], v[168:171], v[32:35]
	v_mfma_f32_16x16x32_bf16 v[20:23], v[132:135], v[176:179], v[20:23]
	v_mfma_f32_16x16x32_bf16 v[16:19], v[148:151], v[176:179], v[16:19]
	v_mfma_f32_16x16x32_bf16 v[4:7], v[132:135], v[184:187], v[4:7]
	v_mfma_f32_16x16x32_bf16 v[0:3], v[148:151], v[184:187], v[0:3]
	v_mfma_f32_16x16x32_bf16 v[52:55], v[140:143], v[164:167], v[52:55]
	v_mfma_f32_16x16x32_bf16 v[48:51], v[156:159], v[164:167], v[48:51]
	v_mfma_f32_16x16x32_bf16 v[36:39], v[140:143], v[172:175], v[36:39]
	v_mfma_f32_16x16x32_bf16 v[32:35], v[156:159], v[172:175], v[32:35]
	v_mfma_f32_16x16x32_bf16 v[20:23], v[140:143], v[180:183], v[20:23]
	v_mfma_f32_16x16x32_bf16 v[16:19], v[156:159], v[180:183], v[16:19]
	v_mfma_f32_16x16x32_bf16 v[4:7], v[140:143], v[194:197], v[4:7]
	v_mfma_f32_16x16x32_bf16 v[0:3], v[156:159], v[194:197], v[0:3]
	s_setprio 0
	s_barrier
	ds_read_b128 v[100:103], v220
	ds_read_b128 v[108:111], v220 offset:1024
	ds_read_b128 v[116:119], v220 offset:2048
	ds_read_b128 v[124:127], v220 offset:3072
	ds_read_b128 v[132:135], v221
	ds_read_b128 v[140:143], v221 offset:1024
	ds_read_b128 v[148:151], v221 offset:2048
	ds_read_b128 v[156:159], v221 offset:3072
	ds_read_b128 v[160:163], v219 offset:32768
	ds_read_b128 v[164:167], v219 offset:33792
	ds_read_b128 v[168:171], v219 offset:34816
	ds_read_b128 v[172:175], v219 offset:35840
	ds_read_b128 v[176:179], v219 offset:36864
	ds_read_b128 v[180:183], v219 offset:37888
	ds_read_b128 v[184:187], v219 offset:38912
	ds_read_b128 v[194:197], v219 offset:39936
	s_add_u32 s36, s42, 0x80000
	s_addc_u32 s37, s43, 0
	s_add_i32 m0, s48, 0x4000
	s_nop 0
	global_load_lds_dwordx4 v213, s[36:37]
	s_nop 0
	s_add_i32 m0, s48, 0x6000
	s_nop 0
	global_load_lds_dwordx4 v214, s[36:37]
	s_waitcnt vmcnt(8)
	s_waitcnt lgkmcnt(0)
	s_barrier
	s_setprio 1
	v_mfma_f32_16x16x32_bf16 v[152:155], v[100:103], v[160:163], v[152:155]
	v_mfma_f32_16x16x32_bf16 v[144:147], v[116:119], v[160:163], v[144:147]
	v_mfma_f32_16x16x32_bf16 v[120:123], v[100:103], v[168:171], v[120:123]
	v_mfma_f32_16x16x32_bf16 v[112:115], v[116:119], v[168:171], v[112:115]
	v_mfma_f32_16x16x32_bf16 v[92:95], v[100:103], v[176:179], v[92:95]
	v_mfma_f32_16x16x32_bf16 v[88:91], v[116:119], v[176:179], v[88:91]
	v_mfma_f32_16x16x32_bf16 v[76:79], v[100:103], v[184:187], v[76:79]
	v_mfma_f32_16x16x32_bf16 v[72:75], v[116:119], v[184:187], v[72:75]
	v_mfma_f32_16x16x32_bf16 v[152:155], v[108:111], v[164:167], v[152:155]
	v_mfma_f32_16x16x32_bf16 v[144:147], v[124:127], v[164:167], v[144:147]
	v_mfma_f32_16x16x32_bf16 v[120:123], v[108:111], v[172:175], v[120:123]
	v_mfma_f32_16x16x32_bf16 v[112:115], v[124:127], v[172:175], v[112:115]
	v_mfma_f32_16x16x32_bf16 v[92:95], v[108:111], v[180:183], v[92:95]
	v_mfma_f32_16x16x32_bf16 v[88:91], v[124:127], v[180:183], v[88:91]
	v_mfma_f32_16x16x32_bf16 v[76:79], v[108:111], v[194:197], v[76:79]
	v_mfma_f32_16x16x32_bf16 v[72:75], v[124:127], v[194:197], v[72:75]
	v_mfma_f32_16x16x32_bf16 v[136:139], v[132:135], v[160:163], v[136:139]
	v_mfma_f32_16x16x32_bf16 v[128:131], v[148:151], v[160:163], v[128:131]
	v_mfma_f32_16x16x32_bf16 v[104:107], v[132:135], v[168:171], v[104:107]
	v_mfma_f32_16x16x32_bf16 v[96:99], v[148:151], v[168:171], v[96:99]
	v_mfma_f32_16x16x32_bf16 v[84:87], v[132:135], v[176:179], v[84:87]
	v_mfma_f32_16x16x32_bf16 v[80:83], v[148:151], v[176:179], v[80:83]
	v_mfma_f32_16x16x32_bf16 v[68:71], v[132:135], v[184:187], v[68:71]
	v_mfma_f32_16x16x32_bf16 v[64:67], v[148:151], v[184:187], v[64:67]
	v_mfma_f32_16x16x32_bf16 v[136:139], v[140:143], v[164:167], v[136:139]
	v_mfma_f32_16x16x32_bf16 v[128:131], v[156:159], v[164:167], v[128:131]
	v_mfma_f32_16x16x32_bf16 v[104:107], v[140:143], v[172:175], v[104:107]
	v_mfma_f32_16x16x32_bf16 v[96:99], v[156:159], v[172:175], v[96:99]
	v_mfma_f32_16x16x32_bf16 v[84:87], v[140:143], v[180:183], v[84:87]
	v_mfma_f32_16x16x32_bf16 v[80:83], v[156:159], v[180:183], v[80:83]
	v_mfma_f32_16x16x32_bf16 v[68:71], v[140:143], v[194:197], v[68:71]
	v_mfma_f32_16x16x32_bf16 v[64:67], v[156:159], v[194:197], v[64:67]
	s_setprio 0
	s_barrier
	ds_read_b128 v[160:163], v219 offset:49152
	ds_read_b128 v[164:167], v219 offset:50176
	ds_read_b128 v[168:171], v219 offset:51200
	ds_read_b128 v[172:175], v219 offset:52224
	ds_read_b128 v[176:179], v219 offset:53248
	ds_read_b128 v[180:183], v219 offset:54272
	ds_read_b128 v[184:187], v219 offset:55296
	ds_read_b128 v[194:197], v219 offset:56320
	s_add_i32 m0, s48, 0x18000
	s_nop 0
	global_load_lds_dwordx4 v213, s[40:41]
	s_nop 0
	s_add_i32 m0, s48, 0x1a000
	s_nop 0
	global_load_lds_dwordx4 v214, s[40:41]
	s_add_u32 s36, s38, 0x80080
	s_addc_u32 s37, s39, 0
	s_add_i32 m0, s48, 0x1c000
	s_nop 0
	global_load_lds_dwordx4 v213, s[36:37]
	s_nop 0
	s_add_i32 m0, s48, 0x1e000
	s_nop 0
	global_load_lds_dwordx4 v214, s[36:37]
	s_nop 0
	s_add_i32 m0, s48, 0x8000
	s_nop 0
	global_load_lds_dwordx4 v213, s[34:35]
	s_nop 0
	s_add_i32 m0, s48, 0xa000
	s_nop 0
	global_load_lds_dwordx4 v214, s[34:35]
	s_waitcnt vmcnt(8)
	s_waitcnt lgkmcnt(0)
	s_barrier
	s_setprio 1
	v_mfma_f32_16x16x32_bf16 v[60:63], v[100:103], v[160:163], v[60:63]
	v_mfma_f32_16x16x32_bf16 v[56:59], v[116:119], v[160:163], v[56:59]
	v_mfma_f32_16x16x32_bf16 v[44:47], v[100:103], v[168:171], v[44:47]
	v_mfma_f32_16x16x32_bf16 v[40:43], v[116:119], v[168:171], v[40:43]
	v_mfma_f32_16x16x32_bf16 v[28:31], v[100:103], v[176:179], v[28:31]
	v_mfma_f32_16x16x32_bf16 v[24:27], v[116:119], v[176:179], v[24:27]
	v_mfma_f32_16x16x32_bf16 v[12:15], v[100:103], v[184:187], v[12:15]
	v_mfma_f32_16x16x32_bf16 v[8:11], v[116:119], v[184:187], v[8:11]
	v_mfma_f32_16x16x32_bf16 v[60:63], v[108:111], v[164:167], v[60:63]
	v_mfma_f32_16x16x32_bf16 v[56:59], v[124:127], v[164:167], v[56:59]
	v_mfma_f32_16x16x32_bf16 v[44:47], v[108:111], v[172:175], v[44:47]
	v_mfma_f32_16x16x32_bf16 v[40:43], v[124:127], v[172:175], v[40:43]
	v_mfma_f32_16x16x32_bf16 v[28:31], v[108:111], v[180:183], v[28:31]
	v_mfma_f32_16x16x32_bf16 v[24:27], v[124:127], v[180:183], v[24:27]
	v_mfma_f32_16x16x32_bf16 v[12:15], v[108:111], v[194:197], v[12:15]
	v_mfma_f32_16x16x32_bf16 v[8:11], v[124:127], v[194:197], v[8:11]
	v_mfma_f32_16x16x32_bf16 v[52:55], v[132:135], v[160:163], v[52:55]
	v_mfma_f32_16x16x32_bf16 v[48:51], v[148:151], v[160:163], v[48:51]
	v_mfma_f32_16x16x32_bf16 v[36:39], v[132:135], v[168:171], v[36:39]
	v_mfma_f32_16x16x32_bf16 v[32:35], v[148:151], v[168:171], v[32:35]
	v_mfma_f32_16x16x32_bf16 v[20:23], v[132:135], v[176:179], v[20:23]
	v_mfma_f32_16x16x32_bf16 v[16:19], v[148:151], v[176:179], v[16:19]
	v_mfma_f32_16x16x32_bf16 v[4:7], v[132:135], v[184:187], v[4:7]
	v_mfma_f32_16x16x32_bf16 v[0:3], v[148:151], v[184:187], v[0:3]
	v_mfma_f32_16x16x32_bf16 v[52:55], v[140:143], v[164:167], v[52:55]
	v_mfma_f32_16x16x32_bf16 v[48:51], v[156:159], v[164:167], v[48:51]
	v_mfma_f32_16x16x32_bf16 v[36:39], v[140:143], v[172:175], v[36:39]
	v_mfma_f32_16x16x32_bf16 v[32:35], v[156:159], v[172:175], v[32:35]
	v_mfma_f32_16x16x32_bf16 v[20:23], v[140:143], v[180:183], v[20:23]
	v_mfma_f32_16x16x32_bf16 v[16:19], v[156:159], v[180:183], v[16:19]
	v_mfma_f32_16x16x32_bf16 v[4:7], v[140:143], v[194:197], v[4:7]
	v_mfma_f32_16x16x32_bf16 v[0:3], v[156:159], v[194:197], v[0:3]
	s_setprio 0
	s_barrier
	s_add_i32 s61, s61, 2
	s_add_u32 s59, s59, 0x100
	s_addc_u32 s60, s60, 0
	s_cmp_gt_u32 s61, 29
	s_mov_b64 s[36:37], s[30:31]
	s_cbranch_scc0 .LBB0_603
	s_and_b64 vcc, exec, s[20:21]
	s_cbranch_vccz .LBB0_606
	s_barrier

.LBB0_752:
	s_ashr_i32 s17, s16, 31
	s_lshl_b64 s[18:19], s[16:17], 19
	s_add_u32 s18, s40, s18
	s_addc_u32 s19, s41, s19
	s_and_b64 s[20:21], s[4:5], exec
	s_cselect_b32 s58, s19, s29
	s_cselect_b32 s59, s18, s28
	s_ashr_i32 s15, s14, 31
	s_lshl_b64 s[20:21], s[14:15], 19
	s_add_u32 s20, s42, s20
	s_addc_u32 s21, s43, s21
	s_and_b64 s[26:27], s[4:5], exec
	ds_read_b128 v[0:3], v204 offset:3072
	ds_read_b128 v[4:7], v204 offset:2048
	ds_read_b128 v[8:11], v204 offset:1024
	ds_read_b128 v[12:15], v204
	ds_read_b128 v[16:19], v205 offset:3072
	ds_read_b128 v[20:23], v205 offset:2048
	ds_read_b128 v[24:27], v205 offset:1024
	ds_read_b128 v[28:31], v205
	s_cselect_b32 s15, s21, s25
	s_cselect_b32 s60, s20, s24
	s_lshl_b32 s26, s55, 11
	s_and_b32 s26, s26, 0x800
	s_or_b32 s38, s26, s49
	s_lshl_b64 s[30:31], s[16:17], 11
	s_add_u32 s26, s28, 0x100
	s_addc_u32 s27, s29, 0
	s_add_u32 s62, s24, 0x100
	s_addc_u32 s63, s25, 0
	s_add_u32 s34, s28, 0x180
	s_addc_u32 s35, s29, 0
	s_add_u32 s36, s24, 0x180
	s_addc_u32 s37, s25, 0
	ds_read_b128 v[32:35], v206
	ds_read_b128 v[36:39], v206 offset:1024
	ds_read_b128 v[40:43], v206 offset:2048
	ds_read_b128 v[44:47], v206 offset:3072
	ds_read_b128 v[48:51], v206 offset:4096
	ds_read_b128 v[52:55], v206 offset:5120
	ds_read_b128 v[56:59], v206 offset:6144
	ds_read_b128 v[60:63], v206 offset:7168
	s_add_u32 s66, s28, 0x40080
	s_addc_u32 s67, s29, 0
	s_add_i32 m0, s46, 0xc000
	s_nop 0
	global_load_lds_dwordx4 v199, s[66:67]
	s_nop 0
	s_add_i32 m0, s46, 0xe000
	s_nop 0
	global_load_lds_dwordx4 v201, s[66:67]
	s_waitcnt vmcnt(8)
	s_waitcnt lgkmcnt(0)
	s_barrier
	s_setprio 1
	s_waitcnt lgkmcnt(7)
	v_mfma_i32_16x16x64_i8 v[64:67], v[28:31], v[32:35], 0
	s_mov_b32 s17, 0
	v_mfma_i32_16x16x64_i8 v[68:71], v[20:23], v[32:35], 0
	s_waitcnt lgkmcnt(5)
	v_mfma_i32_16x16x64_i8 v[72:75], v[28:31], v[40:43], 0
	v_mfma_i32_16x16x64_i8 v[132:135], v[24:27], v[36:39], v[64:67]
	v_mfma_i32_16x16x64_i8 v[136:139], v[16:19], v[36:39], v[68:71]
	s_waitcnt lgkmcnt(4)
	v_mfma_i32_16x16x64_i8 v[144:147], v[24:27], v[44:47], v[72:75]
	v_mfma_i32_16x16x64_i8 v[76:79], v[20:23], v[40:43], 0
	s_waitcnt lgkmcnt(3)
	v_mfma_i32_16x16x64_i8 v[80:83], v[28:31], v[48:51], 0
	v_mfma_i32_16x16x64_i8 v[84:87], v[20:23], v[48:51], 0
	s_waitcnt lgkmcnt(1)
	v_mfma_i32_16x16x64_i8 v[88:91], v[28:31], v[56:59], 0
	v_mfma_i32_16x16x64_i8 v[92:95], v[20:23], v[56:59], 0
	v_mfma_i32_16x16x64_i8 v[76:79], v[16:19], v[44:47], v[76:79]
	v_mfma_i32_16x16x64_i8 v[80:83], v[24:27], v[52:55], v[80:83]
	v_mfma_i32_16x16x64_i8 v[84:87], v[16:19], v[52:55], v[84:87]
	s_waitcnt lgkmcnt(0)
	v_mfma_i32_16x16x64_i8 v[88:91], v[24:27], v[60:63], v[88:91]
	v_mfma_i32_16x16x64_i8 v[92:95], v[16:19], v[60:63], v[92:95]
	s_setprio 0
	s_setprio 1
	v_mfma_i32_16x16x64_i8 v[96:99], v[12:15], v[32:35], 0
	v_mfma_i32_16x16x64_i8 v[32:35], v[4:7], v[32:35], 0
	v_mfma_i32_16x16x64_i8 v[96:99], v[8:11], v[36:39], v[96:99]
	v_mfma_i32_16x16x64_i8 v[32:35], v[0:3], v[36:39], v[32:35]
	v_mfma_i32_16x16x64_i8 v[36:39], v[12:15], v[40:43], 0
	v_mfma_i32_16x16x64_i8 v[40:43], v[4:7], v[40:43], 0
	v_mfma_i32_16x16x64_i8 v[36:39], v[8:11], v[44:47], v[36:39]
	v_mfma_i32_16x16x64_i8 v[40:43], v[0:3], v[44:47], v[40:43]
	v_mfma_i32_16x16x64_i8 v[44:47], v[12:15], v[48:51], 0
	v_mfma_i32_16x16x64_i8 v[48:51], v[4:7], v[48:51], 0
	v_mfma_i32_16x16x64_i8 v[44:47], v[8:11], v[52:55], v[44:47]
	v_mfma_i32_16x16x64_i8 v[48:51], v[0:3], v[52:55], v[48:51]
	v_mfma_i32_16x16x64_i8 v[52:55], v[12:15], v[56:59], 0
	v_mfma_i32_16x16x64_i8 v[56:59], v[4:7], v[56:59], 0
	v_mfma_i32_16x16x64_i8 v[52:55], v[8:11], v[60:63], v[52:55]
	v_mfma_i32_16x16x64_i8 v[56:59], v[0:3], v[60:63], v[56:59]
	s_setprio 0
	s_barrier
	ds_read_b128 v[60:63], v206 offset:16384
	ds_read_b128 v[100:103], v206 offset:17408
	ds_read_b128 v[104:107], v206 offset:18432
	ds_read_b128 v[108:111], v206 offset:19456
	ds_read_b128 v[112:115], v206 offset:20480
	ds_read_b128 v[116:119], v206 offset:21504
	ds_read_b128 v[120:123], v206 offset:22528
	ds_read_b128 v[124:127], v206 offset:23552
	s_add_i32 m0, s46, 0x10000
	s_nop 0
	global_load_lds_dwordx4 v200, s[62:63]
	s_nop 0
	s_add_i32 m0, s46, 0x12000
	s_nop 0
	global_load_lds_dwordx4 v202, s[62:63]
	s_add_u32 s62, s24, 0x40100
	s_addc_u32 s63, s25, 0
	s_add_i32 m0, s46, 0x14000
	s_nop 0
	global_load_lds_dwordx4 v200, s[62:63]
	s_nop 0
	s_add_i32 m0, s46, 0x16000
	s_nop 0
	global_load_lds_dwordx4 v202, s[62:63]
	s_nop 0
	s_add_i32 m0, s46, 0
	s_nop 0
	global_load_lds_dwordx4 v199, s[26:27]
	s_nop 0
	s_add_i32 m0, s46, 0x2000
	s_nop 0
	global_load_lds_dwordx4 v201, s[26:27]
	s_waitcnt vmcnt(8)
	s_waitcnt lgkmcnt(0)
	s_barrier
	s_setprio 1
	v_mfma_i32_16x16x64_i8 v[128:131], v[28:31], v[60:63], 0
	v_mfma_i32_16x16x64_i8 v[210:213], v[24:27], v[100:103], v[128:131]
	v_mfma_i32_16x16x64_i8 v[128:131], v[20:23], v[60:63], 0
	v_mfma_i32_16x16x64_i8 v[214:217], v[16:19], v[100:103], v[128:131]
	v_mfma_i32_16x16x64_i8 v[128:131], v[28:31], v[104:107], 0
	v_mfma_i32_16x16x64_i8 v[218:221], v[24:27], v[108:111], v[128:131]
	v_mfma_i32_16x16x64_i8 v[128:131], v[20:23], v[104:107], 0
	v_mfma_i32_16x16x64_i8 v[222:225], v[16:19], v[108:111], v[128:131]
	v_mfma_i32_16x16x64_i8 v[128:131], v[28:31], v[112:115], 0
	v_mfma_i32_16x16x64_i8 v[226:229], v[24:27], v[116:119], v[128:131]
	v_mfma_i32_16x16x64_i8 v[128:131], v[20:23], v[112:115], 0
	v_mfma_i32_16x16x64_i8 v[28:31], v[28:31], v[120:123], 0
	v_mfma_i32_16x16x64_i8 v[20:23], v[20:23], v[120:123], 0
	v_mfma_i32_16x16x64_i8 v[230:233], v[16:19], v[116:119], v[128:131]
	v_mfma_i32_16x16x64_i8 v[24:27], v[24:27], v[124:127], v[28:31]
	v_mfma_i32_16x16x64_i8 v[20:23], v[16:19], v[124:127], v[20:23]
	v_mfma_i32_16x16x64_i8 v[16:19], v[12:15], v[60:63], 0
	v_mfma_i32_16x16x64_i8 v[28:31], v[8:11], v[100:103], v[16:19]
	v_mfma_i32_16x16x64_i8 v[16:19], v[4:7], v[60:63], 0
	v_mfma_i32_16x16x64_i8 v[60:63], v[0:3], v[100:103], v[16:19]
	v_mfma_i32_16x16x64_i8 v[16:19], v[12:15], v[104:107], 0
	v_mfma_i32_16x16x64_i8 v[100:103], v[8:11], v[108:111], v[16:19]
	v_mfma_i32_16x16x64_i8 v[16:19], v[4:7], v[104:107], 0
	v_mfma_i32_16x16x64_i8 v[234:237], v[0:3], v[108:111], v[16:19]
	v_mfma_i32_16x16x64_i8 v[16:19], v[12:15], v[112:115], 0
	v_mfma_i32_16x16x64_i8 v[238:241], v[8:11], v[116:119], v[16:19]
	v_mfma_i32_16x16x64_i8 v[16:19], v[4:7], v[112:115], 0
	v_mfma_i32_16x16x64_i8 v[12:15], v[12:15], v[120:123], 0
	v_mfma_i32_16x16x64_i8 v[4:7], v[4:7], v[120:123], 0
	v_mfma_i32_16x16x64_i8 v[12:15], v[8:11], v[124:127], v[12:15]
	v_mfma_i32_16x16x64_i8 v[4:7], v[0:3], v[124:127], v[4:7]
	v_mfma_i32_16x16x64_i8 v[242:245], v[0:3], v[116:119], v[16:19]
	s_setprio 0
	s_barrier
	ds_read_b128 v[0:3], v207
	ds_read_b128 v[8:11], v207 offset:1024
	ds_read_b128 v[108:111], v207 offset:2048
	ds_read_b128 v[116:119], v207 offset:3072
	ds_read_b128 v[246:249], v208
	ds_read_b128 v[250:253], v208 offset:1024
	ds_read_b128 v[192:195], v208 offset:2048
	ds_read_b128 v[64:67], v208 offset:3072
	ds_read_b128 v[16:19], v206 offset:32768
	ds_read_b128 v[104:107], v206 offset:33792
	ds_read_b128 v[112:115], v206 offset:34816
	ds_read_b128 v[120:123], v206 offset:35840
	ds_read_b128 v[124:127], v206 offset:36864
	ds_read_b128 v[140:143], v206 offset:37888
	ds_read_b128 v[68:71], v206 offset:38912
	ds_read_b128 v[72:75], v206 offset:39936
	s_add_u32 s28, s28, 0x40100
	s_addc_u32 s29, s29, 0
	s_add_i32 m0, s46, 0x4000
	s_nop 0
	global_load_lds_dwordx4 v199, s[28:29]
	s_nop 0
	s_add_i32 m0, s46, 0x6000
	s_nop 0
	global_load_lds_dwordx4 v201, s[28:29]
	s_waitcnt vmcnt(8)
	s_waitcnt lgkmcnt(0)
	s_barrier
	s_setprio 1
	v_mfma_i32_16x16x64_i8 v[76:79], v[108:111], v[112:115], v[76:79]
	v_mfma_i32_16x16x64_i8 v[128:131], v[0:3], v[16:19], v[132:135]
	v_mfma_i32_16x16x64_i8 v[160:163], v[116:119], v[120:123], v[76:79]
	v_mfma_i32_16x16x64_i8 v[76:79], v[0:3], v[124:127], v[80:83]
	v_mfma_i32_16x16x64_i8 v[184:187], v[8:11], v[104:107], v[128:131]
	v_mfma_i32_16x16x64_i8 v[128:131], v[108:111], v[16:19], v[136:139]
	v_mfma_i32_16x16x64_i8 v[152:155], v[8:11], v[140:143], v[76:79]
	v_mfma_i32_16x16x64_i8 v[76:79], v[108:111], v[124:127], v[84:87]
	v_mfma_i32_16x16x64_i8 v[176:179], v[116:119], v[104:107], v[128:131]
	v_mfma_i32_16x16x64_i8 v[128:131], v[0:3], v[112:115], v[144:147]
	v_mfma_i32_16x16x64_i8 v[144:147], v[116:119], v[140:143], v[76:79]
	v_mfma_i32_16x16x64_i8 v[76:79], v[0:3], v[68:71], v[88:91]
	v_mfma_i32_16x16x64_i8 v[136:139], v[8:11], v[72:75], v[76:79]
	v_mfma_i32_16x16x64_i8 v[76:79], v[108:111], v[68:71], v[92:95]
	v_mfma_i32_16x16x64_i8 v[168:171], v[8:11], v[120:123], v[128:131]
	v_mfma_i32_16x16x64_i8 v[128:131], v[116:119], v[72:75], v[76:79]
	v_mfma_i32_16x16x64_i8 v[76:79], v[246:249], v[16:19], v[96:99]
	v_mfma_i32_16x16x64_i8 v[16:19], v[192:195], v[16:19], v[32:35]
	v_mfma_i32_16x16x64_i8 v[180:183], v[64:67], v[104:107], v[16:19]
	v_mfma_i32_16x16x64_i8 v[16:19], v[246:249], v[112:115], v[36:39]
	v_mfma_i32_16x16x64_i8 v[172:175], v[250:253], v[120:123], v[16:19]
	v_mfma_i32_16x16x64_i8 v[16:19], v[192:195], v[112:115], v[40:43]
	v_mfma_i32_16x16x64_i8 v[164:167], v[64:67], v[120:123], v[16:19]
	v_mfma_i32_16x16x64_i8 v[16:19], v[246:249], v[124:127], v[44:47]
	v_mfma_i32_16x16x64_i8 v[156:159], v[250:253], v[140:143], v[16:19]
	v_mfma_i32_16x16x64_i8 v[16:19], v[192:195], v[124:127], v[48:51]
	v_mfma_i32_16x16x64_i8 v[148:151], v[64:67], v[140:143], v[16:19]
	v_mfma_i32_16x16x64_i8 v[16:19], v[246:249], v[68:71], v[52:55]
	v_mfma_i32_16x16x64_i8 v[140:143], v[250:253], v[72:75], v[16:19]
	v_mfma_i32_16x16x64_i8 v[16:19], v[192:195], v[68:71], v[56:59]
	v_mfma_i32_16x16x64_i8 v[188:191], v[250:253], v[104:107], v[76:79]
	v_mfma_i32_16x16x64_i8 v[132:135], v[64:67], v[72:75], v[16:19]
	s_setprio 0
	s_barrier
	ds_read_b128 v[32:35], v206 offset:49152
	ds_read_b128 v[36:39], v206 offset:50176
	ds_read_b128 v[40:43], v206 offset:51200
	ds_read_b128 v[44:47], v206 offset:52224
	ds_read_b128 v[52:55], v206 offset:53248
	ds_read_b128 v[56:59], v206 offset:54272
	ds_read_b128 v[68:71], v206 offset:55296
	ds_read_b128 v[72:75], v206 offset:56320
	s_add_i32 m0, s46, 0x18000
	s_nop 0
	global_load_lds_dwordx4 v200, s[36:37]
	s_nop 0
	s_add_i32 m0, s46, 0x1a000
	s_nop 0
	global_load_lds_dwordx4 v202, s[36:37]
	s_add_u32 s28, s24, 0x40180
	s_addc_u32 s29, s25, 0
	s_add_i32 m0, s46, 0x1c000
	s_nop 0
	global_load_lds_dwordx4 v200, s[28:29]
	s_nop 0
	s_add_i32 m0, s46, 0x1e000
	s_nop 0
	global_load_lds_dwordx4 v202, s[28:29]
	s_nop 0
	s_add_i32 m0, s46, 0x8000
	s_nop 0
	global_load_lds_dwordx4 v199, s[34:35]
	s_nop 0
	s_add_i32 m0, s46, 0xa000
	s_nop 0
	global_load_lds_dwordx4 v201, s[34:35]
	s_waitcnt vmcnt(8)
	s_waitcnt lgkmcnt(0)
	s_barrier
	s_setprio 1
	v_mfma_i32_16x16x64_i8 v[16:19], v[0:3], v[32:35], v[210:213]
	v_mfma_i32_16x16x64_i8 v[120:123], v[8:11], v[36:39], v[16:19]
	v_mfma_i32_16x16x64_i8 v[16:19], v[108:111], v[32:35], v[214:217]
	v_mfma_i32_16x16x64_i8 v[112:115], v[116:119], v[36:39], v[16:19]
	v_mfma_i32_16x16x64_i8 v[16:19], v[0:3], v[40:43], v[218:221]
	v_mfma_i32_16x16x64_i8 v[104:107], v[8:11], v[44:47], v[16:19]
	v_mfma_i32_16x16x64_i8 v[16:19], v[108:111], v[40:43], v[222:225]
	v_mfma_i32_16x16x64_i8 v[96:99], v[116:119], v[44:47], v[16:19]
	v_mfma_i32_16x16x64_i8 v[16:19], v[0:3], v[52:55], v[226:229]
	v_mfma_i32_16x16x64_i8 v[0:3], v[0:3], v[68:71], v[24:27]
	v_mfma_i32_16x16x64_i8 v[48:51], v[8:11], v[56:59], v[16:19]
	v_mfma_i32_16x16x64_i8 v[16:19], v[108:111], v[52:55], v[230:233]
	v_mfma_i32_16x16x64_i8 v[8:11], v[8:11], v[72:75], v[0:3]
	v_mfma_i32_16x16x64_i8 v[0:3], v[108:111], v[68:71], v[20:23]
	v_mfma_i32_16x16x64_i8 v[16:19], v[116:119], v[56:59], v[16:19]
	v_mfma_i32_16x16x64_i8 v[0:3], v[116:119], v[72:75], v[0:3]
	v_mfma_i32_16x16x64_i8 v[20:23], v[246:249], v[32:35], v[28:31]
	v_mfma_i32_16x16x64_i8 v[124:127], v[250:253], v[36:39], v[20:23]
	v_mfma_i32_16x16x64_i8 v[20:23], v[192:195], v[32:35], v[60:63]
	v_mfma_i32_16x16x64_i8 v[116:119], v[64:67], v[36:39], v[20:23]
	v_mfma_i32_16x16x64_i8 v[20:23], v[246:249], v[40:43], v[100:103]
	v_mfma_i32_16x16x64_i8 v[108:111], v[250:253], v[44:47], v[20:23]
	v_mfma_i32_16x16x64_i8 v[20:23], v[192:195], v[40:43], v[234:237]
	v_mfma_i32_16x16x64_i8 v[100:103], v[64:67], v[44:47], v[20:23]
	v_mfma_i32_16x16x64_i8 v[20:23], v[246:249], v[52:55], v[238:241]
	v_mfma_i32_16x16x64_i8 v[60:63], v[250:253], v[56:59], v[20:23]
	v_mfma_i32_16x16x64_i8 v[20:23], v[192:195], v[52:55], v[242:245]
	v_mfma_i32_16x16x64_i8 v[12:15], v[246:249], v[68:71], v[12:15]
	v_mfma_i32_16x16x64_i8 v[4:7], v[192:195], v[68:71], v[4:7]
	v_mfma_i32_16x16x64_i8 v[44:47], v[64:67], v[56:59], v[20:23]
	v_mfma_i32_16x16x64_i8 v[12:15], v[250:253], v[72:75], v[12:15]
	v_mfma_i32_16x16x64_i8 v[4:7], v[64:67], v[72:75], v[4:7]
	s_setprio 0
	s_barrier
	s_add_u32 s28, s44, s30
	s_addc_u32 s29, s45, s31
	s_add_u32 s61, s24, 0x200
	s_addc_u32 s62, s25, 0
	s_add_i32 s63, s38, 0
	s_add_i32 s63, s63, 0x20000

.LBB0_755:
	ds_read_b128 v[20:23], v205
	ds_read_b128 v[24:27], v205 offset:1024
	ds_read_b128 v[28:31], v205 offset:2048
	ds_read_b128 v[32:35], v205 offset:3072
	ds_read_b128 v[36:39], v204
	ds_read_b128 v[40:43], v204 offset:1024
	ds_read_b128 v[52:55], v204 offset:2048
	ds_read_b128 v[56:59], v204 offset:3072
	s_add_u32 s24, s26, 0x100
	s_addc_u32 s25, s27, 0
	s_and_b64 s[30:31], s[30:31], exec
	s_cselect_b32 s38, s59, s24
	s_cselect_b32 s39, s58, s25
	s_cselect_b32 s35, s15, s62
	s_cselect_b32 s34, s60, s61
	s_add_u32 s30, s38, 0x80
	s_addc_u32 s31, s39, 0
	s_add_u32 s36, s34, 0x80
	s_addc_u32 s37, s35, 0
	ds_read_b128 v[64:67], v206
	ds_read_b128 v[68:71], v206 offset:1024
	ds_read_b128 v[72:75], v206 offset:2048
	ds_read_b128 v[76:79], v206 offset:3072
	ds_read_b128 v[80:83], v206 offset:4096
	ds_read_b128 v[84:87], v206 offset:5120
	ds_read_b128 v[88:91], v206 offset:6144
	ds_read_b128 v[92:95], v206 offset:7168
	s_add_u32 s26, s26, 0x40080
	s_addc_u32 s27, s27, 0
	s_add_i32 m0, s46, 0xc000
	s_nop 0
	global_load_lds_dwordx4 v199, s[26:27]
	s_nop 0
	s_add_i32 m0, s46, 0xe000
	s_nop 0
	global_load_lds_dwordx4 v201, s[26:27]
	s_waitcnt vmcnt(8)
	s_waitcnt lgkmcnt(0)
	s_barrier
	s_setprio 1
	v_mfma_i32_16x16x64_i8 v[184:187], v[20:23], v[64:67], v[184:187]
	v_mfma_i32_16x16x64_i8 v[176:179], v[28:31], v[64:67], v[176:179]
	v_mfma_i32_16x16x64_i8 v[168:171], v[20:23], v[72:75], v[168:171]
	v_mfma_i32_16x16x64_i8 v[160:163], v[28:31], v[72:75], v[160:163]
	v_mfma_i32_16x16x64_i8 v[152:155], v[20:23], v[80:83], v[152:155]
	v_mfma_i32_16x16x64_i8 v[144:147], v[28:31], v[80:83], v[144:147]
	v_mfma_i32_16x16x64_i8 v[136:139], v[20:23], v[88:91], v[136:139]
	v_mfma_i32_16x16x64_i8 v[128:131], v[28:31], v[88:91], v[128:131]
	v_mfma_i32_16x16x64_i8 v[184:187], v[24:27], v[68:71], v[184:187]
	v_mfma_i32_16x16x64_i8 v[176:179], v[32:35], v[68:71], v[176:179]
	v_mfma_i32_16x16x64_i8 v[168:171], v[24:27], v[76:79], v[168:171]
	v_mfma_i32_16x16x64_i8 v[160:163], v[32:35], v[76:79], v[160:163]
	v_mfma_i32_16x16x64_i8 v[152:155], v[24:27], v[84:87], v[152:155]
	v_mfma_i32_16x16x64_i8 v[144:147], v[32:35], v[84:87], v[144:147]
	v_mfma_i32_16x16x64_i8 v[136:139], v[24:27], v[92:95], v[136:139]
	v_mfma_i32_16x16x64_i8 v[128:131], v[32:35], v[92:95], v[128:131]
	v_mfma_i32_16x16x64_i8 v[188:191], v[36:39], v[64:67], v[188:191]
	v_mfma_i32_16x16x64_i8 v[64:67], v[52:55], v[64:67], v[180:183]
	v_mfma_i32_16x16x64_i8 v[188:191], v[40:43], v[68:71], v[188:191]
	v_mfma_i32_16x16x64_i8 v[64:67], v[56:59], v[68:71], v[64:67]
	v_mfma_i32_16x16x64_i8 v[68:71], v[36:39], v[72:75], v[172:175]
	v_mfma_i32_16x16x64_i8 v[72:75], v[52:55], v[72:75], v[164:167]
	v_mfma_i32_16x16x64_i8 v[68:71], v[40:43], v[76:79], v[68:71]
	v_mfma_i32_16x16x64_i8 v[72:75], v[56:59], v[76:79], v[72:75]
	v_mfma_i32_16x16x64_i8 v[76:79], v[36:39], v[80:83], v[156:159]
	v_mfma_i32_16x16x64_i8 v[80:83], v[52:55], v[80:83], v[148:151]
	v_mfma_i32_16x16x64_i8 v[76:79], v[40:43], v[84:87], v[76:79]
	v_mfma_i32_16x16x64_i8 v[80:83], v[56:59], v[84:87], v[80:83]
	v_mfma_i32_16x16x64_i8 v[84:87], v[36:39], v[88:91], v[140:143]
	v_mfma_i32_16x16x64_i8 v[88:91], v[52:55], v[88:91], v[132:135]
	v_mfma_i32_16x16x64_i8 v[84:87], v[40:43], v[92:95], v[84:87]
	v_mfma_i32_16x16x64_i8 v[88:91], v[56:59], v[92:95], v[88:91]
	s_setprio 0
	s_barrier
	ds_read_b128 v[92:95], v206 offset:16384
	ds_read_b128 v[132:135], v206 offset:17408
	ds_read_b128 v[140:143], v206 offset:18432
	ds_read_b128 v[148:151], v206 offset:19456
	ds_read_b128 v[156:159], v206 offset:20480
	ds_read_b128 v[164:167], v206 offset:21504
	ds_read_b128 v[172:175], v206 offset:22528
	ds_read_b128 v[180:183], v206 offset:23552
	s_add_i32 m0, s46, 0x10000
	s_nop 0
	global_load_lds_dwordx4 v200, s[34:35]
	s_nop 0
	s_add_i32 m0, s46, 0x12000
	s_nop 0
	global_load_lds_dwordx4 v202, s[34:35]
	s_add_u32 s26, s34, 0x40000
	s_addc_u32 s27, s35, 0
	s_add_i32 m0, s46, 0x14000
	s_nop 0
	global_load_lds_dwordx4 v200, s[26:27]
	s_nop 0
	s_add_i32 m0, s46, 0x16000
	s_nop 0
	global_load_lds_dwordx4 v202, s[26:27]
	s_nop 0
	s_add_i32 m0, s46, 0
	s_nop 0
	global_load_lds_dwordx4 v199, s[38:39]
	s_nop 0
	s_add_i32 m0, s46, 0x2000
	s_nop 0
	global_load_lds_dwordx4 v201, s[38:39]
	s_waitcnt vmcnt(8)
	s_waitcnt lgkmcnt(0)
	s_barrier
	s_setprio 1
	v_mfma_i32_16x16x64_i8 v[120:123], v[20:23], v[92:95], v[120:123]
	v_mfma_i32_16x16x64_i8 v[112:115], v[28:31], v[92:95], v[112:115]
	v_mfma_i32_16x16x64_i8 v[104:107], v[20:23], v[140:143], v[104:107]
	v_mfma_i32_16x16x64_i8 v[96:99], v[28:31], v[140:143], v[96:99]
	v_mfma_i32_16x16x64_i8 v[48:51], v[20:23], v[156:159], v[48:51]
	v_mfma_i32_16x16x64_i8 v[16:19], v[28:31], v[156:159], v[16:19]
	v_mfma_i32_16x16x64_i8 v[8:11], v[20:23], v[172:175], v[8:11]
	v_mfma_i32_16x16x64_i8 v[0:3], v[28:31], v[172:175], v[0:3]
	v_mfma_i32_16x16x64_i8 v[120:123], v[24:27], v[132:135], v[120:123]
	v_mfma_i32_16x16x64_i8 v[112:115], v[32:35], v[132:135], v[112:115]
	v_mfma_i32_16x16x64_i8 v[104:107], v[24:27], v[148:151], v[104:107]
	v_mfma_i32_16x16x64_i8 v[96:99], v[32:35], v[148:151], v[96:99]
	v_mfma_i32_16x16x64_i8 v[48:51], v[24:27], v[164:167], v[48:51]
	v_mfma_i32_16x16x64_i8 v[16:19], v[32:35], v[164:167], v[16:19]
	v_mfma_i32_16x16x64_i8 v[8:11], v[24:27], v[180:183], v[8:11]
	v_mfma_i32_16x16x64_i8 v[0:3], v[32:35], v[180:183], v[0:3]
	v_mfma_i32_16x16x64_i8 v[20:23], v[36:39], v[92:95], v[124:127]
	v_mfma_i32_16x16x64_i8 v[124:127], v[40:43], v[132:135], v[20:23]
	v_mfma_i32_16x16x64_i8 v[20:23], v[52:55], v[92:95], v[116:119]
	v_mfma_i32_16x16x64_i8 v[116:119], v[56:59], v[132:135], v[20:23]
	v_mfma_i32_16x16x64_i8 v[20:23], v[36:39], v[140:143], v[108:111]
	v_mfma_i32_16x16x64_i8 v[108:111], v[40:43], v[148:151], v[20:23]
	v_mfma_i32_16x16x64_i8 v[20:23], v[52:55], v[140:143], v[100:103]
	v_mfma_i32_16x16x64_i8 v[100:103], v[56:59], v[148:151], v[20:23]
	v_mfma_i32_16x16x64_i8 v[20:23], v[36:39], v[156:159], v[60:63]
	v_mfma_i32_16x16x64_i8 v[60:63], v[40:43], v[164:167], v[20:23]
	v_mfma_i32_16x16x64_i8 v[20:23], v[52:55], v[156:159], v[44:47]
	v_mfma_i32_16x16x64_i8 v[12:15], v[36:39], v[172:175], v[12:15]
	v_mfma_i32_16x16x64_i8 v[4:7], v[52:55], v[172:175], v[4:7]
	v_mfma_i32_16x16x64_i8 v[44:47], v[56:59], v[164:167], v[20:23]
	v_mfma_i32_16x16x64_i8 v[12:15], v[40:43], v[180:183], v[12:15]
	v_mfma_i32_16x16x64_i8 v[4:7], v[56:59], v[180:183], v[4:7]
	s_setprio 0
	s_barrier
	ds_read_b128 v[36:39], v207
	ds_read_b128 v[28:31], v207 offset:1024
	ds_read_b128 v[24:27], v207 offset:2048
	ds_read_b128 v[20:23], v207 offset:3072
	ds_read_b128 v[56:59], v208
	ds_read_b128 v[52:55], v208 offset:1024
	ds_read_b128 v[40:43], v208 offset:2048
	ds_read_b128 v[32:35], v208 offset:3072
	ds_read_b128 v[92:95], v206 offset:32768
	ds_read_b128 v[132:135], v206 offset:33792
	ds_read_b128 v[140:143], v206 offset:34816
	ds_read_b128 v[148:151], v206 offset:35840
	ds_read_b128 v[192:195], v206 offset:36864
	ds_read_b128 v[210:213], v206 offset:37888
	ds_read_b128 v[214:217], v206 offset:38912
	ds_read_b128 v[218:221], v206 offset:39936
	s_add_u32 s26, s38, 0x40000
	s_addc_u32 s27, s39, 0
	s_add_i32 m0, s46, 0x4000
	s_nop 0
	global_load_lds_dwordx4 v199, s[26:27]
	s_nop 0
	s_add_i32 m0, s46, 0x6000
	s_nop 0
	global_load_lds_dwordx4 v201, s[26:27]
	s_waitcnt vmcnt(8)
	s_waitcnt lgkmcnt(0)
	s_barrier
	s_setprio 1
	v_mfma_i32_16x16x64_i8 v[156:159], v[36:39], v[92:95], v[184:187]
	v_mfma_i32_16x16x64_i8 v[184:187], v[28:31], v[132:135], v[156:159]
	v_mfma_i32_16x16x64_i8 v[156:159], v[24:27], v[92:95], v[176:179]
	v_mfma_i32_16x16x64_i8 v[176:179], v[20:23], v[132:135], v[156:159]
	v_mfma_i32_16x16x64_i8 v[156:159], v[36:39], v[140:143], v[168:171]
	v_mfma_i32_16x16x64_i8 v[168:171], v[28:31], v[148:151], v[156:159]
	v_mfma_i32_16x16x64_i8 v[156:159], v[24:27], v[140:143], v[160:163]
	v_mfma_i32_16x16x64_i8 v[152:155], v[36:39], v[192:195], v[152:155]
	v_mfma_i32_16x16x64_i8 v[144:147], v[24:27], v[192:195], v[144:147]
	v_mfma_i32_16x16x64_i8 v[136:139], v[36:39], v[214:217], v[136:139]
	v_mfma_i32_16x16x64_i8 v[128:131], v[24:27], v[214:217], v[128:131]
	v_mfma_i32_16x16x64_i8 v[160:163], v[20:23], v[148:151], v[156:159]
	v_mfma_i32_16x16x64_i8 v[152:155], v[28:31], v[210:213], v[152:155]
	v_mfma_i32_16x16x64_i8 v[144:147], v[20:23], v[210:213], v[144:147]
	v_mfma_i32_16x16x64_i8 v[136:139], v[28:31], v[218:221], v[136:139]
	v_mfma_i32_16x16x64_i8 v[128:131], v[20:23], v[218:221], v[128:131]
	v_mfma_i32_16x16x64_i8 v[64:67], v[40:43], v[92:95], v[64:67]
	v_mfma_i32_16x16x64_i8 v[180:183], v[32:35], v[132:135], v[64:67]
	v_mfma_i32_16x16x64_i8 v[64:67], v[56:59], v[140:143], v[68:71]
	v_mfma_i32_16x16x64_i8 v[172:175], v[52:55], v[148:151], v[64:67]
	v_mfma_i32_16x16x64_i8 v[64:67], v[40:43], v[140:143], v[72:75]
	v_mfma_i32_16x16x64_i8 v[156:159], v[56:59], v[92:95], v[188:191]
	v_mfma_i32_16x16x64_i8 v[164:167], v[32:35], v[148:151], v[64:67]
	v_mfma_i32_16x16x64_i8 v[64:67], v[56:59], v[192:195], v[76:79]
	v_mfma_i32_16x16x64_i8 v[188:191], v[52:55], v[132:135], v[156:159]
	v_mfma_i32_16x16x64_i8 v[156:159], v[52:55], v[210:213], v[64:67]
	v_mfma_i32_16x16x64_i8 v[64:67], v[40:43], v[192:195], v[80:83]
	v_mfma_i32_16x16x64_i8 v[148:151], v[32:35], v[210:213], v[64:67]
	v_mfma_i32_16x16x64_i8 v[64:67], v[56:59], v[214:217], v[84:87]
	v_mfma_i32_16x16x64_i8 v[140:143], v[52:55], v[218:221], v[64:67]
	v_mfma_i32_16x16x64_i8 v[64:67], v[40:43], v[214:217], v[88:91]
	v_mfma_i32_16x16x64_i8 v[132:135], v[32:35], v[218:221], v[64:67]
	s_setprio 0
	s_barrier
	ds_read_b128 v[92:95], v206 offset:49152
	ds_read_b128 v[88:91], v206 offset:50176
	ds_read_b128 v[84:87], v206 offset:51200
	ds_read_b128 v[80:83], v206 offset:52224
	ds_read_b128 v[76:79], v206 offset:53248
	ds_read_b128 v[72:75], v206 offset:54272
	ds_read_b128 v[68:71], v206 offset:55296
	ds_read_b128 v[64:67], v206 offset:56320
	s_add_i32 m0, s46, 0x18000
	s_nop 0
	global_load_lds_dwordx4 v200, s[36:37]
	s_nop 0
	s_add_i32 m0, s46, 0x1a000
	s_nop 0
	global_load_lds_dwordx4 v202, s[36:37]
	s_add_u32 s26, s34, 0x40080
	s_addc_u32 s27, s35, 0
	s_add_i32 m0, s46, 0x1c000
	s_nop 0
	global_load_lds_dwordx4 v200, s[26:27]
	s_nop 0
	s_add_i32 m0, s46, 0x1e000
	s_nop 0
	global_load_lds_dwordx4 v202, s[26:27]
	s_nop 0
	s_add_i32 m0, s46, 0x8000
	s_nop 0
	global_load_lds_dwordx4 v199, s[30:31]
	s_nop 0
	s_add_i32 m0, s46, 0xa000
	s_nop 0
	global_load_lds_dwordx4 v201, s[30:31]
	s_waitcnt vmcnt(8)
	s_waitcnt lgkmcnt(0)
	s_barrier
	s_setprio 1
	v_mfma_i32_16x16x64_i8 v[120:123], v[36:39], v[92:95], v[120:123]
	v_mfma_i32_16x16x64_i8 v[112:115], v[24:27], v[92:95], v[112:115]
	v_mfma_i32_16x16x64_i8 v[104:107], v[36:39], v[84:87], v[104:107]
	v_mfma_i32_16x16x64_i8 v[96:99], v[24:27], v[84:87], v[96:99]
	v_mfma_i32_16x16x64_i8 v[48:51], v[36:39], v[76:79], v[48:51]
	v_mfma_i32_16x16x64_i8 v[16:19], v[24:27], v[76:79], v[16:19]
	v_mfma_i32_16x16x64_i8 v[8:11], v[36:39], v[68:71], v[8:11]
	v_mfma_i32_16x16x64_i8 v[0:3], v[24:27], v[68:71], v[0:3]
	v_mfma_i32_16x16x64_i8 v[120:123], v[28:31], v[88:91], v[120:123]
	v_mfma_i32_16x16x64_i8 v[112:115], v[20:23], v[88:91], v[112:115]
	v_mfma_i32_16x16x64_i8 v[104:107], v[28:31], v[80:83], v[104:107]
	v_mfma_i32_16x16x64_i8 v[96:99], v[20:23], v[80:83], v[96:99]
	v_mfma_i32_16x16x64_i8 v[48:51], v[28:31], v[72:75], v[48:51]
	v_mfma_i32_16x16x64_i8 v[16:19], v[20:23], v[72:75], v[16:19]
	v_mfma_i32_16x16x64_i8 v[8:11], v[28:31], v[64:67], v[8:11]
	v_mfma_i32_16x16x64_i8 v[0:3], v[20:23], v[64:67], v[0:3]
	v_mfma_i32_16x16x64_i8 v[124:127], v[56:59], v[92:95], v[124:127]
	v_mfma_i32_16x16x64_i8 v[116:119], v[40:43], v[92:95], v[116:119]
	v_mfma_i32_16x16x64_i8 v[108:111], v[56:59], v[84:87], v[108:111]
	v_mfma_i32_16x16x64_i8 v[100:103], v[40:43], v[84:87], v[100:103]
	v_mfma_i32_16x16x64_i8 v[60:63], v[56:59], v[76:79], v[60:63]
	v_mfma_i32_16x16x64_i8 v[44:47], v[40:43], v[76:79], v[44:47]
	v_mfma_i32_16x16x64_i8 v[12:15], v[56:59], v[68:71], v[12:15]
	v_mfma_i32_16x16x64_i8 v[4:7], v[40:43], v[68:71], v[4:7]
	v_mfma_i32_16x16x64_i8 v[124:127], v[52:55], v[88:91], v[124:127]
	v_mfma_i32_16x16x64_i8 v[116:119], v[32:35], v[88:91], v[116:119]
	v_mfma_i32_16x16x64_i8 v[108:111], v[52:55], v[80:83], v[108:111]
	v_mfma_i32_16x16x64_i8 v[100:103], v[32:35], v[80:83], v[100:103]
	v_mfma_i32_16x16x64_i8 v[60:63], v[52:55], v[72:75], v[60:63]
	v_mfma_i32_16x16x64_i8 v[44:47], v[32:35], v[72:75], v[44:47]
	v_mfma_i32_16x16x64_i8 v[12:15], v[52:55], v[64:67], v[12:15]
	v_mfma_i32_16x16x64_i8 v[4:7], v[32:35], v[64:67], v[4:7]
	s_setprio 0
	s_barrier
	s_add_i32 s17, s17, 2
	s_add_u32 s61, s61, 0x100
	s_addc_u32 s62, s62, 0
	s_cmp_gt_u32 s17, 13
	s_cbranch_scc1 .LBB0_757
	s_mov_b64 s[26:27], s[24:25]
	s_branch .LBB0_753

.LBB0_837:
	s_waitcnt lgkmcnt(0)
	ds_read_b128 v[0:3], v181
	ds_read_b128 v[4:7], v181 offset:1024
	ds_read_b128 v[8:11], v181 offset:2048
	ds_read_b128 v[12:15], v181 offset:3072
	ds_read_b128 v[16:19], v182
	ds_read_b128 v[20:23], v182 offset:1024
	ds_read_b128 v[24:27], v182 offset:2048
	ds_read_b128 v[28:31], v182 offset:3072
	s_add_u32 s28, s22, 0x100
	s_addc_u32 s29, s23, 0
	s_add_u32 s52, s24, 0x100
	s_addc_u32 s53, s25, 0
	s_add_u32 s6, s22, 0x180
	s_addc_u32 s7, s23, 0
	ds_read_b128 v[32:35], v183
	ds_read_b128 v[36:39], v183 offset:1024
	ds_read_b128 v[40:43], v183 offset:2048
	ds_read_b128 v[44:47], v183 offset:3072
	ds_read_b128 v[48:51], v183 offset:4096
	ds_read_b128 v[52:55], v183 offset:5120
	ds_read_b128 v[56:59], v183 offset:6144
	ds_read_b128 v[60:63], v183 offset:7168
	s_add_u32 s26, s24, 0x180
	s_addc_u32 s27, s25, 0
	s_add_u32 s54, s22, 0x160080
	s_addc_u32 s55, s23, 0
	s_add_i32 m0, s36, 0xc000
	s_nop 0
	global_load_lds_dwordx4 v175, s[54:55]
	s_nop 0
	s_add_i32 m0, s36, 0xe000
	s_nop 0
	global_load_lds_dwordx4 v177, s[54:55]
	s_waitcnt vmcnt(8)
	s_waitcnt lgkmcnt(0)
	s_barrier
	s_setprio 1
	v_mfma_f32_16x16x32_bf16 v[88:91], v[0:3], v[56:59], 0
	v_mfma_f32_16x16x32_bf16 v[64:67], v[0:3], v[32:35], 0
	v_mfma_f32_16x16x32_bf16 v[68:71], v[8:11], v[32:35], 0
	v_mfma_f32_16x16x32_bf16 v[72:75], v[0:3], v[40:43], 0
	v_mfma_f32_16x16x32_bf16 v[76:79], v[8:11], v[40:43], 0
	v_mfma_f32_16x16x32_bf16 v[80:83], v[0:3], v[48:51], 0
	v_mfma_f32_16x16x32_bf16 v[84:87], v[8:11], v[48:51], 0
	v_mfma_f32_16x16x32_bf16 v[96:99], v[4:7], v[60:63], v[88:91]
	v_mfma_f32_16x16x32_bf16 v[88:91], v[8:11], v[56:59], 0
	v_mfma_f32_16x16x32_bf16 v[64:67], v[4:7], v[36:39], v[64:67]
	v_mfma_f32_16x16x32_bf16 v[68:71], v[12:15], v[36:39], v[68:71]
	v_mfma_f32_16x16x32_bf16 v[72:75], v[4:7], v[44:47], v[72:75]
	v_mfma_f32_16x16x32_bf16 v[76:79], v[12:15], v[44:47], v[76:79]
	v_mfma_f32_16x16x32_bf16 v[80:83], v[4:7], v[52:55], v[80:83]
	v_mfma_f32_16x16x32_bf16 v[84:87], v[12:15], v[52:55], v[84:87]
	v_mfma_f32_16x16x32_bf16 v[100:103], v[12:15], v[60:63], v[88:91]
	v_mfma_f32_16x16x32_bf16 v[88:91], v[16:19], v[32:35], 0
	v_mfma_f32_16x16x32_bf16 v[32:35], v[24:27], v[32:35], 0
	v_mfma_f32_16x16x32_bf16 v[112:115], v[20:23], v[36:39], v[88:91]
	v_mfma_f32_16x16x32_bf16 v[32:35], v[28:31], v[36:39], v[32:35]
	v_mfma_f32_16x16x32_bf16 v[36:39], v[16:19], v[40:43], 0
	v_mfma_f32_16x16x32_bf16 v[40:43], v[24:27], v[40:43], 0
	v_mfma_f32_16x16x32_bf16 v[36:39], v[20:23], v[44:47], v[36:39]
	v_mfma_f32_16x16x32_bf16 v[40:43], v[28:31], v[44:47], v[40:43]
	v_mfma_f32_16x16x32_bf16 v[44:47], v[16:19], v[48:51], 0
	v_mfma_f32_16x16x32_bf16 v[48:51], v[24:27], v[48:51], 0
	v_mfma_f32_16x16x32_bf16 v[44:47], v[20:23], v[52:55], v[44:47]
	v_mfma_f32_16x16x32_bf16 v[48:51], v[28:31], v[52:55], v[48:51]
	v_mfma_f32_16x16x32_bf16 v[52:55], v[16:19], v[56:59], 0
	v_mfma_f32_16x16x32_bf16 v[56:59], v[24:27], v[56:59], 0
	v_mfma_f32_16x16x32_bf16 v[52:55], v[20:23], v[60:63], v[52:55]
	v_mfma_f32_16x16x32_bf16 v[56:59], v[28:31], v[60:63], v[56:59]
	s_setprio 0
	s_barrier
	ds_read_b128 v[60:63], v183 offset:16384
	ds_read_b128 v[88:91], v183 offset:17408
	ds_read_b128 v[92:95], v183 offset:18432
	ds_read_b128 v[104:107], v183 offset:19456
	ds_read_b128 v[108:111], v183 offset:20480
	ds_read_b128 v[116:119], v183 offset:21504
	ds_read_b128 v[120:123], v183 offset:22528
	ds_read_b128 v[124:127], v183 offset:23552
	s_add_i32 m0, s36, 0x10000
	s_nop 0
	global_load_lds_dwordx4 v176, s[52:53]
	s_nop 0
	s_add_i32 m0, s36, 0x12000
	s_nop 0
	global_load_lds_dwordx4 v178, s[52:53]
	s_add_u32 s52, s24, 0x160100
	s_addc_u32 s53, s25, 0
	s_add_i32 m0, s36, 0x14000
	s_nop 0
	global_load_lds_dwordx4 v176, s[52:53]
	s_nop 0
	s_add_i32 m0, s36, 0x16000
	s_nop 0
	global_load_lds_dwordx4 v178, s[52:53]
	s_nop 0
	s_add_i32 m0, s36, 0
	s_nop 0
	global_load_lds_dwordx4 v175, s[28:29]
	s_nop 0
	s_add_i32 m0, s36, 0x2000
	s_nop 0
	global_load_lds_dwordx4 v177, s[28:29]
	s_waitcnt vmcnt(8)
	s_waitcnt lgkmcnt(0)
	s_barrier
	s_setprio 1
	v_mfma_f32_16x16x32_bf16 v[128:131], v[0:3], v[60:63], 0
	v_mfma_f32_16x16x32_bf16 v[136:139], v[4:7], v[88:91], v[128:131]
	v_mfma_f32_16x16x32_bf16 v[128:131], v[8:11], v[60:63], 0
	v_mfma_f32_16x16x32_bf16 v[140:143], v[12:15], v[88:91], v[128:131]
	v_mfma_f32_16x16x32_bf16 v[128:131], v[0:3], v[92:95], 0
	v_mfma_f32_16x16x32_bf16 v[144:147], v[4:7], v[104:107], v[128:131]
	v_mfma_f32_16x16x32_bf16 v[128:131], v[8:11], v[92:95], 0
	v_mfma_f32_16x16x32_bf16 v[148:151], v[12:15], v[104:107], v[128:131]
	v_mfma_f32_16x16x32_bf16 v[128:131], v[0:3], v[108:111], 0
	v_mfma_f32_16x16x32_bf16 v[0:3], v[0:3], v[120:123], 0
	v_mfma_f32_16x16x32_bf16 v[156:159], v[4:7], v[116:119], v[128:131]
	v_mfma_f32_16x16x32_bf16 v[0:3], v[4:7], v[124:127], v[0:3]
	v_mfma_f32_16x16x32_bf16 v[4:7], v[8:11], v[120:123], 0
	v_mfma_f32_16x16x32_bf16 v[128:131], v[8:11], v[108:111], 0
	v_mfma_f32_16x16x32_bf16 v[4:7], v[12:15], v[124:127], v[4:7]
	v_mfma_f32_16x16x32_bf16 v[160:163], v[12:15], v[116:119], v[128:131]
	v_mfma_f32_16x16x32_bf16 v[8:11], v[16:19], v[60:63], 0
	v_mfma_f32_16x16x32_bf16 v[164:167], v[20:23], v[88:91], v[8:11]
	v_mfma_f32_16x16x32_bf16 v[8:11], v[24:27], v[60:63], 0
	v_mfma_f32_16x16x32_bf16 v[168:171], v[28:31], v[88:91], v[8:11]
	v_mfma_f32_16x16x32_bf16 v[8:11], v[16:19], v[92:95], 0
	v_mfma_f32_16x16x32_bf16 v[188:191], v[20:23], v[104:107], v[8:11]
	v_mfma_f32_16x16x32_bf16 v[8:11], v[24:27], v[92:95], 0
	v_mfma_f32_16x16x32_bf16 v[192:195], v[28:31], v[104:107], v[8:11]
	v_mfma_f32_16x16x32_bf16 v[8:11], v[16:19], v[108:111], 0
	v_mfma_f32_16x16x32_bf16 v[196:199], v[20:23], v[116:119], v[8:11]
	v_mfma_f32_16x16x32_bf16 v[8:11], v[24:27], v[108:111], 0
	v_mfma_f32_16x16x32_bf16 v[116:119], v[28:31], v[116:119], v[8:11]
	v_mfma_f32_16x16x32_bf16 v[8:11], v[16:19], v[120:123], 0
	v_mfma_f32_16x16x32_bf16 v[200:203], v[20:23], v[124:127], v[8:11]
	v_mfma_f32_16x16x32_bf16 v[8:11], v[24:27], v[120:123], 0
	v_mfma_f32_16x16x32_bf16 v[204:207], v[28:31], v[124:127], v[8:11]
	s_setprio 0
	s_barrier
	s_nop 4
	ds_read_b128 v[8:11], v184
	ds_read_b128 v[12:15], v184 offset:1024
	ds_read_b128 v[16:19], v184 offset:2048
	ds_read_b128 v[20:23], v184 offset:3072
	ds_read_b128 v[208:211], v185
	ds_read_b128 v[212:215], v185 offset:1024
	ds_read_b128 v[216:219], v185 offset:2048
	ds_read_b128 v[220:223], v185 offset:3072
	ds_read_b128 v[24:27], v183 offset:32768
	ds_read_b128 v[28:31], v183 offset:33792
	ds_read_b128 v[60:63], v183 offset:34816
	ds_read_b128 v[224:227], v183 offset:35840
	ds_read_b128 v[228:231], v183 offset:36864
	ds_read_b128 v[232:235], v183 offset:37888
	ds_read_b128 v[236:239], v183 offset:38912
	ds_read_b128 v[240:243], v183 offset:39936
	s_add_u32 s28, s22, 0x160100
	s_addc_u32 s29, s23, 0
	s_add_i32 m0, s36, 0x4000
	s_nop 0
	global_load_lds_dwordx4 v175, s[28:29]
	s_nop 0
	s_add_i32 m0, s36, 0x6000
	s_nop 0
	global_load_lds_dwordx4 v177, s[28:29]
	s_waitcnt vmcnt(8)
	s_waitcnt lgkmcnt(0)
	s_barrier
	s_setprio 1
	v_mfma_f32_16x16x32_bf16 v[64:67], v[8:11], v[24:27], v[64:67]
	v_mfma_f32_16x16x32_bf16 v[132:135], v[12:15], v[28:31], v[64:67]
	v_mfma_f32_16x16x32_bf16 v[64:67], v[16:19], v[24:27], v[68:71]
	v_mfma_f32_16x16x32_bf16 v[128:131], v[20:23], v[28:31], v[64:67]
	v_mfma_f32_16x16x32_bf16 v[64:67], v[8:11], v[60:63], v[72:75]
	v_mfma_f32_16x16x32_bf16 v[108:111], v[12:15], v[224:227], v[64:67]
	v_mfma_f32_16x16x32_bf16 v[64:67], v[16:19], v[60:63], v[76:79]
	v_mfma_f32_16x16x32_bf16 v[104:107], v[20:23], v[224:227], v[64:67]
	v_mfma_f32_16x16x32_bf16 v[64:67], v[8:11], v[228:231], v[80:83]
	v_mfma_f32_16x16x32_bf16 v[92:95], v[12:15], v[232:235], v[64:67]
	v_mfma_f32_16x16x32_bf16 v[64:67], v[16:19], v[228:231], v[84:87]
	v_mfma_f32_16x16x32_bf16 v[88:91], v[20:23], v[232:235], v[64:67]
	v_mfma_f32_16x16x32_bf16 v[64:67], v[8:11], v[236:239], v[96:99]
	v_mfma_f32_16x16x32_bf16 v[76:79], v[12:15], v[240:243], v[64:67]
	v_mfma_f32_16x16x32_bf16 v[64:67], v[16:19], v[236:239], v[100:103]
	v_mfma_f32_16x16x32_bf16 v[72:75], v[20:23], v[240:243], v[64:67]
	v_mfma_f32_16x16x32_bf16 v[64:67], v[208:211], v[24:27], v[112:115]
	v_mfma_f32_16x16x32_bf16 v[24:27], v[216:219], v[24:27], v[32:35]
	v_mfma_f32_16x16x32_bf16 v[120:123], v[220:223], v[28:31], v[24:27]
	v_mfma_f32_16x16x32_bf16 v[24:27], v[208:211], v[60:63], v[36:39]
	v_mfma_f32_16x16x32_bf16 v[100:103], v[212:215], v[224:227], v[24:27]
	v_mfma_f32_16x16x32_bf16 v[24:27], v[216:219], v[60:63], v[40:43]
	v_mfma_f32_16x16x32_bf16 v[96:99], v[220:223], v[224:227], v[24:27]
	v_mfma_f32_16x16x32_bf16 v[24:27], v[208:211], v[228:231], v[44:47]
	v_mfma_f32_16x16x32_bf16 v[84:87], v[212:215], v[232:235], v[24:27]
	v_mfma_f32_16x16x32_bf16 v[24:27], v[216:219], v[228:231], v[48:51]
	v_mfma_f32_16x16x32_bf16 v[80:83], v[220:223], v[232:235], v[24:27]
	v_mfma_f32_16x16x32_bf16 v[24:27], v[208:211], v[236:239], v[52:55]
	v_mfma_f32_16x16x32_bf16 v[68:71], v[212:215], v[240:243], v[24:27]
	v_mfma_f32_16x16x32_bf16 v[24:27], v[216:219], v[236:239], v[56:59]
	v_mfma_f32_16x16x32_bf16 v[124:127], v[212:215], v[28:31], v[64:67]
	v_mfma_f32_16x16x32_bf16 v[64:67], v[220:223], v[240:243], v[24:27]
	s_setprio 0
	s_barrier
	ds_read_b128 v[32:35], v183 offset:49152
	ds_read_b128 v[36:39], v183 offset:50176
	ds_read_b128 v[112:115], v183 offset:51200
	ds_read_b128 v[224:227], v183 offset:52224
	ds_read_b128 v[228:231], v183 offset:53248
	ds_read_b128 v[232:235], v183 offset:54272
	ds_read_b128 v[236:239], v183 offset:55296
	ds_read_b128 v[240:243], v183 offset:56320
	s_add_i32 m0, s36, 0x18000
	s_nop 0
	global_load_lds_dwordx4 v176, s[26:27]
	s_nop 0
	s_add_i32 m0, s36, 0x1a000
	s_nop 0
	global_load_lds_dwordx4 v178, s[26:27]
	s_add_u32 s26, s24, 0x160180
	s_addc_u32 s27, s25, 0
	s_add_i32 m0, s36, 0x1c000
	s_nop 0
	global_load_lds_dwordx4 v176, s[26:27]
	s_nop 0
	s_add_i32 m0, s36, 0x1e000
	s_nop 0
	global_load_lds_dwordx4 v178, s[26:27]
	s_nop 0
	s_add_i32 m0, s36, 0x8000
	s_nop 0
	global_load_lds_dwordx4 v175, s[6:7]
	s_nop 0
	s_add_i32 m0, s36, 0xa000
	s_nop 0
	global_load_lds_dwordx4 v177, s[6:7]
	s_waitcnt vmcnt(8)
	s_waitcnt lgkmcnt(0)
	s_barrier
	s_setprio 1
	v_mfma_f32_16x16x32_bf16 v[24:27], v[8:11], v[32:35], v[136:139]
	v_mfma_f32_16x16x32_bf16 v[60:63], v[12:15], v[36:39], v[24:27]
	v_mfma_f32_16x16x32_bf16 v[24:27], v[16:19], v[32:35], v[140:143]
	v_mfma_f32_16x16x32_bf16 v[56:59], v[20:23], v[36:39], v[24:27]
	v_mfma_f32_16x16x32_bf16 v[24:27], v[8:11], v[112:115], v[144:147]
	v_mfma_f32_16x16x32_bf16 v[44:47], v[12:15], v[224:227], v[24:27]
	v_mfma_f32_16x16x32_bf16 v[24:27], v[16:19], v[112:115], v[148:151]
	v_mfma_f32_16x16x32_bf16 v[40:43], v[20:23], v[224:227], v[24:27]
	v_mfma_f32_16x16x32_bf16 v[24:27], v[8:11], v[228:231], v[156:159]
	v_mfma_f32_16x16x32_bf16 v[0:3], v[8:11], v[236:239], v[0:3]
	v_mfma_f32_16x16x32_bf16 v[28:31], v[12:15], v[232:235], v[24:27]
	v_mfma_f32_16x16x32_bf16 v[24:27], v[16:19], v[228:231], v[160:163]
	v_mfma_f32_16x16x32_bf16 v[12:15], v[12:15], v[240:243], v[0:3]
	v_mfma_f32_16x16x32_bf16 v[0:3], v[16:19], v[236:239], v[4:7]
	v_mfma_f32_16x16x32_bf16 v[24:27], v[20:23], v[232:235], v[24:27]
	v_mfma_f32_16x16x32_bf16 v[8:11], v[20:23], v[240:243], v[0:3]
	v_mfma_f32_16x16x32_bf16 v[0:3], v[208:211], v[32:35], v[164:167]
	v_mfma_f32_16x16x32_bf16 v[52:55], v[212:215], v[36:39], v[0:3]
	v_mfma_f32_16x16x32_bf16 v[0:3], v[216:219], v[32:35], v[168:171]
	v_mfma_f32_16x16x32_bf16 v[48:51], v[220:223], v[36:39], v[0:3]
	v_mfma_f32_16x16x32_bf16 v[0:3], v[208:211], v[112:115], v[188:191]
	v_mfma_f32_16x16x32_bf16 v[36:39], v[212:215], v[224:227], v[0:3]
	v_mfma_f32_16x16x32_bf16 v[0:3], v[216:219], v[112:115], v[192:195]
	v_mfma_f32_16x16x32_bf16 v[32:35], v[220:223], v[224:227], v[0:3]
	v_mfma_f32_16x16x32_bf16 v[0:3], v[208:211], v[228:231], v[196:199]
	v_mfma_f32_16x16x32_bf16 v[20:23], v[212:215], v[232:235], v[0:3]
	v_mfma_f32_16x16x32_bf16 v[0:3], v[216:219], v[228:231], v[116:119]
	v_mfma_f32_16x16x32_bf16 v[16:19], v[220:223], v[232:235], v[0:3]
	v_mfma_f32_16x16x32_bf16 v[0:3], v[208:211], v[236:239], v[200:203]
	v_mfma_f32_16x16x32_bf16 v[4:7], v[212:215], v[240:243], v[0:3]
	v_mfma_f32_16x16x32_bf16 v[0:3], v[216:219], v[236:239], v[204:207]
	v_mfma_f32_16x16x32_bf16 v[0:3], v[220:223], v[240:243], v[0:3]
	s_setprio 0
	s_barrier
	s_add_u32 s51, s22, 0x200
	s_addc_u32 s52, s23, 0
	s_add_u32 s53, s24, 0x200
	s_addc_u32 s54, s25, 0
	s_add_u32 s6, s22, 0x160180
	s_addc_u32 s7, s23, 0
	s_mov_b32 s55, 0
.LBB0_838:
	ds_read_b128 v[112:115], v181
	ds_read_b128 v[116:119], v181 offset:1024
	ds_read_b128 v[136:139], v181 offset:2048
	ds_read_b128 v[140:143], v181 offset:3072
	ds_read_b128 v[144:147], v182
	ds_read_b128 v[148:151], v182 offset:1024
	ds_read_b128 v[156:159], v182 offset:2048
	ds_read_b128 v[160:163], v182 offset:3072
	s_cmpk_eq_i32 s55, 0x54
	s_cselect_b32 s28, s18, s51
	s_cselect_b32 s29, s19, s52
	s_cselect_b32 s24, s20, s53
	s_cselect_b32 s25, s21, s54
	s_add_u32 s22, s28, 0x80
	s_addc_u32 s23, s29, 0
	ds_read_b128 v[164:167], v183
	ds_read_b128 v[168:171], v183 offset:1024
	ds_read_b128 v[188:191], v183 offset:2048
	ds_read_b128 v[192:195], v183 offset:3072
	ds_read_b128 v[196:199], v183 offset:4096
	ds_read_b128 v[200:203], v183 offset:5120
	ds_read_b128 v[204:207], v183 offset:6144
	ds_read_b128 v[208:211], v183 offset:7168
	s_add_u32 s26, s24, 0x80
	s_addc_u32 s27, s25, 0
	s_add_i32 m0, s36, 0xc000
	s_nop 0
	global_load_lds_dwordx4 v175, s[6:7]
	s_nop 0
	s_add_i32 m0, s36, 0xe000
	s_nop 0
	global_load_lds_dwordx4 v177, s[6:7]
	s_waitcnt vmcnt(8)
	s_waitcnt lgkmcnt(0)
	s_barrier
	s_setprio 1
	v_mfma_f32_16x16x32_bf16 v[132:135], v[112:115], v[164:167], v[132:135]
	v_mfma_f32_16x16x32_bf16 v[128:131], v[136:139], v[164:167], v[128:131]
	v_mfma_f32_16x16x32_bf16 v[108:111], v[112:115], v[188:191], v[108:111]
	v_mfma_f32_16x16x32_bf16 v[104:107], v[136:139], v[188:191], v[104:107]
	v_mfma_f32_16x16x32_bf16 v[92:95], v[112:115], v[196:199], v[92:95]
	v_mfma_f32_16x16x32_bf16 v[88:91], v[136:139], v[196:199], v[88:91]
	v_mfma_f32_16x16x32_bf16 v[76:79], v[112:115], v[204:207], v[76:79]
	v_mfma_f32_16x16x32_bf16 v[72:75], v[136:139], v[204:207], v[72:75]
	v_mfma_f32_16x16x32_bf16 v[132:135], v[116:119], v[168:171], v[132:135]
	v_mfma_f32_16x16x32_bf16 v[128:131], v[140:143], v[168:171], v[128:131]
	v_mfma_f32_16x16x32_bf16 v[108:111], v[116:119], v[192:195], v[108:111]
	v_mfma_f32_16x16x32_bf16 v[104:107], v[140:143], v[192:195], v[104:107]
	v_mfma_f32_16x16x32_bf16 v[92:95], v[116:119], v[200:203], v[92:95]
	v_mfma_f32_16x16x32_bf16 v[88:91], v[140:143], v[200:203], v[88:91]
	v_mfma_f32_16x16x32_bf16 v[76:79], v[116:119], v[208:211], v[76:79]
	v_mfma_f32_16x16x32_bf16 v[72:75], v[140:143], v[208:211], v[72:75]
	v_mfma_f32_16x16x32_bf16 v[124:127], v[144:147], v[164:167], v[124:127]
	v_mfma_f32_16x16x32_bf16 v[120:123], v[156:159], v[164:167], v[120:123]
	v_mfma_f32_16x16x32_bf16 v[100:103], v[144:147], v[188:191], v[100:103]
	v_mfma_f32_16x16x32_bf16 v[96:99], v[156:159], v[188:191], v[96:99]
	v_mfma_f32_16x16x32_bf16 v[84:87], v[144:147], v[196:199], v[84:87]
	v_mfma_f32_16x16x32_bf16 v[80:83], v[156:159], v[196:199], v[80:83]
	v_mfma_f32_16x16x32_bf16 v[68:71], v[144:147], v[204:207], v[68:71]
	v_mfma_f32_16x16x32_bf16 v[64:67], v[156:159], v[204:207], v[64:67]
	v_mfma_f32_16x16x32_bf16 v[124:127], v[148:151], v[168:171], v[124:127]
	v_mfma_f32_16x16x32_bf16 v[120:123], v[160:163], v[168:171], v[120:123]
	v_mfma_f32_16x16x32_bf16 v[100:103], v[148:151], v[192:195], v[100:103]
	v_mfma_f32_16x16x32_bf16 v[96:99], v[160:163], v[192:195], v[96:99]
	v_mfma_f32_16x16x32_bf16 v[84:87], v[148:151], v[200:203], v[84:87]
	v_mfma_f32_16x16x32_bf16 v[80:83], v[160:163], v[200:203], v[80:83]
	v_mfma_f32_16x16x32_bf16 v[68:71], v[148:151], v[208:211], v[68:71]
	v_mfma_f32_16x16x32_bf16 v[64:67], v[160:163], v[208:211], v[64:67]
	s_setprio 0
	s_barrier
	ds_read_b128 v[164:167], v183 offset:16384
	ds_read_b128 v[168:171], v183 offset:17408
	ds_read_b128 v[188:191], v183 offset:18432
	ds_read_b128 v[192:195], v183 offset:19456
	ds_read_b128 v[196:199], v183 offset:20480
	ds_read_b128 v[200:203], v183 offset:21504
	ds_read_b128 v[204:207], v183 offset:22528
	ds_read_b128 v[208:211], v183 offset:23552
	s_add_i32 m0, s36, 0x10000
	s_nop 0
	global_load_lds_dwordx4 v176, s[24:25]
	s_nop 0
	s_add_i32 m0, s36, 0x12000
	s_nop 0
	global_load_lds_dwordx4 v178, s[24:25]
	s_add_u32 s56, s24, 0x160000
	s_addc_u32 s57, s25, 0
	s_add_i32 m0, s36, 0x14000
	s_nop 0
	global_load_lds_dwordx4 v176, s[56:57]
	s_nop 0
	s_add_i32 m0, s36, 0x16000
	s_nop 0
	global_load_lds_dwordx4 v178, s[56:57]
	s_nop 0
	s_add_i32 m0, s36, 0
	s_nop 0
	global_load_lds_dwordx4 v175, s[28:29]
	s_nop 0
	s_add_i32 m0, s36, 0x2000
	s_nop 0
	global_load_lds_dwordx4 v177, s[28:29]
	s_waitcnt vmcnt(8)
	s_waitcnt lgkmcnt(0)
	s_barrier
	s_setprio 1
	v_mfma_f32_16x16x32_bf16 v[60:63], v[112:115], v[164:167], v[60:63]
	v_mfma_f32_16x16x32_bf16 v[56:59], v[136:139], v[164:167], v[56:59]
	v_mfma_f32_16x16x32_bf16 v[44:47], v[112:115], v[188:191], v[44:47]
	v_mfma_f32_16x16x32_bf16 v[40:43], v[136:139], v[188:191], v[40:43]
	v_mfma_f32_16x16x32_bf16 v[28:31], v[112:115], v[196:199], v[28:31]
	v_mfma_f32_16x16x32_bf16 v[24:27], v[136:139], v[196:199], v[24:27]
	v_mfma_f32_16x16x32_bf16 v[12:15], v[112:115], v[204:207], v[12:15]
	v_mfma_f32_16x16x32_bf16 v[8:11], v[136:139], v[204:207], v[8:11]
	v_mfma_f32_16x16x32_bf16 v[60:63], v[116:119], v[168:171], v[60:63]
	v_mfma_f32_16x16x32_bf16 v[56:59], v[140:143], v[168:171], v[56:59]
	v_mfma_f32_16x16x32_bf16 v[44:47], v[116:119], v[192:195], v[44:47]
	v_mfma_f32_16x16x32_bf16 v[40:43], v[140:143], v[192:195], v[40:43]
	v_mfma_f32_16x16x32_bf16 v[28:31], v[116:119], v[200:203], v[28:31]
	v_mfma_f32_16x16x32_bf16 v[24:27], v[140:143], v[200:203], v[24:27]
	v_mfma_f32_16x16x32_bf16 v[12:15], v[116:119], v[208:211], v[12:15]
	v_mfma_f32_16x16x32_bf16 v[8:11], v[140:143], v[208:211], v[8:11]
	v_mfma_f32_16x16x32_bf16 v[52:55], v[144:147], v[164:167], v[52:55]
	v_mfma_f32_16x16x32_bf16 v[48:51], v[156:159], v[164:167], v[48:51]
	v_mfma_f32_16x16x32_bf16 v[36:39], v[144:147], v[188:191], v[36:39]
	v_mfma_f32_16x16x32_bf16 v[32:35], v[156:159], v[188:191], v[32:35]
	v_mfma_f32_16x16x32_bf16 v[20:23], v[144:147], v[196:199], v[20:23]
	v_mfma_f32_16x16x32_bf16 v[16:19], v[156:159], v[196:199], v[16:19]
	v_mfma_f32_16x16x32_bf16 v[4:7], v[144:147], v[204:207], v[4:7]
	v_mfma_f32_16x16x32_bf16 v[0:3], v[156:159], v[204:207], v[0:3]
	v_mfma_f32_16x16x32_bf16 v[52:55], v[148:151], v[168:171], v[52:55]
	v_mfma_f32_16x16x32_bf16 v[48:51], v[160:163], v[168:171], v[48:51]
	v_mfma_f32_16x16x32_bf16 v[36:39], v[148:151], v[192:195], v[36:39]
	v_mfma_f32_16x16x32_bf16 v[32:35], v[160:163], v[192:195], v[32:35]
	v_mfma_f32_16x16x32_bf16 v[20:23], v[148:151], v[200:203], v[20:23]
	v_mfma_f32_16x16x32_bf16 v[16:19], v[160:163], v[200:203], v[16:19]
	v_mfma_f32_16x16x32_bf16 v[4:7], v[148:151], v[208:211], v[4:7]
	v_mfma_f32_16x16x32_bf16 v[0:3], v[160:163], v[208:211], v[0:3]
	s_setprio 0
	s_barrier
	ds_read_b128 v[112:115], v184
	ds_read_b128 v[116:119], v184 offset:1024
	ds_read_b128 v[136:139], v184 offset:2048
	ds_read_b128 v[140:143], v184 offset:3072
	ds_read_b128 v[144:147], v185
	ds_read_b128 v[148:151], v185 offset:1024
	ds_read_b128 v[156:159], v185 offset:2048
	ds_read_b128 v[160:163], v185 offset:3072
	ds_read_b128 v[164:167], v183 offset:32768
	ds_read_b128 v[168:171], v183 offset:33792
	ds_read_b128 v[188:191], v183 offset:34816
	ds_read_b128 v[192:195], v183 offset:35840
	ds_read_b128 v[196:199], v183 offset:36864
	ds_read_b128 v[200:203], v183 offset:37888
	ds_read_b128 v[204:207], v183 offset:38912
	ds_read_b128 v[208:211], v183 offset:39936
	s_add_u32 s28, s28, 0x160000
	s_addc_u32 s29, s29, 0
	s_add_i32 m0, s36, 0x4000
	s_nop 0
	global_load_lds_dwordx4 v175, s[28:29]
	s_nop 0
	s_add_i32 m0, s36, 0x6000
	s_nop 0
	global_load_lds_dwordx4 v177, s[28:29]
	s_waitcnt vmcnt(8)
	s_waitcnt lgkmcnt(0)
	s_barrier
	s_setprio 1
	v_mfma_f32_16x16x32_bf16 v[132:135], v[112:115], v[164:167], v[132:135]
	v_mfma_f32_16x16x32_bf16 v[128:131], v[136:139], v[164:167], v[128:131]
	v_mfma_f32_16x16x32_bf16 v[108:111], v[112:115], v[188:191], v[108:111]
	v_mfma_f32_16x16x32_bf16 v[104:107], v[136:139], v[188:191], v[104:107]
	v_mfma_f32_16x16x32_bf16 v[92:95], v[112:115], v[196:199], v[92:95]
	v_mfma_f32_16x16x32_bf16 v[88:91], v[136:139], v[196:199], v[88:91]
	v_mfma_f32_16x16x32_bf16 v[76:79], v[112:115], v[204:207], v[76:79]
	v_mfma_f32_16x16x32_bf16 v[72:75], v[136:139], v[204:207], v[72:75]
	v_mfma_f32_16x16x32_bf16 v[132:135], v[116:119], v[168:171], v[132:135]
	v_mfma_f32_16x16x32_bf16 v[128:131], v[140:143], v[168:171], v[128:131]
	v_mfma_f32_16x16x32_bf16 v[108:111], v[116:119], v[192:195], v[108:111]
	v_mfma_f32_16x16x32_bf16 v[104:107], v[140:143], v[192:195], v[104:107]
	v_mfma_f32_16x16x32_bf16 v[92:95], v[116:119], v[200:203], v[92:95]
	v_mfma_f32_16x16x32_bf16 v[88:91], v[140:143], v[200:203], v[88:91]
	v_mfma_f32_16x16x32_bf16 v[76:79], v[116:119], v[208:211], v[76:79]
	v_mfma_f32_16x16x32_bf16 v[72:75], v[140:143], v[208:211], v[72:75]
	v_mfma_f32_16x16x32_bf16 v[124:127], v[144:147], v[164:167], v[124:127]
	v_mfma_f32_16x16x32_bf16 v[120:123], v[156:159], v[164:167], v[120:123]
	v_mfma_f32_16x16x32_bf16 v[100:103], v[144:147], v[188:191], v[100:103]
	v_mfma_f32_16x16x32_bf16 v[96:99], v[156:159], v[188:191], v[96:99]
	v_mfma_f32_16x16x32_bf16 v[84:87], v[144:147], v[196:199], v[84:87]
	v_mfma_f32_16x16x32_bf16 v[80:83], v[156:159], v[196:199], v[80:83]
	v_mfma_f32_16x16x32_bf16 v[68:71], v[144:147], v[204:207], v[68:71]
	v_mfma_f32_16x16x32_bf16 v[64:67], v[156:159], v[204:207], v[64:67]
	v_mfma_f32_16x16x32_bf16 v[124:127], v[148:151], v[168:171], v[124:127]
	v_mfma_f32_16x16x32_bf16 v[120:123], v[160:163], v[168:171], v[120:123]
	v_mfma_f32_16x16x32_bf16 v[100:103], v[148:151], v[192:195], v[100:103]
	v_mfma_f32_16x16x32_bf16 v[96:99], v[160:163], v[192:195], v[96:99]
	v_mfma_f32_16x16x32_bf16 v[84:87], v[148:151], v[200:203], v[84:87]
	v_mfma_f32_16x16x32_bf16 v[80:83], v[160:163], v[200:203], v[80:83]
	v_mfma_f32_16x16x32_bf16 v[68:71], v[148:151], v[208:211], v[68:71]
	v_mfma_f32_16x16x32_bf16 v[64:67], v[160:163], v[208:211], v[64:67]
	s_setprio 0
	s_barrier
	ds_read_b128 v[164:167], v183 offset:49152
	ds_read_b128 v[168:171], v183 offset:50176
	ds_read_b128 v[188:191], v183 offset:51200
	ds_read_b128 v[192:195], v183 offset:52224
	ds_read_b128 v[196:199], v183 offset:53248
	ds_read_b128 v[200:203], v183 offset:54272
	ds_read_b128 v[204:207], v183 offset:55296
	ds_read_b128 v[208:211], v183 offset:56320
	s_add_i32 m0, s36, 0x18000
	s_nop 0
	global_load_lds_dwordx4 v176, s[26:27]
	s_nop 0
	s_add_i32 m0, s36, 0x1a000
	s_nop 0
	global_load_lds_dwordx4 v178, s[26:27]
	s_add_u32 s24, s24, 0x160080
	s_addc_u32 s25, s25, 0
	s_add_i32 m0, s36, 0x1c000
	s_nop 0
	global_load_lds_dwordx4 v176, s[24:25]
	s_nop 0
	s_add_i32 m0, s36, 0x1e000
	s_nop 0
	global_load_lds_dwordx4 v178, s[24:25]
	s_nop 0
	s_add_i32 m0, s36, 0x8000
	s_nop 0
	global_load_lds_dwordx4 v175, s[22:23]
	s_nop 0
	s_add_i32 m0, s36, 0xa000
	s_nop 0
	global_load_lds_dwordx4 v177, s[22:23]
	s_waitcnt vmcnt(8)
	s_waitcnt lgkmcnt(0)
	s_barrier
	s_setprio 1
	v_mfma_f32_16x16x32_bf16 v[60:63], v[112:115], v[164:167], v[60:63]
	v_mfma_f32_16x16x32_bf16 v[56:59], v[136:139], v[164:167], v[56:59]
	v_mfma_f32_16x16x32_bf16 v[44:47], v[112:115], v[188:191], v[44:47]
	v_mfma_f32_16x16x32_bf16 v[40:43], v[136:139], v[188:191], v[40:43]
	v_mfma_f32_16x16x32_bf16 v[28:31], v[112:115], v[196:199], v[28:31]
	v_mfma_f32_16x16x32_bf16 v[24:27], v[136:139], v[196:199], v[24:27]
	v_mfma_f32_16x16x32_bf16 v[12:15], v[112:115], v[204:207], v[12:15]
	v_mfma_f32_16x16x32_bf16 v[8:11], v[136:139], v[204:207], v[8:11]
	v_mfma_f32_16x16x32_bf16 v[60:63], v[116:119], v[168:171], v[60:63]
	v_mfma_f32_16x16x32_bf16 v[56:59], v[140:143], v[168:171], v[56:59]
	v_mfma_f32_16x16x32_bf16 v[44:47], v[116:119], v[192:195], v[44:47]
	v_mfma_f32_16x16x32_bf16 v[40:43], v[140:143], v[192:195], v[40:43]
	v_mfma_f32_16x16x32_bf16 v[28:31], v[116:119], v[200:203], v[28:31]
	v_mfma_f32_16x16x32_bf16 v[24:27], v[140:143], v[200:203], v[24:27]
	v_mfma_f32_16x16x32_bf16 v[12:15], v[116:119], v[208:211], v[12:15]
	v_mfma_f32_16x16x32_bf16 v[8:11], v[140:143], v[208:211], v[8:11]
	v_mfma_f32_16x16x32_bf16 v[52:55], v[144:147], v[164:167], v[52:55]
	v_mfma_f32_16x16x32_bf16 v[48:51], v[156:159], v[164:167], v[48:51]
	v_mfma_f32_16x16x32_bf16 v[36:39], v[144:147], v[188:191], v[36:39]
	v_mfma_f32_16x16x32_bf16 v[32:35], v[156:159], v[188:191], v[32:35]
	v_mfma_f32_16x16x32_bf16 v[20:23], v[144:147], v[196:199], v[20:23]
	v_mfma_f32_16x16x32_bf16 v[16:19], v[156:159], v[196:199], v[16:19]
	v_mfma_f32_16x16x32_bf16 v[4:7], v[144:147], v[204:207], v[4:7]
	v_mfma_f32_16x16x32_bf16 v[0:3], v[156:159], v[204:207], v[0:3]
	v_mfma_f32_16x16x32_bf16 v[52:55], v[148:151], v[168:171], v[52:55]
	v_mfma_f32_16x16x32_bf16 v[48:51], v[160:163], v[168:171], v[48:51]
	v_mfma_f32_16x16x32_bf16 v[36:39], v[148:151], v[192:195], v[36:39]
	v_mfma_f32_16x16x32_bf16 v[32:35], v[160:163], v[192:195], v[32:35]
	v_mfma_f32_16x16x32_bf16 v[20:23], v[148:151], v[200:203], v[20:23]
	v_mfma_f32_16x16x32_bf16 v[16:19], v[160:163], v[200:203], v[16:19]
	v_mfma_f32_16x16x32_bf16 v[4:7], v[148:151], v[208:211], v[4:7]
	v_mfma_f32_16x16x32_bf16 v[0:3], v[160:163], v[208:211], v[0:3]
	s_setprio 0
	s_barrier
	s_add_i32 s55, s55, 2
	s_add_u32 s51, s51, 0x100
	s_addc_u32 s52, s52, 0
	s_add_u32 s53, s53, 0x100
	s_addc_u32 s54, s54, 0
	s_add_u32 s6, s6, 0x100
	s_addc_u32 s7, s7, 0
	s_cmpk_gt_u32 s55, 0x55
	s_cbranch_scc0 .LBB0_838
	s_and_b64 vcc, exec, s[16:17]
	s_cbranch_vccz .LBB0_841
	s_barrier

.LBB0_930:
	s_ashr_i32 s37, s36, 31
	s_lshl_b64 s[38:39], s[36:37], 19
	s_add_u32 s38, s19, s38
	s_addc_u32 s39, s21, s39
	s_and_b64 s[40:41], s[4:5], exec
	s_cselect_b32 s9, s39, s45
	s_cselect_b32 s76, s38, s44
	s_ashr_i32 s35, s34, 31
	s_lshl_b64 s[40:41], s[34:35], 19
	s_add_u32 s40, s23, s40
	s_addc_u32 s41, s25, s41
	s_and_b64 s[46:47], s[4:5], exec
	ds_read_b128 v[0:3], v226 offset:3072
	ds_read_b128 v[4:7], v226 offset:2048
	ds_read_b128 v[8:11], v226 offset:1024
	ds_read_b128 v[12:15], v226
	ds_read_b128 v[16:19], v227 offset:3072
	ds_read_b128 v[20:23], v227 offset:2048
	ds_read_b128 v[24:27], v227 offset:1024
	ds_read_b128 v[28:31], v227
	s_cselect_b32 s35, s41, s43
	s_cselect_b32 s77, s40, s42
	s_lshl_b32 s46, s78, 11
	s_and_b32 s46, s46, 0x800
	s_or_b32 s54, s46, s56
	s_lshl_b64 s[48:49], s[36:37], 11
	s_add_u32 s46, s44, 0x100
	s_addc_u32 s47, s45, 0
	s_add_u32 s80, s42, 0x100
	s_addc_u32 s81, s43, 0
	s_add_u32 s50, s44, 0x180
	s_addc_u32 s51, s45, 0
	s_add_u32 s52, s42, 0x180
	s_addc_u32 s53, s43, 0
	ds_read_b128 v[32:35], v228
	ds_read_b128 v[36:39], v228 offset:1024
	ds_read_b128 v[40:43], v228 offset:2048
	ds_read_b128 v[44:47], v228 offset:3072
	ds_read_b128 v[48:51], v228 offset:4096
	ds_read_b128 v[52:55], v228 offset:5120
	ds_read_b128 v[56:59], v228 offset:6144
	ds_read_b128 v[60:63], v228 offset:7168
	s_add_u32 s82, s44, 0x40080
	s_addc_u32 s83, s45, 0
	s_add_i32 m0, s31, 0xc000
	s_nop 0
	global_load_lds_dwordx4 v219, s[82:83]
	s_nop 0
	s_add_i32 m0, s31, 0xe000
	s_nop 0
	global_load_lds_dwordx4 v221, s[82:83]
	s_waitcnt vmcnt(8)
	s_waitcnt lgkmcnt(0)
	s_barrier
	s_setprio 1
	s_waitcnt lgkmcnt(7)
	v_mfma_i32_16x16x64_i8 v[64:67], v[28:31], v[32:35], 0
	s_mov_b32 s37, 0
	v_mfma_i32_16x16x64_i8 v[68:71], v[20:23], v[32:35], 0
	s_waitcnt lgkmcnt(5)
	v_mfma_i32_16x16x64_i8 v[72:75], v[28:31], v[40:43], 0
	v_mfma_i32_16x16x64_i8 v[76:79], v[20:23], v[40:43], 0
	s_waitcnt lgkmcnt(3)
	v_mfma_i32_16x16x64_i8 v[80:83], v[28:31], v[48:51], 0
	v_mfma_i32_16x16x64_i8 v[84:87], v[20:23], v[48:51], 0
	s_waitcnt lgkmcnt(1)
	v_mfma_i32_16x16x64_i8 v[92:95], v[20:23], v[56:59], 0
	v_mfma_i32_16x16x64_i8 v[136:139], v[24:27], v[36:39], v[64:67]
	v_mfma_i32_16x16x64_i8 v[144:147], v[16:19], v[36:39], v[68:71]
	v_mfma_i32_16x16x64_i8 v[148:151], v[24:27], v[44:47], v[72:75]
	v_mfma_i32_16x16x64_i8 v[76:79], v[16:19], v[44:47], v[76:79]
	v_mfma_i32_16x16x64_i8 v[80:83], v[24:27], v[52:55], v[80:83]
	v_mfma_i32_16x16x64_i8 v[84:87], v[16:19], v[52:55], v[84:87]
	v_mfma_i32_16x16x64_i8 v[88:91], v[28:31], v[56:59], 0
	s_waitcnt lgkmcnt(0)
	v_mfma_i32_16x16x64_i8 v[92:95], v[16:19], v[60:63], v[92:95]
	v_mfma_i32_16x16x64_i8 v[88:91], v[24:27], v[60:63], v[88:91]
	s_setprio 0
	s_setprio 1
	v_mfma_i32_16x16x64_i8 v[96:99], v[12:15], v[32:35], 0
	v_mfma_i32_16x16x64_i8 v[32:35], v[4:7], v[32:35], 0
	v_mfma_i32_16x16x64_i8 v[96:99], v[8:11], v[36:39], v[96:99]
	v_mfma_i32_16x16x64_i8 v[32:35], v[0:3], v[36:39], v[32:35]
	v_mfma_i32_16x16x64_i8 v[36:39], v[12:15], v[40:43], 0
	v_mfma_i32_16x16x64_i8 v[40:43], v[4:7], v[40:43], 0
	v_mfma_i32_16x16x64_i8 v[36:39], v[8:11], v[44:47], v[36:39]
	v_mfma_i32_16x16x64_i8 v[40:43], v[0:3], v[44:47], v[40:43]
	v_mfma_i32_16x16x64_i8 v[44:47], v[12:15], v[48:51], 0
	v_mfma_i32_16x16x64_i8 v[48:51], v[4:7], v[48:51], 0
	v_mfma_i32_16x16x64_i8 v[44:47], v[8:11], v[52:55], v[44:47]
	v_mfma_i32_16x16x64_i8 v[48:51], v[0:3], v[52:55], v[48:51]
	v_mfma_i32_16x16x64_i8 v[52:55], v[12:15], v[56:59], 0
	v_mfma_i32_16x16x64_i8 v[56:59], v[4:7], v[56:59], 0
	v_mfma_i32_16x16x64_i8 v[52:55], v[8:11], v[60:63], v[52:55]
	v_mfma_i32_16x16x64_i8 v[56:59], v[0:3], v[60:63], v[56:59]
	s_setprio 0
	s_barrier
	ds_read_b128 v[60:63], v228 offset:16384
	ds_read_b128 v[100:103], v228 offset:17408
	ds_read_b128 v[104:107], v228 offset:18432
	ds_read_b128 v[108:111], v228 offset:19456
	ds_read_b128 v[112:115], v228 offset:20480
	ds_read_b128 v[116:119], v228 offset:21504
	ds_read_b128 v[120:123], v228 offset:22528
	ds_read_b128 v[124:127], v228 offset:23552
	s_add_i32 m0, s31, 0x10000
	s_nop 0
	global_load_lds_dwordx4 v220, s[80:81]
	s_nop 0
	s_add_i32 m0, s31, 0x12000
	s_nop 0
	global_load_lds_dwordx4 v222, s[80:81]
	s_add_u32 s80, s42, 0x40100
	s_addc_u32 s81, s43, 0
	s_add_i32 m0, s31, 0x14000
	s_nop 0
	global_load_lds_dwordx4 v220, s[80:81]
	s_nop 0
	s_add_i32 m0, s31, 0x16000
	s_nop 0
	global_load_lds_dwordx4 v222, s[80:81]
	s_nop 0
	s_add_i32 m0, s31, 0
	s_nop 0
	global_load_lds_dwordx4 v219, s[46:47]
	s_nop 0
	s_add_i32 m0, s31, 0x2000
	s_nop 0
	global_load_lds_dwordx4 v221, s[46:47]
	s_waitcnt vmcnt(8)
	s_waitcnt lgkmcnt(0)
	s_barrier
	s_setprio 1
	v_mfma_i32_16x16x64_i8 v[132:135], v[20:23], v[60:63], 0
	v_mfma_i32_16x16x64_i8 v[168:171], v[16:19], v[100:103], v[132:135]
	v_mfma_i32_16x16x64_i8 v[132:135], v[28:31], v[104:107], 0
	v_mfma_i32_16x16x64_i8 v[204:207], v[24:27], v[108:111], v[132:135]
	v_mfma_i32_16x16x64_i8 v[132:135], v[20:23], v[104:107], 0
	v_mfma_i32_16x16x64_i8 v[128:131], v[28:31], v[60:63], 0
	v_mfma_i32_16x16x64_i8 v[214:217], v[16:19], v[108:111], v[132:135]
	v_mfma_i32_16x16x64_i8 v[132:135], v[28:31], v[112:115], 0
	v_mfma_i32_16x16x64_i8 v[128:131], v[24:27], v[100:103], v[128:131]
	v_mfma_i32_16x16x64_i8 v[232:235], v[24:27], v[116:119], v[132:135]
	v_mfma_i32_16x16x64_i8 v[132:135], v[20:23], v[112:115], 0
	v_mfma_i32_16x16x64_i8 v[28:31], v[28:31], v[120:123], 0
	v_mfma_i32_16x16x64_i8 v[20:23], v[20:23], v[120:123], 0
	v_mfma_i32_16x16x64_i8 v[236:239], v[16:19], v[116:119], v[132:135]
	v_mfma_i32_16x16x64_i8 v[24:27], v[24:27], v[124:127], v[28:31]
	v_mfma_i32_16x16x64_i8 v[16:19], v[16:19], v[124:127], v[20:23]
	v_mfma_i32_16x16x64_i8 v[20:23], v[12:15], v[60:63], 0
	v_mfma_i32_16x16x64_i8 v[28:31], v[4:7], v[60:63], 0
	v_mfma_i32_16x16x64_i8 v[20:23], v[8:11], v[100:103], v[20:23]
	v_mfma_i32_16x16x64_i8 v[28:31], v[0:3], v[100:103], v[28:31]
	v_mfma_i32_16x16x64_i8 v[60:63], v[12:15], v[104:107], 0
	v_mfma_i32_16x16x64_i8 v[100:103], v[4:7], v[104:107], 0
	v_mfma_i32_16x16x64_i8 v[104:107], v[12:15], v[112:115], 0
	v_mfma_i32_16x16x64_i8 v[100:103], v[0:3], v[108:111], v[100:103]
	v_mfma_i32_16x16x64_i8 v[240:243], v[8:11], v[116:119], v[104:107]
	v_mfma_i32_16x16x64_i8 v[104:107], v[4:7], v[112:115], 0
	v_mfma_i32_16x16x64_i8 v[12:15], v[12:15], v[120:123], 0
	v_mfma_i32_16x16x64_i8 v[4:7], v[4:7], v[120:123], 0
	v_mfma_i32_16x16x64_i8 v[60:63], v[8:11], v[108:111], v[60:63]
	v_mfma_i32_16x16x64_i8 v[244:247], v[0:3], v[116:119], v[104:107]
	v_mfma_i32_16x16x64_i8 v[8:11], v[8:11], v[124:127], v[12:15]
	v_mfma_i32_16x16x64_i8 v[0:3], v[0:3], v[124:127], v[4:7]
	s_setprio 0
	s_barrier
	s_nop 1
	ds_read_b128 v[4:7], v229
	ds_read_b128 v[12:15], v229 offset:1024
	ds_read_b128 v[104:107], v229 offset:2048
	ds_read_b128 v[116:119], v229 offset:3072
	ds_read_b128 v[124:127], v230
	ds_read_b128 v[248:251], v230 offset:1024
	ds_read_b128 v[208:211], v230 offset:2048
	ds_read_b128 v[64:67], v230 offset:3072
	ds_read_b128 v[108:111], v228 offset:32768
	ds_read_b128 v[112:115], v228 offset:33792
	ds_read_b128 v[120:123], v228 offset:34816
	ds_read_b128 v[132:135], v228 offset:35840
	ds_read_b128 v[140:143], v228 offset:36864
	ds_read_b128 v[152:155], v228 offset:37888
	ds_read_b128 v[68:71], v228 offset:38912
	ds_read_b128 v[72:75], v228 offset:39936
	s_add_u32 s44, s44, 0x40100
	s_addc_u32 s45, s45, 0
	s_add_i32 m0, s31, 0x4000
	s_nop 0
	global_load_lds_dwordx4 v219, s[44:45]
	s_nop 0
	s_add_i32 m0, s31, 0x6000
	s_nop 0
	global_load_lds_dwordx4 v221, s[44:45]
	s_waitcnt vmcnt(8)
	s_waitcnt lgkmcnt(0)
	s_barrier
	s_setprio 1
	v_mfma_i32_16x16x64_i8 v[76:79], v[104:107], v[120:123], v[76:79]
	v_mfma_i32_16x16x64_i8 v[180:183], v[116:119], v[132:135], v[76:79]
	v_mfma_i32_16x16x64_i8 v[76:79], v[4:7], v[140:143], v[80:83]
	v_mfma_i32_16x16x64_i8 v[136:139], v[4:7], v[108:111], v[136:139]
	v_mfma_i32_16x16x64_i8 v[164:167], v[12:15], v[152:155], v[76:79]
	v_mfma_i32_16x16x64_i8 v[76:79], v[104:107], v[140:143], v[84:87]
	v_mfma_i32_16x16x64_i8 v[200:203], v[12:15], v[112:115], v[136:139]
	v_mfma_i32_16x16x64_i8 v[136:139], v[104:107], v[108:111], v[144:147]
	v_mfma_i32_16x16x64_i8 v[160:163], v[116:119], v[152:155], v[76:79]
	v_mfma_i32_16x16x64_i8 v[76:79], v[4:7], v[68:71], v[88:91]
	v_mfma_i32_16x16x64_i8 v[196:199], v[116:119], v[112:115], v[136:139]
	v_mfma_i32_16x16x64_i8 v[136:139], v[4:7], v[120:123], v[148:151]
	v_mfma_i32_16x16x64_i8 v[148:151], v[12:15], v[72:75], v[76:79]
	v_mfma_i32_16x16x64_i8 v[76:79], v[104:107], v[68:71], v[92:95]
	v_mfma_i32_16x16x64_i8 v[184:187], v[12:15], v[132:135], v[136:139]
	v_mfma_i32_16x16x64_i8 v[144:147], v[116:119], v[72:75], v[76:79]
	v_mfma_i32_16x16x64_i8 v[32:35], v[208:211], v[108:111], v[32:35]
	v_mfma_i32_16x16x64_i8 v[188:191], v[64:67], v[112:115], v[32:35]
	v_mfma_i32_16x16x64_i8 v[32:35], v[124:127], v[120:123], v[36:39]
	v_mfma_i32_16x16x64_i8 v[176:179], v[248:251], v[132:135], v[32:35]
	v_mfma_i32_16x16x64_i8 v[32:35], v[208:211], v[120:123], v[40:43]
	v_mfma_i32_16x16x64_i8 v[172:175], v[64:67], v[132:135], v[32:35]
	v_mfma_i32_16x16x64_i8 v[32:35], v[124:127], v[140:143], v[44:47]
	v_mfma_i32_16x16x64_i8 v[156:159], v[248:251], v[152:155], v[32:35]
	v_mfma_i32_16x16x64_i8 v[32:35], v[208:211], v[140:143], v[48:51]
	v_mfma_i32_16x16x64_i8 v[152:155], v[64:67], v[152:155], v[32:35]
	v_mfma_i32_16x16x64_i8 v[32:35], v[124:127], v[68:71], v[52:55]
	v_mfma_i32_16x16x64_i8 v[76:79], v[124:127], v[108:111], v[96:99]
	v_mfma_i32_16x16x64_i8 v[140:143], v[248:251], v[72:75], v[32:35]
	v_mfma_i32_16x16x64_i8 v[32:35], v[208:211], v[68:71], v[56:59]
	v_mfma_i32_16x16x64_i8 v[192:195], v[248:251], v[112:115], v[76:79]
	v_mfma_i32_16x16x64_i8 v[136:139], v[64:67], v[72:75], v[32:35]
	s_setprio 0
	s_barrier
	s_nop 3
	ds_read_b128 v[32:35], v228 offset:49152
	ds_read_b128 v[36:39], v228 offset:50176
	ds_read_b128 v[40:43], v228 offset:51200
	ds_read_b128 v[44:47], v228 offset:52224
	ds_read_b128 v[48:51], v228 offset:53248
	ds_read_b128 v[52:55], v228 offset:54272
	ds_read_b128 v[56:59], v228 offset:55296
	ds_read_b128 v[88:91], v228 offset:56320
	s_add_i32 m0, s31, 0x18000
	s_nop 0
	global_load_lds_dwordx4 v220, s[52:53]
	s_nop 0
	s_add_i32 m0, s31, 0x1a000
	s_nop 0
	global_load_lds_dwordx4 v222, s[52:53]
	s_add_u32 s44, s42, 0x40180
	s_addc_u32 s45, s43, 0
	s_add_i32 m0, s31, 0x1c000
	s_nop 0
	global_load_lds_dwordx4 v220, s[44:45]
	s_nop 0
	s_add_i32 m0, s31, 0x1e000
	s_nop 0
	global_load_lds_dwordx4 v222, s[44:45]
	s_nop 0
	s_add_i32 m0, s31, 0x8000
	s_nop 0
	global_load_lds_dwordx4 v219, s[50:51]
	s_nop 0
	s_add_i32 m0, s31, 0xa000
	s_nop 0
	global_load_lds_dwordx4 v221, s[50:51]
	s_waitcnt vmcnt(8)
	s_waitcnt lgkmcnt(0)
	s_barrier
	s_setprio 1
	v_mfma_i32_16x16x64_i8 v[68:71], v[4:7], v[32:35], v[128:131]
	v_mfma_i32_16x16x64_i8 v[132:135], v[12:15], v[36:39], v[68:71]
	v_mfma_i32_16x16x64_i8 v[68:71], v[104:107], v[32:35], v[168:171]
	v_mfma_i32_16x16x64_i8 v[128:131], v[116:119], v[36:39], v[68:71]
	v_mfma_i32_16x16x64_i8 v[68:71], v[4:7], v[40:43], v[204:207]
	v_mfma_i32_16x16x64_i8 v[112:115], v[12:15], v[44:47], v[68:71]
	v_mfma_i32_16x16x64_i8 v[68:71], v[104:107], v[40:43], v[214:217]
	v_mfma_i32_16x16x64_i8 v[108:111], v[116:119], v[44:47], v[68:71]
	v_mfma_i32_16x16x64_i8 v[68:71], v[4:7], v[48:51], v[232:235]
	v_mfma_i32_16x16x64_i8 v[4:7], v[4:7], v[56:59], v[24:27]
	v_mfma_i32_16x16x64_i8 v[96:99], v[12:15], v[52:55], v[68:71]
	v_mfma_i32_16x16x64_i8 v[68:71], v[104:107], v[48:51], v[236:239]
	v_mfma_i32_16x16x64_i8 v[76:79], v[12:15], v[88:91], v[4:7]
	v_mfma_i32_16x16x64_i8 v[4:7], v[104:107], v[56:59], v[16:19]
	v_mfma_i32_16x16x64_i8 v[92:95], v[116:119], v[52:55], v[68:71]
	v_mfma_i32_16x16x64_i8 v[72:75], v[116:119], v[88:91], v[4:7]
	v_mfma_i32_16x16x64_i8 v[4:7], v[124:127], v[32:35], v[20:23]
	v_mfma_i32_16x16x64_i8 v[120:123], v[248:251], v[36:39], v[4:7]
	v_mfma_i32_16x16x64_i8 v[4:7], v[208:211], v[32:35], v[28:31]
	v_mfma_i32_16x16x64_i8 v[116:119], v[64:67], v[36:39], v[4:7]
	v_mfma_i32_16x16x64_i8 v[4:7], v[124:127], v[40:43], v[60:63]
	v_mfma_i32_16x16x64_i8 v[104:107], v[248:251], v[44:47], v[4:7]
	v_mfma_i32_16x16x64_i8 v[4:7], v[208:211], v[40:43], v[100:103]
	v_mfma_i32_16x16x64_i8 v[100:103], v[64:67], v[44:47], v[4:7]
	v_mfma_i32_16x16x64_i8 v[4:7], v[124:127], v[48:51], v[240:243]
	v_mfma_i32_16x16x64_i8 v[84:87], v[248:251], v[52:55], v[4:7]
	v_mfma_i32_16x16x64_i8 v[4:7], v[208:211], v[48:51], v[244:247]
	v_mfma_i32_16x16x64_i8 v[80:83], v[64:67], v[52:55], v[4:7]
	v_mfma_i32_16x16x64_i8 v[4:7], v[124:127], v[56:59], v[8:11]
	v_mfma_i32_16x16x64_i8 v[0:3], v[208:211], v[56:59], v[0:3]
	v_mfma_i32_16x16x64_i8 v[68:71], v[248:251], v[88:91], v[4:7]
	v_mfma_i32_16x16x64_i8 v[64:67], v[64:67], v[88:91], v[0:3]
	s_setprio 0
	s_barrier
	s_add_u32 s44, s27, s48
	s_addc_u32 s45, s29, s49
	s_add_u32 s79, s42, 0x200
	s_addc_u32 s80, s43, 0
	s_add_i32 s81, s54, 0
	s_add_i32 s81, s81, 0x20000

.LBB0_933:
	ds_read_b128 v[0:3], v227
	ds_read_b128 v[4:7], v227 offset:1024
	ds_read_b128 v[8:11], v227 offset:2048
	ds_read_b128 v[12:15], v227 offset:3072
	ds_read_b128 v[16:19], v226
	ds_read_b128 v[20:23], v226 offset:1024
	ds_read_b128 v[24:27], v226 offset:2048
	ds_read_b128 v[28:31], v226 offset:3072
	s_add_u32 s42, s46, 0x100
	s_addc_u32 s43, s47, 0
	s_and_b64 s[48:49], s[48:49], exec
	s_cselect_b32 s54, s76, s42
	s_cselect_b32 s55, s9, s43
	s_cselect_b32 s51, s35, s80
	s_cselect_b32 s50, s77, s79
	s_add_u32 s48, s54, 0x80
	s_addc_u32 s49, s55, 0
	s_add_u32 s52, s50, 0x80
	s_addc_u32 s53, s51, 0
	ds_read_b128 v[32:35], v228
	ds_read_b128 v[36:39], v228 offset:1024
	ds_read_b128 v[40:43], v228 offset:2048
	ds_read_b128 v[44:47], v228 offset:3072
	ds_read_b128 v[48:51], v228 offset:4096
	ds_read_b128 v[52:55], v228 offset:5120
	ds_read_b128 v[56:59], v228 offset:6144
	ds_read_b128 v[60:63], v228 offset:7168
	s_add_u32 s46, s46, 0x40080
	s_addc_u32 s47, s47, 0
	s_add_i32 m0, s31, 0xc000
	s_nop 0
	global_load_lds_dwordx4 v219, s[46:47]
	s_nop 0
	s_add_i32 m0, s31, 0xe000
	s_nop 0
	global_load_lds_dwordx4 v221, s[46:47]
	s_waitcnt vmcnt(8)
	s_waitcnt lgkmcnt(0)
	s_barrier
	s_setprio 1
	v_mfma_i32_16x16x64_i8 v[180:183], v[8:11], v[40:43], v[180:183]
	v_mfma_i32_16x16x64_i8 v[164:167], v[0:3], v[48:51], v[164:167]
	v_mfma_i32_16x16x64_i8 v[160:163], v[8:11], v[48:51], v[160:163]
	v_mfma_i32_16x16x64_i8 v[148:151], v[0:3], v[56:59], v[148:151]
	v_mfma_i32_16x16x64_i8 v[144:147], v[8:11], v[56:59], v[144:147]
	v_mfma_i32_16x16x64_i8 v[88:91], v[0:3], v[32:35], v[200:203]
	v_mfma_i32_16x16x64_i8 v[124:127], v[8:11], v[32:35], v[196:199]
	v_mfma_i32_16x16x64_i8 v[168:171], v[0:3], v[40:43], v[184:187]
	v_mfma_i32_16x16x64_i8 v[180:183], v[12:15], v[44:47], v[180:183]
	v_mfma_i32_16x16x64_i8 v[164:167], v[4:7], v[52:55], v[164:167]
	v_mfma_i32_16x16x64_i8 v[160:163], v[12:15], v[52:55], v[160:163]
	v_mfma_i32_16x16x64_i8 v[148:151], v[4:7], v[60:63], v[148:151]
	v_mfma_i32_16x16x64_i8 v[144:147], v[12:15], v[60:63], v[144:147]
	v_mfma_i32_16x16x64_i8 v[88:91], v[4:7], v[36:39], v[88:91]
	v_mfma_i32_16x16x64_i8 v[124:127], v[12:15], v[36:39], v[124:127]
	v_mfma_i32_16x16x64_i8 v[168:171], v[4:7], v[44:47], v[168:171]
	v_mfma_i32_16x16x64_i8 v[184:187], v[16:19], v[32:35], v[192:195]
	v_mfma_i32_16x16x64_i8 v[32:35], v[24:27], v[32:35], v[188:191]
	v_mfma_i32_16x16x64_i8 v[192:195], v[20:23], v[36:39], v[184:187]
	v_mfma_i32_16x16x64_i8 v[32:35], v[28:31], v[36:39], v[32:35]
	v_mfma_i32_16x16x64_i8 v[36:39], v[16:19], v[40:43], v[176:179]
	v_mfma_i32_16x16x64_i8 v[40:43], v[24:27], v[40:43], v[172:175]
	v_mfma_i32_16x16x64_i8 v[36:39], v[20:23], v[44:47], v[36:39]
	v_mfma_i32_16x16x64_i8 v[40:43], v[28:31], v[44:47], v[40:43]
	v_mfma_i32_16x16x64_i8 v[44:47], v[16:19], v[48:51], v[156:159]
	v_mfma_i32_16x16x64_i8 v[48:51], v[24:27], v[48:51], v[152:155]
	v_mfma_i32_16x16x64_i8 v[44:47], v[20:23], v[52:55], v[44:47]
	v_mfma_i32_16x16x64_i8 v[48:51], v[28:31], v[52:55], v[48:51]
	v_mfma_i32_16x16x64_i8 v[52:55], v[16:19], v[56:59], v[140:143]
	v_mfma_i32_16x16x64_i8 v[56:59], v[24:27], v[56:59], v[136:139]
	v_mfma_i32_16x16x64_i8 v[52:55], v[20:23], v[60:63], v[52:55]
	v_mfma_i32_16x16x64_i8 v[56:59], v[28:31], v[60:63], v[56:59]
	s_setprio 0
	s_barrier
	ds_read_b128 v[60:63], v228 offset:16384
	ds_read_b128 v[136:139], v228 offset:17408
	ds_read_b128 v[140:143], v228 offset:18432
	ds_read_b128 v[152:155], v228 offset:19456
	ds_read_b128 v[156:159], v228 offset:20480
	ds_read_b128 v[172:175], v228 offset:21504
	ds_read_b128 v[176:179], v228 offset:22528
	ds_read_b128 v[184:187], v228 offset:23552
	s_add_i32 m0, s31, 0x10000
	s_nop 0
	global_load_lds_dwordx4 v220, s[50:51]
	s_nop 0
	s_add_i32 m0, s31, 0x12000
	s_nop 0
	global_load_lds_dwordx4 v222, s[50:51]
	s_add_u32 s46, s50, 0x40000
	s_addc_u32 s47, s51, 0
	s_add_i32 m0, s31, 0x14000
	s_nop 0
	global_load_lds_dwordx4 v220, s[46:47]
	s_nop 0
	s_add_i32 m0, s31, 0x16000
	s_nop 0
	global_load_lds_dwordx4 v222, s[46:47]
	s_nop 0
	s_add_i32 m0, s31, 0
	s_nop 0
	global_load_lds_dwordx4 v219, s[54:55]
	s_nop 0
	s_add_i32 m0, s31, 0x2000
	s_nop 0
	global_load_lds_dwordx4 v221, s[54:55]
	s_waitcnt vmcnt(8)
	s_waitcnt lgkmcnt(0)
	s_barrier
	s_setprio 1
	v_mfma_i32_16x16x64_i8 v[132:135], v[0:3], v[60:63], v[132:135]
	v_mfma_i32_16x16x64_i8 v[112:115], v[0:3], v[140:143], v[112:115]
	v_mfma_i32_16x16x64_i8 v[96:99], v[0:3], v[156:159], v[96:99]
	v_mfma_i32_16x16x64_i8 v[0:3], v[0:3], v[176:179], v[76:79]
	v_mfma_i32_16x16x64_i8 v[128:131], v[8:11], v[60:63], v[128:131]
	v_mfma_i32_16x16x64_i8 v[108:111], v[8:11], v[140:143], v[108:111]
	v_mfma_i32_16x16x64_i8 v[92:95], v[8:11], v[156:159], v[92:95]
	v_mfma_i32_16x16x64_i8 v[76:79], v[4:7], v[184:187], v[0:3]
	v_mfma_i32_16x16x64_i8 v[0:3], v[8:11], v[176:179], v[72:75]
	v_mfma_i32_16x16x64_i8 v[132:135], v[4:7], v[136:139], v[132:135]
	v_mfma_i32_16x16x64_i8 v[128:131], v[12:15], v[136:139], v[128:131]
	v_mfma_i32_16x16x64_i8 v[112:115], v[4:7], v[152:155], v[112:115]
	v_mfma_i32_16x16x64_i8 v[108:111], v[12:15], v[152:155], v[108:111]
	v_mfma_i32_16x16x64_i8 v[96:99], v[4:7], v[172:175], v[96:99]
	v_mfma_i32_16x16x64_i8 v[92:95], v[12:15], v[172:175], v[92:95]
	v_mfma_i32_16x16x64_i8 v[72:75], v[12:15], v[184:187], v[0:3]
	v_mfma_i32_16x16x64_i8 v[0:3], v[16:19], v[60:63], v[120:123]
	v_mfma_i32_16x16x64_i8 v[120:123], v[20:23], v[136:139], v[0:3]
	v_mfma_i32_16x16x64_i8 v[0:3], v[24:27], v[60:63], v[116:119]
	v_mfma_i32_16x16x64_i8 v[116:119], v[28:31], v[136:139], v[0:3]
	v_mfma_i32_16x16x64_i8 v[0:3], v[16:19], v[140:143], v[104:107]
	v_mfma_i32_16x16x64_i8 v[104:107], v[20:23], v[152:155], v[0:3]
	v_mfma_i32_16x16x64_i8 v[0:3], v[24:27], v[140:143], v[100:103]
	v_mfma_i32_16x16x64_i8 v[100:103], v[28:31], v[152:155], v[0:3]
	v_mfma_i32_16x16x64_i8 v[0:3], v[16:19], v[156:159], v[84:87]
	v_mfma_i32_16x16x64_i8 v[84:87], v[20:23], v[172:175], v[0:3]
	v_mfma_i32_16x16x64_i8 v[0:3], v[24:27], v[156:159], v[80:83]
	v_mfma_i32_16x16x64_i8 v[80:83], v[28:31], v[172:175], v[0:3]
	v_mfma_i32_16x16x64_i8 v[0:3], v[16:19], v[176:179], v[68:71]
	v_mfma_i32_16x16x64_i8 v[68:71], v[20:23], v[184:187], v[0:3]
	v_mfma_i32_16x16x64_i8 v[0:3], v[24:27], v[176:179], v[64:67]
	v_mfma_i32_16x16x64_i8 v[64:67], v[28:31], v[184:187], v[0:3]
	s_setprio 0
	s_barrier
	ds_read_b128 v[16:19], v229
	ds_read_b128 v[8:11], v229 offset:1024
	ds_read_b128 v[4:7], v229 offset:2048
	s_nop 1
	ds_read_b128 v[0:3], v229 offset:3072
	ds_read_b128 v[28:31], v230
	ds_read_b128 v[24:27], v230 offset:1024
	ds_read_b128 v[20:23], v230 offset:2048
	ds_read_b128 v[12:15], v230 offset:3072
	ds_read_b128 v[60:63], v228 offset:32768
	ds_read_b128 v[136:139], v228 offset:33792
	ds_read_b128 v[140:143], v228 offset:34816
	ds_read_b128 v[152:155], v228 offset:35840
	ds_read_b128 v[204:207], v228 offset:36864
	ds_read_b128 v[208:211], v228 offset:37888
	ds_read_b128 v[214:217], v228 offset:38912
	ds_read_b128 v[232:235], v228 offset:39936
	s_add_u32 s46, s54, 0x40000
	s_addc_u32 s47, s55, 0
	s_add_i32 m0, s31, 0x4000
	s_nop 0
	global_load_lds_dwordx4 v219, s[46:47]
	s_nop 0
	s_add_i32 m0, s31, 0x6000
	s_nop 0
	global_load_lds_dwordx4 v221, s[46:47]
	s_waitcnt vmcnt(8)
	s_waitcnt lgkmcnt(0)
	s_barrier
	s_setprio 1
	v_mfma_i32_16x16x64_i8 v[88:91], v[16:19], v[60:63], v[88:91]
	v_mfma_i32_16x16x64_i8 v[200:203], v[8:11], v[136:139], v[88:91]
	v_mfma_i32_16x16x64_i8 v[88:91], v[4:7], v[60:63], v[124:127]
	v_mfma_i32_16x16x64_i8 v[196:199], v[0:3], v[136:139], v[88:91]
	v_mfma_i32_16x16x64_i8 v[88:91], v[16:19], v[140:143], v[168:171]
	v_mfma_i32_16x16x64_i8 v[184:187], v[8:11], v[152:155], v[88:91]
	v_mfma_i32_16x16x64_i8 v[88:91], v[4:7], v[140:143], v[180:183]
	v_mfma_i32_16x16x64_i8 v[180:183], v[0:3], v[152:155], v[88:91]
	v_mfma_i32_16x16x64_i8 v[88:91], v[16:19], v[204:207], v[164:167]
	v_mfma_i32_16x16x64_i8 v[164:167], v[8:11], v[208:211], v[88:91]
	v_mfma_i32_16x16x64_i8 v[88:91], v[4:7], v[204:207], v[160:163]
	v_mfma_i32_16x16x64_i8 v[160:163], v[0:3], v[208:211], v[88:91]
	v_mfma_i32_16x16x64_i8 v[88:91], v[16:19], v[214:217], v[148:151]
	v_mfma_i32_16x16x64_i8 v[148:151], v[8:11], v[232:235], v[88:91]
	v_mfma_i32_16x16x64_i8 v[88:91], v[4:7], v[214:217], v[144:147]
	v_mfma_i32_16x16x64_i8 v[144:147], v[0:3], v[232:235], v[88:91]
	v_mfma_i32_16x16x64_i8 v[32:35], v[20:23], v[60:63], v[32:35]
	v_mfma_i32_16x16x64_i8 v[188:191], v[12:15], v[136:139], v[32:35]
	v_mfma_i32_16x16x64_i8 v[32:35], v[28:31], v[140:143], v[36:39]
	v_mfma_i32_16x16x64_i8 v[176:179], v[24:27], v[152:155], v[32:35]
	v_mfma_i32_16x16x64_i8 v[32:35], v[20:23], v[140:143], v[40:43]
	v_mfma_i32_16x16x64_i8 v[172:175], v[12:15], v[152:155], v[32:35]
	v_mfma_i32_16x16x64_i8 v[32:35], v[28:31], v[204:207], v[44:47]
	v_mfma_i32_16x16x64_i8 v[156:159], v[24:27], v[208:211], v[32:35]
	v_mfma_i32_16x16x64_i8 v[32:35], v[20:23], v[204:207], v[48:51]
	v_mfma_i32_16x16x64_i8 v[152:155], v[12:15], v[208:211], v[32:35]
	v_mfma_i32_16x16x64_i8 v[32:35], v[28:31], v[214:217], v[52:55]
	v_mfma_i32_16x16x64_i8 v[88:91], v[28:31], v[60:63], v[192:195]
	v_mfma_i32_16x16x64_i8 v[140:143], v[24:27], v[232:235], v[32:35]
	v_mfma_i32_16x16x64_i8 v[32:35], v[20:23], v[214:217], v[56:59]
	v_mfma_i32_16x16x64_i8 v[192:195], v[24:27], v[136:139], v[88:91]
	v_mfma_i32_16x16x64_i8 v[136:139], v[12:15], v[232:235], v[32:35]
	s_setprio 0
	s_barrier
	ds_read_b128 v[60:63], v228 offset:49152
	ds_read_b128 v[56:59], v228 offset:50176
	ds_read_b128 v[52:55], v228 offset:51200
	ds_read_b128 v[48:51], v228 offset:52224
	ds_read_b128 v[44:47], v228 offset:53248
	ds_read_b128 v[40:43], v228 offset:54272
	ds_read_b128 v[36:39], v228 offset:55296
	ds_read_b128 v[32:35], v228 offset:56320
	s_add_i32 m0, s31, 0x18000
	s_nop 0
	global_load_lds_dwordx4 v220, s[52:53]
	s_nop 0
	s_add_i32 m0, s31, 0x1a000
	s_nop 0
	global_load_lds_dwordx4 v222, s[52:53]
	s_add_u32 s46, s50, 0x40080
	s_addc_u32 s47, s51, 0
	s_add_i32 m0, s31, 0x1c000
	s_nop 0
	global_load_lds_dwordx4 v220, s[46:47]
	s_nop 0
	s_add_i32 m0, s31, 0x1e000
	s_nop 0
	global_load_lds_dwordx4 v222, s[46:47]
	s_nop 0
	s_add_i32 m0, s31, 0x8000
	s_nop 0
	global_load_lds_dwordx4 v219, s[48:49]
	s_nop 0
	s_add_i32 m0, s31, 0xa000
	s_nop 0
	global_load_lds_dwordx4 v221, s[48:49]
	s_waitcnt vmcnt(8)
	s_waitcnt lgkmcnt(0)
	s_barrier
	s_setprio 1
	v_mfma_i32_16x16x64_i8 v[88:91], v[16:19], v[60:63], v[132:135]
	v_mfma_i32_16x16x64_i8 v[132:135], v[8:11], v[56:59], v[88:91]
	v_mfma_i32_16x16x64_i8 v[88:91], v[4:7], v[60:63], v[128:131]
	v_mfma_i32_16x16x64_i8 v[128:131], v[0:3], v[56:59], v[88:91]
	v_mfma_i32_16x16x64_i8 v[88:91], v[16:19], v[52:55], v[112:115]
	v_mfma_i32_16x16x64_i8 v[112:115], v[8:11], v[48:51], v[88:91]
	v_mfma_i32_16x16x64_i8 v[88:91], v[4:7], v[52:55], v[108:111]
	v_mfma_i32_16x16x64_i8 v[108:111], v[0:3], v[48:51], v[88:91]
	v_mfma_i32_16x16x64_i8 v[88:91], v[16:19], v[44:47], v[96:99]
	v_mfma_i32_16x16x64_i8 v[96:99], v[8:11], v[40:43], v[88:91]
	v_mfma_i32_16x16x64_i8 v[88:91], v[4:7], v[44:47], v[92:95]
	v_mfma_i32_16x16x64_i8 v[76:79], v[16:19], v[36:39], v[76:79]
	v_mfma_i32_16x16x64_i8 v[72:75], v[4:7], v[36:39], v[72:75]
	v_mfma_i32_16x16x64_i8 v[92:95], v[0:3], v[40:43], v[88:91]
	v_mfma_i32_16x16x64_i8 v[76:79], v[8:11], v[32:35], v[76:79]
	v_mfma_i32_16x16x64_i8 v[72:75], v[0:3], v[32:35], v[72:75]
	v_mfma_i32_16x16x64_i8 v[88:91], v[28:31], v[60:63], v[120:123]
	v_mfma_i32_16x16x64_i8 v[120:123], v[24:27], v[56:59], v[88:91]
	v_mfma_i32_16x16x64_i8 v[88:91], v[20:23], v[60:63], v[116:119]
	v_mfma_i32_16x16x64_i8 v[116:119], v[12:15], v[56:59], v[88:91]
	v_mfma_i32_16x16x64_i8 v[88:91], v[28:31], v[52:55], v[104:107]
	v_mfma_i32_16x16x64_i8 v[104:107], v[24:27], v[48:51], v[88:91]
	v_mfma_i32_16x16x64_i8 v[88:91], v[20:23], v[52:55], v[100:103]
	v_mfma_i32_16x16x64_i8 v[84:87], v[28:31], v[44:47], v[84:87]
	v_mfma_i32_16x16x64_i8 v[80:83], v[20:23], v[44:47], v[80:83]
	v_mfma_i32_16x16x64_i8 v[68:71], v[28:31], v[36:39], v[68:71]
	v_mfma_i32_16x16x64_i8 v[64:67], v[20:23], v[36:39], v[64:67]
	v_mfma_i32_16x16x64_i8 v[100:103], v[12:15], v[48:51], v[88:91]
	v_mfma_i32_16x16x64_i8 v[84:87], v[24:27], v[40:43], v[84:87]
	v_mfma_i32_16x16x64_i8 v[80:83], v[12:15], v[40:43], v[80:83]
	v_mfma_i32_16x16x64_i8 v[68:71], v[24:27], v[32:35], v[68:71]
	v_mfma_i32_16x16x64_i8 v[64:67], v[12:15], v[32:35], v[64:67]
	s_setprio 0
	s_barrier
	s_add_i32 s37, s37, 2
	s_add_u32 s79, s79, 0x100
	s_addc_u32 s80, s80, 0
	s_cmp_gt_u32 s37, 13
	s_cbranch_scc1 .LBB0_935
	s_mov_b64 s[46:47], s[42:43]
	s_branch .LBB0_931

.LBB0_1108:
	s_ashr_i32 s23, s22, 31
	s_lshl_b64 s[24:25], s[22:23], 20
	s_add_u32 s24, s42, s24
	s_addc_u32 s25, s43, s25
	s_and_b64 s[26:27], s[4:5], exec
	ds_read_b128 v[0:3], v143
	ds_read_b128 v[4:7], v143 offset:1024
	ds_read_b128 v[8:11], v143 offset:2048
	s_waitcnt vmcnt(2)
	ds_read_b128 v[12:15], v143 offset:3072
	s_waitcnt vmcnt(1)
	ds_read_b128 v[16:19], v144
	s_waitcnt vmcnt(0)
	ds_read_b128 v[20:23], v144 offset:1024
	ds_read_b128 v[24:27], v144 offset:2048
	ds_read_b128 v[28:31], v144 offset:3072
	s_cselect_b32 s23, s25, s31
	s_cselect_b32 s51, s24, s30
	s_ashr_i32 s21, s20, 31
	s_lshl_b64 s[26:27], s[20:21], 20
	s_add_u32 s26, s44, s26
	s_addc_u32 s27, s45, s27
	s_and_b64 s[36:37], s[4:5], exec
	s_cselect_b32 s21, s27, s35
	s_cselect_b32 s52, s26, s34
	s_add_u32 s40, s30, 0x100
	s_addc_u32 s41, s31, 0
	s_add_u32 s54, s34, 0x100
	s_addc_u32 s55, s35, 0
	s_add_u32 s36, s30, 0x180
	s_addc_u32 s37, s31, 0
	ds_read_b128 v[32:35], v145
	ds_read_b128 v[36:39], v145 offset:1024
	ds_read_b128 v[40:43], v145 offset:2048
	ds_read_b128 v[44:47], v145 offset:3072
	ds_read_b128 v[48:51], v145 offset:4096
	ds_read_b128 v[52:55], v145 offset:5120
	ds_read_b128 v[56:59], v145 offset:6144
	ds_read_b128 v[60:63], v145 offset:7168
	s_add_u32 s38, s34, 0x180
	s_addc_u32 s39, s35, 0
	s_add_u32 s56, s30, 0x80080
	s_addc_u32 s57, s31, 0
	s_add_i32 m0, s2, 0xc000
	s_nop 0
	global_load_lds_dwordx4 v139, s[56:57]
	s_nop 0
	s_add_i32 m0, s2, 0xe000
	s_nop 0
	global_load_lds_dwordx4 v141, s[56:57]
	s_waitcnt vmcnt(8)
	s_waitcnt lgkmcnt(0)
	s_barrier
	s_setprio 1
	v_mfma_f32_16x16x32_bf16 v[64:67], v[0:3], v[32:35], 0
	v_mfma_f32_16x16x32_bf16 v[68:71], v[8:11], v[32:35], 0
	v_mfma_f32_16x16x32_bf16 v[72:75], v[0:3], v[40:43], 0
	v_mfma_f32_16x16x32_bf16 v[76:79], v[8:11], v[40:43], 0
	v_mfma_f32_16x16x32_bf16 v[80:83], v[0:3], v[48:51], 0
	v_mfma_f32_16x16x32_bf16 v[84:87], v[8:11], v[48:51], 0
	v_mfma_f32_16x16x32_bf16 v[88:91], v[0:3], v[56:59], 0
	v_mfma_f32_16x16x32_bf16 v[92:95], v[8:11], v[56:59], 0
	v_mfma_f32_16x16x32_bf16 v[64:67], v[4:7], v[36:39], v[64:67]
	v_mfma_f32_16x16x32_bf16 v[68:71], v[12:15], v[36:39], v[68:71]
	v_mfma_f32_16x16x32_bf16 v[72:75], v[4:7], v[44:47], v[72:75]
	v_mfma_f32_16x16x32_bf16 v[76:79], v[12:15], v[44:47], v[76:79]
	v_mfma_f32_16x16x32_bf16 v[80:83], v[4:7], v[52:55], v[80:83]
	v_mfma_f32_16x16x32_bf16 v[84:87], v[12:15], v[52:55], v[84:87]
	v_mfma_f32_16x16x32_bf16 v[88:91], v[4:7], v[60:63], v[88:91]
	v_mfma_f32_16x16x32_bf16 v[96:99], v[12:15], v[60:63], v[92:95]
	v_mfma_f32_16x16x32_bf16 v[92:95], v[16:19], v[32:35], 0
	v_mfma_f32_16x16x32_bf16 v[32:35], v[24:27], v[32:35], 0
	v_mfma_f32_16x16x32_bf16 v[104:107], v[20:23], v[36:39], v[92:95]
	v_mfma_f32_16x16x32_bf16 v[32:35], v[28:31], v[36:39], v[32:35]
	v_mfma_f32_16x16x32_bf16 v[36:39], v[16:19], v[40:43], 0
	v_mfma_f32_16x16x32_bf16 v[40:43], v[24:27], v[40:43], 0
	v_mfma_f32_16x16x32_bf16 v[36:39], v[20:23], v[44:47], v[36:39]
	v_mfma_f32_16x16x32_bf16 v[40:43], v[28:31], v[44:47], v[40:43]
	v_mfma_f32_16x16x32_bf16 v[44:47], v[16:19], v[48:51], 0
	v_mfma_f32_16x16x32_bf16 v[48:51], v[24:27], v[48:51], 0
	v_mfma_f32_16x16x32_bf16 v[44:47], v[20:23], v[52:55], v[44:47]
	v_mfma_f32_16x16x32_bf16 v[48:51], v[28:31], v[52:55], v[48:51]
	v_mfma_f32_16x16x32_bf16 v[52:55], v[16:19], v[56:59], 0
	v_mfma_f32_16x16x32_bf16 v[56:59], v[24:27], v[56:59], 0
	v_mfma_f32_16x16x32_bf16 v[52:55], v[20:23], v[60:63], v[52:55]
	v_mfma_f32_16x16x32_bf16 v[60:63], v[28:31], v[60:63], v[56:59]
	s_setprio 0
	s_barrier
	s_nop 3
	ds_read_b128 v[56:59], v145 offset:16384
	ds_read_b128 v[92:95], v145 offset:17408
	ds_read_b128 v[100:103], v145 offset:18432
	ds_read_b128 v[108:111], v145 offset:19456
	ds_read_b128 v[112:115], v145 offset:20480
	ds_read_b128 v[116:119], v145 offset:21504
	ds_read_b128 v[120:123], v145 offset:22528
	ds_read_b128 v[124:127], v145 offset:23552
	s_add_i32 m0, s2, 0x10000
	s_nop 0
	global_load_lds_dwordx4 v140, s[54:55]
	s_nop 0
	s_add_i32 m0, s2, 0x12000
	s_nop 0
	global_load_lds_dwordx4 v142, s[54:55]
	s_add_u32 s54, s34, 0x80100
	s_addc_u32 s55, s35, 0
	s_add_i32 m0, s2, 0x14000
	s_nop 0
	global_load_lds_dwordx4 v140, s[54:55]
	s_nop 0
	s_add_i32 m0, s2, 0x16000
	s_nop 0
	global_load_lds_dwordx4 v142, s[54:55]
	s_nop 0
	s_add_i32 m0, s2, 0
	s_nop 0
	global_load_lds_dwordx4 v139, s[40:41]
	s_nop 0
	s_add_i32 m0, s2, 0x2000
	s_nop 0
	global_load_lds_dwordx4 v141, s[40:41]
	s_waitcnt vmcnt(8)
	s_waitcnt lgkmcnt(0)
	s_barrier
	s_setprio 1
	v_mfma_f32_16x16x32_bf16 v[132:135], v[0:3], v[56:59], 0
	v_mfma_f32_16x16x32_bf16 v[152:155], v[0:3], v[100:103], 0
	v_mfma_f32_16x16x32_bf16 v[160:163], v[0:3], v[112:115], 0
	v_mfma_f32_16x16x32_bf16 v[0:3], v[0:3], v[120:123], 0
	v_mfma_f32_16x16x32_bf16 v[132:135], v[4:7], v[92:95], v[132:135]
	v_mfma_f32_16x16x32_bf16 v[152:155], v[4:7], v[108:111], v[152:155]
	v_mfma_f32_16x16x32_bf16 v[160:163], v[4:7], v[116:119], v[160:163]
	v_mfma_f32_16x16x32_bf16 v[0:3], v[4:7], v[124:127], v[0:3]
	v_mfma_f32_16x16x32_bf16 v[4:7], v[8:11], v[120:123], 0
	v_mfma_f32_16x16x32_bf16 v[148:151], v[8:11], v[56:59], 0
	v_mfma_f32_16x16x32_bf16 v[156:159], v[8:11], v[100:103], 0
	v_mfma_f32_16x16x32_bf16 v[164:167], v[8:11], v[112:115], 0
	v_mfma_f32_16x16x32_bf16 v[4:7], v[12:15], v[124:127], v[4:7]
	v_mfma_f32_16x16x32_bf16 v[148:151], v[12:15], v[92:95], v[148:151]
	v_mfma_f32_16x16x32_bf16 v[156:159], v[12:15], v[108:111], v[156:159]
	v_mfma_f32_16x16x32_bf16 v[164:167], v[12:15], v[116:119], v[164:167]
	v_mfma_f32_16x16x32_bf16 v[12:15], v[24:27], v[56:59], 0
	v_mfma_f32_16x16x32_bf16 v[168:171], v[28:31], v[92:95], v[12:15]
	v_mfma_f32_16x16x32_bf16 v[12:15], v[16:19], v[100:103], 0
	v_mfma_f32_16x16x32_bf16 v[172:175], v[20:23], v[108:111], v[12:15]
	v_mfma_f32_16x16x32_bf16 v[12:15], v[24:27], v[100:103], 0
	v_mfma_f32_16x16x32_bf16 v[176:179], v[28:31], v[108:111], v[12:15]
	v_mfma_f32_16x16x32_bf16 v[12:15], v[16:19], v[112:115], 0
	v_mfma_f32_16x16x32_bf16 v[180:183], v[20:23], v[116:119], v[12:15]
	v_mfma_f32_16x16x32_bf16 v[12:15], v[24:27], v[112:115], 0
	v_mfma_f32_16x16x32_bf16 v[8:11], v[16:19], v[56:59], 0
	v_mfma_f32_16x16x32_bf16 v[184:187], v[28:31], v[116:119], v[12:15]
	v_mfma_f32_16x16x32_bf16 v[12:15], v[16:19], v[120:123], 0
	v_mfma_f32_16x16x32_bf16 v[8:11], v[20:23], v[92:95], v[8:11]
	v_mfma_f32_16x16x32_bf16 v[188:191], v[20:23], v[124:127], v[12:15]
	v_mfma_f32_16x16x32_bf16 v[12:15], v[24:27], v[120:123], 0
	v_mfma_f32_16x16x32_bf16 v[192:195], v[28:31], v[124:127], v[12:15]
	s_setprio 0
	s_barrier
	s_nop 4
	ds_read_b128 v[12:15], v146
	ds_read_b128 v[16:19], v146 offset:1024
	ds_read_b128 v[24:27], v146 offset:2048
	ds_read_b128 v[196:199], v146 offset:3072
	ds_read_b128 v[200:203], v147
	ds_read_b128 v[204:207], v147 offset:1024
	ds_read_b128 v[208:211], v147 offset:2048
	ds_read_b128 v[212:215], v147 offset:3072
	ds_read_b128 v[20:23], v145 offset:32768
	ds_read_b128 v[28:31], v145 offset:33792
	ds_read_b128 v[216:219], v145 offset:34816
	ds_read_b128 v[220:223], v145 offset:35840
	ds_read_b128 v[224:227], v145 offset:36864
	ds_read_b128 v[228:231], v145 offset:37888
	ds_read_b128 v[232:235], v145 offset:38912
	ds_read_b128 v[236:239], v145 offset:39936
	s_add_u32 s40, s30, 0x80100
	s_addc_u32 s41, s31, 0
	s_add_i32 m0, s2, 0x4000
	s_nop 0
	global_load_lds_dwordx4 v139, s[40:41]
	s_nop 0
	s_add_i32 m0, s2, 0x6000
	s_nop 0
	global_load_lds_dwordx4 v141, s[40:41]
	s_waitcnt vmcnt(8)
	s_waitcnt lgkmcnt(0)
	s_barrier
	s_setprio 1
	v_mfma_f32_16x16x32_bf16 v[56:59], v[12:15], v[20:23], v[64:67]
	v_mfma_f32_16x16x32_bf16 v[116:119], v[16:19], v[28:31], v[56:59]
	v_mfma_f32_16x16x32_bf16 v[56:59], v[24:27], v[20:23], v[68:71]
	v_mfma_f32_16x16x32_bf16 v[112:115], v[196:199], v[28:31], v[56:59]
	v_mfma_f32_16x16x32_bf16 v[56:59], v[12:15], v[216:219], v[72:75]
	v_mfma_f32_16x16x32_bf16 v[108:111], v[16:19], v[220:223], v[56:59]
	v_mfma_f32_16x16x32_bf16 v[56:59], v[24:27], v[216:219], v[76:79]
	v_mfma_f32_16x16x32_bf16 v[100:103], v[196:199], v[220:223], v[56:59]
	v_mfma_f32_16x16x32_bf16 v[56:59], v[12:15], v[224:227], v[80:83]
	v_mfma_f32_16x16x32_bf16 v[92:95], v[16:19], v[228:231], v[56:59]
	v_mfma_f32_16x16x32_bf16 v[56:59], v[24:27], v[224:227], v[84:87]
	v_mfma_f32_16x16x32_bf16 v[84:87], v[196:199], v[228:231], v[56:59]
	v_mfma_f32_16x16x32_bf16 v[56:59], v[12:15], v[232:235], v[88:91]
	v_mfma_f32_16x16x32_bf16 v[72:75], v[16:19], v[236:239], v[56:59]
	v_mfma_f32_16x16x32_bf16 v[56:59], v[24:27], v[232:235], v[96:99]
	v_mfma_f32_16x16x32_bf16 v[56:59], v[196:199], v[236:239], v[56:59]
	v_mfma_f32_16x16x32_bf16 v[64:67], v[200:203], v[20:23], v[104:107]
	v_mfma_f32_16x16x32_bf16 v[20:23], v[208:211], v[20:23], v[32:35]
	v_mfma_f32_16x16x32_bf16 v[120:123], v[212:215], v[28:31], v[20:23]
	v_mfma_f32_16x16x32_bf16 v[20:23], v[200:203], v[216:219], v[36:39]
	v_mfma_f32_16x16x32_bf16 v[104:107], v[204:207], v[220:223], v[20:23]
	v_mfma_f32_16x16x32_bf16 v[20:23], v[208:211], v[216:219], v[40:43]
	v_mfma_f32_16x16x32_bf16 v[96:99], v[212:215], v[220:223], v[20:23]
	v_mfma_f32_16x16x32_bf16 v[20:23], v[200:203], v[224:227], v[44:47]
	v_mfma_f32_16x16x32_bf16 v[88:91], v[204:207], v[228:231], v[20:23]
	v_mfma_f32_16x16x32_bf16 v[20:23], v[208:211], v[224:227], v[48:51]
	v_mfma_f32_16x16x32_bf16 v[80:83], v[212:215], v[228:231], v[20:23]
	v_mfma_f32_16x16x32_bf16 v[20:23], v[200:203], v[232:235], v[52:55]
	v_mfma_f32_16x16x32_bf16 v[124:127], v[204:207], v[28:31], v[64:67]
	v_mfma_f32_16x16x32_bf16 v[64:67], v[204:207], v[236:239], v[20:23]
	v_mfma_f32_16x16x32_bf16 v[20:23], v[208:211], v[232:235], v[60:63]
	v_mfma_f32_16x16x32_bf16 v[48:51], v[212:215], v[236:239], v[20:23]
	s_setprio 0
	s_barrier
	ds_read_b128 v[32:35], v145 offset:49152
	ds_read_b128 v[40:43], v145 offset:50176
	ds_read_b128 v[216:219], v145 offset:51200
	ds_read_b128 v[220:223], v145 offset:52224
	ds_read_b128 v[224:227], v145 offset:53248
	ds_read_b128 v[228:231], v145 offset:54272
	ds_read_b128 v[232:235], v145 offset:55296
	ds_read_b128 v[236:239], v145 offset:56320
	s_add_i32 m0, s2, 0x18000
	s_nop 0
	global_load_lds_dwordx4 v140, s[38:39]
	s_nop 0
	s_add_i32 m0, s2, 0x1a000
	s_nop 0
	global_load_lds_dwordx4 v142, s[38:39]
	s_add_u32 s38, s34, 0x80180
	s_addc_u32 s39, s35, 0
	s_add_i32 m0, s2, 0x1c000
	s_nop 0
	global_load_lds_dwordx4 v140, s[38:39]
	s_nop 0
	s_add_i32 m0, s2, 0x1e000
	s_nop 0
	global_load_lds_dwordx4 v142, s[38:39]
	s_nop 0
	s_add_i32 m0, s2, 0x8000
	s_nop 0
	global_load_lds_dwordx4 v139, s[36:37]
	s_nop 0
	s_add_i32 m0, s2, 0xa000
	s_nop 0
	global_load_lds_dwordx4 v141, s[36:37]
	s_waitcnt vmcnt(8)
	s_waitcnt lgkmcnt(0)
	s_barrier
	s_setprio 1
	v_mfma_f32_16x16x32_bf16 v[20:23], v[12:15], v[32:35], v[132:135]
	v_mfma_f32_16x16x32_bf16 v[76:79], v[16:19], v[40:43], v[20:23]
	v_mfma_f32_16x16x32_bf16 v[20:23], v[24:27], v[32:35], v[148:151]
	v_mfma_f32_16x16x32_bf16 v[60:63], v[196:199], v[40:43], v[20:23]
	v_mfma_f32_16x16x32_bf16 v[20:23], v[12:15], v[216:219], v[152:155]
	v_mfma_f32_16x16x32_bf16 v[44:47], v[16:19], v[220:223], v[20:23]
	v_mfma_f32_16x16x32_bf16 v[20:23], v[24:27], v[216:219], v[156:159]
	v_mfma_f32_16x16x32_bf16 v[36:39], v[196:199], v[220:223], v[20:23]
	v_mfma_f32_16x16x32_bf16 v[20:23], v[12:15], v[224:227], v[160:163]
	v_mfma_f32_16x16x32_bf16 v[0:3], v[12:15], v[232:235], v[0:3]
	v_mfma_f32_16x16x32_bf16 v[28:31], v[16:19], v[228:231], v[20:23]
	v_mfma_f32_16x16x32_bf16 v[20:23], v[24:27], v[224:227], v[164:167]
	v_mfma_f32_16x16x32_bf16 v[12:15], v[16:19], v[236:239], v[0:3]
	v_mfma_f32_16x16x32_bf16 v[0:3], v[24:27], v[232:235], v[4:7]
	v_mfma_f32_16x16x32_bf16 v[20:23], v[196:199], v[228:231], v[20:23]
	v_mfma_f32_16x16x32_bf16 v[4:7], v[196:199], v[236:239], v[0:3]
	v_mfma_f32_16x16x32_bf16 v[0:3], v[200:203], v[32:35], v[8:11]
	v_mfma_f32_16x16x32_bf16 v[68:71], v[204:207], v[40:43], v[0:3]
	v_mfma_f32_16x16x32_bf16 v[0:3], v[208:211], v[32:35], v[168:171]
	v_mfma_f32_16x16x32_bf16 v[52:55], v[212:215], v[40:43], v[0:3]
	v_mfma_f32_16x16x32_bf16 v[0:3], v[200:203], v[216:219], v[172:175]
	v_mfma_f32_16x16x32_bf16 v[40:43], v[204:207], v[220:223], v[0:3]
	v_mfma_f32_16x16x32_bf16 v[0:3], v[208:211], v[216:219], v[176:179]
	v_mfma_f32_16x16x32_bf16 v[32:35], v[212:215], v[220:223], v[0:3]
	v_mfma_f32_16x16x32_bf16 v[0:3], v[200:203], v[224:227], v[180:183]
	v_mfma_f32_16x16x32_bf16 v[24:27], v[204:207], v[228:231], v[0:3]
	v_mfma_f32_16x16x32_bf16 v[0:3], v[208:211], v[224:227], v[184:187]
	v_mfma_f32_16x16x32_bf16 v[16:19], v[212:215], v[228:231], v[0:3]
	v_mfma_f32_16x16x32_bf16 v[0:3], v[200:203], v[232:235], v[188:191]
	v_mfma_f32_16x16x32_bf16 v[8:11], v[204:207], v[236:239], v[0:3]
	v_mfma_f32_16x16x32_bf16 v[0:3], v[208:211], v[232:235], v[192:195]
	v_mfma_f32_16x16x32_bf16 v[0:3], v[212:215], v[236:239], v[0:3]
	s_setprio 0
	s_barrier
	s_add_u32 s53, s30, 0x200
	s_addc_u32 s54, s31, 0
	s_add_u32 s55, s34, 0x200
	s_addc_u32 s56, s35, 0
	s_add_u32 s30, s30, 0x80180
	s_addc_u32 s31, s31, 0
	s_mov_b32 s57, 0
.LBB0_1109:
	ds_read_b128 v[132:135], v143
	ds_read_b128 v[148:151], v143 offset:1024
	ds_read_b128 v[152:155], v143 offset:2048
	ds_read_b128 v[156:159], v143 offset:3072
	ds_read_b128 v[160:163], v144
	ds_read_b128 v[164:167], v144 offset:1024
	ds_read_b128 v[168:171], v144 offset:2048
	ds_read_b128 v[172:175], v144 offset:3072
	s_cmp_eq_u32 s57, 28
	s_cselect_b32 s40, s51, s53
	s_cselect_b32 s41, s23, s54
	s_cselect_b32 s36, s52, s55
	s_cselect_b32 s37, s21, s56
	s_add_u32 s34, s40, 0x80
	s_addc_u32 s35, s41, 0
	ds_read_b128 v[176:179], v145
	ds_read_b128 v[180:183], v145 offset:1024
	ds_read_b128 v[184:187], v145 offset:2048
	ds_read_b128 v[188:191], v145 offset:3072
	ds_read_b128 v[192:195], v145 offset:4096
	ds_read_b128 v[196:199], v145 offset:5120
	ds_read_b128 v[200:203], v145 offset:6144
	ds_read_b128 v[204:207], v145 offset:7168
	s_add_u32 s38, s36, 0x80
	s_addc_u32 s39, s37, 0
	s_add_i32 m0, s2, 0xc000
	s_nop 0
	global_load_lds_dwordx4 v139, s[30:31]
	s_nop 0
	s_add_i32 m0, s2, 0xe000
	s_nop 0
	global_load_lds_dwordx4 v141, s[30:31]
	s_waitcnt vmcnt(8)
	s_waitcnt lgkmcnt(0)
	s_barrier
	s_setprio 1
	v_mfma_f32_16x16x32_bf16 v[116:119], v[132:135], v[176:179], v[116:119]
	v_mfma_f32_16x16x32_bf16 v[112:115], v[152:155], v[176:179], v[112:115]
	v_mfma_f32_16x16x32_bf16 v[108:111], v[132:135], v[184:187], v[108:111]
	v_mfma_f32_16x16x32_bf16 v[100:103], v[152:155], v[184:187], v[100:103]
	v_mfma_f32_16x16x32_bf16 v[92:95], v[132:135], v[192:195], v[92:95]
	v_mfma_f32_16x16x32_bf16 v[84:87], v[152:155], v[192:195], v[84:87]
	v_mfma_f32_16x16x32_bf16 v[72:75], v[132:135], v[200:203], v[72:75]
	v_mfma_f32_16x16x32_bf16 v[56:59], v[152:155], v[200:203], v[56:59]
	v_mfma_f32_16x16x32_bf16 v[116:119], v[148:151], v[180:183], v[116:119]
	v_mfma_f32_16x16x32_bf16 v[112:115], v[156:159], v[180:183], v[112:115]
	v_mfma_f32_16x16x32_bf16 v[108:111], v[148:151], v[188:191], v[108:111]
	v_mfma_f32_16x16x32_bf16 v[100:103], v[156:159], v[188:191], v[100:103]
	v_mfma_f32_16x16x32_bf16 v[92:95], v[148:151], v[196:199], v[92:95]
	v_mfma_f32_16x16x32_bf16 v[84:87], v[156:159], v[196:199], v[84:87]
	v_mfma_f32_16x16x32_bf16 v[72:75], v[148:151], v[204:207], v[72:75]
	v_mfma_f32_16x16x32_bf16 v[56:59], v[156:159], v[204:207], v[56:59]
	v_mfma_f32_16x16x32_bf16 v[124:127], v[160:163], v[176:179], v[124:127]
	v_mfma_f32_16x16x32_bf16 v[120:123], v[168:171], v[176:179], v[120:123]
	v_mfma_f32_16x16x32_bf16 v[104:107], v[160:163], v[184:187], v[104:107]
	v_mfma_f32_16x16x32_bf16 v[96:99], v[168:171], v[184:187], v[96:99]
	v_mfma_f32_16x16x32_bf16 v[88:91], v[160:163], v[192:195], v[88:91]
	v_mfma_f32_16x16x32_bf16 v[80:83], v[168:171], v[192:195], v[80:83]
	v_mfma_f32_16x16x32_bf16 v[64:67], v[160:163], v[200:203], v[64:67]
	v_mfma_f32_16x16x32_bf16 v[48:51], v[168:171], v[200:203], v[48:51]
	v_mfma_f32_16x16x32_bf16 v[124:127], v[164:167], v[180:183], v[124:127]
	v_mfma_f32_16x16x32_bf16 v[120:123], v[172:175], v[180:183], v[120:123]
	v_mfma_f32_16x16x32_bf16 v[104:107], v[164:167], v[188:191], v[104:107]
	v_mfma_f32_16x16x32_bf16 v[96:99], v[172:175], v[188:191], v[96:99]
	v_mfma_f32_16x16x32_bf16 v[88:91], v[164:167], v[196:199], v[88:91]
	v_mfma_f32_16x16x32_bf16 v[80:83], v[172:175], v[196:199], v[80:83]
	v_mfma_f32_16x16x32_bf16 v[64:67], v[164:167], v[204:207], v[64:67]
	v_mfma_f32_16x16x32_bf16 v[48:51], v[172:175], v[204:207], v[48:51]
	s_setprio 0
	s_barrier
	ds_read_b128 v[176:179], v145 offset:16384
	ds_read_b128 v[180:183], v145 offset:17408
	ds_read_b128 v[184:187], v145 offset:18432
	ds_read_b128 v[188:191], v145 offset:19456
	ds_read_b128 v[192:195], v145 offset:20480
	ds_read_b128 v[196:199], v145 offset:21504
	ds_read_b128 v[200:203], v145 offset:22528
	ds_read_b128 v[204:207], v145 offset:23552
	s_add_i32 m0, s2, 0x10000
	s_nop 0
	global_load_lds_dwordx4 v140, s[36:37]
	s_nop 0
	s_add_i32 m0, s2, 0x12000
	s_nop 0
	global_load_lds_dwordx4 v142, s[36:37]
	s_add_u32 s58, s36, 0x80000
	s_addc_u32 s59, s37, 0
	s_add_i32 m0, s2, 0x14000
	s_nop 0
	global_load_lds_dwordx4 v140, s[58:59]
	s_nop 0
	s_add_i32 m0, s2, 0x16000
	s_nop 0
	global_load_lds_dwordx4 v142, s[58:59]
	s_nop 0
	s_add_i32 m0, s2, 0
	s_nop 0
	global_load_lds_dwordx4 v139, s[40:41]
	s_nop 0
	s_add_i32 m0, s2, 0x2000
	s_nop 0
	global_load_lds_dwordx4 v141, s[40:41]
	s_waitcnt vmcnt(8)
	s_waitcnt lgkmcnt(0)
	s_barrier
	s_setprio 1
	v_mfma_f32_16x16x32_bf16 v[76:79], v[132:135], v[176:179], v[76:79]
	v_mfma_f32_16x16x32_bf16 v[60:63], v[152:155], v[176:179], v[60:63]
	v_mfma_f32_16x16x32_bf16 v[44:47], v[132:135], v[184:187], v[44:47]
	v_mfma_f32_16x16x32_bf16 v[36:39], v[152:155], v[184:187], v[36:39]
	v_mfma_f32_16x16x32_bf16 v[28:31], v[132:135], v[192:195], v[28:31]
	v_mfma_f32_16x16x32_bf16 v[20:23], v[152:155], v[192:195], v[20:23]
	v_mfma_f32_16x16x32_bf16 v[12:15], v[132:135], v[200:203], v[12:15]
	v_mfma_f32_16x16x32_bf16 v[4:7], v[152:155], v[200:203], v[4:7]
	v_mfma_f32_16x16x32_bf16 v[76:79], v[148:151], v[180:183], v[76:79]
	v_mfma_f32_16x16x32_bf16 v[60:63], v[156:159], v[180:183], v[60:63]
	v_mfma_f32_16x16x32_bf16 v[44:47], v[148:151], v[188:191], v[44:47]
	v_mfma_f32_16x16x32_bf16 v[36:39], v[156:159], v[188:191], v[36:39]
	v_mfma_f32_16x16x32_bf16 v[28:31], v[148:151], v[196:199], v[28:31]
	v_mfma_f32_16x16x32_bf16 v[20:23], v[156:159], v[196:199], v[20:23]
	v_mfma_f32_16x16x32_bf16 v[12:15], v[148:151], v[204:207], v[12:15]
	v_mfma_f32_16x16x32_bf16 v[4:7], v[156:159], v[204:207], v[4:7]
	v_mfma_f32_16x16x32_bf16 v[68:71], v[160:163], v[176:179], v[68:71]
	v_mfma_f32_16x16x32_bf16 v[52:55], v[168:171], v[176:179], v[52:55]
	v_mfma_f32_16x16x32_bf16 v[40:43], v[160:163], v[184:187], v[40:43]
	v_mfma_f32_16x16x32_bf16 v[32:35], v[168:171], v[184:187], v[32:35]
	v_mfma_f32_16x16x32_bf16 v[24:27], v[160:163], v[192:195], v[24:27]
	v_mfma_f32_16x16x32_bf16 v[16:19], v[168:171], v[192:195], v[16:19]
	v_mfma_f32_16x16x32_bf16 v[8:11], v[160:163], v[200:203], v[8:11]
	v_mfma_f32_16x16x32_bf16 v[0:3], v[168:171], v[200:203], v[0:3]
	v_mfma_f32_16x16x32_bf16 v[68:71], v[164:167], v[180:183], v[68:71]
	v_mfma_f32_16x16x32_bf16 v[52:55], v[172:175], v[180:183], v[52:55]
	v_mfma_f32_16x16x32_bf16 v[40:43], v[164:167], v[188:191], v[40:43]
	v_mfma_f32_16x16x32_bf16 v[32:35], v[172:175], v[188:191], v[32:35]
	v_mfma_f32_16x16x32_bf16 v[24:27], v[164:167], v[196:199], v[24:27]
	v_mfma_f32_16x16x32_bf16 v[16:19], v[172:175], v[196:199], v[16:19]
	v_mfma_f32_16x16x32_bf16 v[8:11], v[164:167], v[204:207], v[8:11]
	v_mfma_f32_16x16x32_bf16 v[0:3], v[172:175], v[204:207], v[0:3]
	s_setprio 0
	s_barrier
	ds_read_b128 v[132:135], v146
	ds_read_b128 v[148:151], v146 offset:1024
	ds_read_b128 v[152:155], v146 offset:2048
	ds_read_b128 v[156:159], v146 offset:3072
	ds_read_b128 v[160:163], v147
	ds_read_b128 v[164:167], v147 offset:1024
	ds_read_b128 v[168:171], v147 offset:2048
	ds_read_b128 v[172:175], v147 offset:3072
	ds_read_b128 v[176:179], v145 offset:32768
	ds_read_b128 v[180:183], v145 offset:33792
	ds_read_b128 v[184:187], v145 offset:34816
	ds_read_b128 v[188:191], v145 offset:35840
	ds_read_b128 v[192:195], v145 offset:36864
	ds_read_b128 v[196:199], v145 offset:37888
	ds_read_b128 v[200:203], v145 offset:38912
	ds_read_b128 v[204:207], v145 offset:39936
	s_add_u32 s40, s40, 0x80000
	s_addc_u32 s41, s41, 0
	s_add_i32 m0, s2, 0x4000
	s_nop 0
	global_load_lds_dwordx4 v139, s[40:41]
	s_nop 0
	s_add_i32 m0, s2, 0x6000
	s_nop 0
	global_load_lds_dwordx4 v141, s[40:41]
	s_waitcnt vmcnt(8)
	s_waitcnt lgkmcnt(0)
	s_barrier
	s_setprio 1
	v_mfma_f32_16x16x32_bf16 v[116:119], v[132:135], v[176:179], v[116:119]
	v_mfma_f32_16x16x32_bf16 v[112:115], v[152:155], v[176:179], v[112:115]
	v_mfma_f32_16x16x32_bf16 v[108:111], v[132:135], v[184:187], v[108:111]
	v_mfma_f32_16x16x32_bf16 v[100:103], v[152:155], v[184:187], v[100:103]
	v_mfma_f32_16x16x32_bf16 v[92:95], v[132:135], v[192:195], v[92:95]
	v_mfma_f32_16x16x32_bf16 v[84:87], v[152:155], v[192:195], v[84:87]
	v_mfma_f32_16x16x32_bf16 v[72:75], v[132:135], v[200:203], v[72:75]
	v_mfma_f32_16x16x32_bf16 v[56:59], v[152:155], v[200:203], v[56:59]
	v_mfma_f32_16x16x32_bf16 v[116:119], v[148:151], v[180:183], v[116:119]
	v_mfma_f32_16x16x32_bf16 v[112:115], v[156:159], v[180:183], v[112:115]
	v_mfma_f32_16x16x32_bf16 v[108:111], v[148:151], v[188:191], v[108:111]
	v_mfma_f32_16x16x32_bf16 v[100:103], v[156:159], v[188:191], v[100:103]
	v_mfma_f32_16x16x32_bf16 v[92:95], v[148:151], v[196:199], v[92:95]
	v_mfma_f32_16x16x32_bf16 v[84:87], v[156:159], v[196:199], v[84:87]
	v_mfma_f32_16x16x32_bf16 v[72:75], v[148:151], v[204:207], v[72:75]
	v_mfma_f32_16x16x32_bf16 v[56:59], v[156:159], v[204:207], v[56:59]
	v_mfma_f32_16x16x32_bf16 v[124:127], v[160:163], v[176:179], v[124:127]
	v_mfma_f32_16x16x32_bf16 v[120:123], v[168:171], v[176:179], v[120:123]
	v_mfma_f32_16x16x32_bf16 v[104:107], v[160:163], v[184:187], v[104:107]
	v_mfma_f32_16x16x32_bf16 v[96:99], v[168:171], v[184:187], v[96:99]
	v_mfma_f32_16x16x32_bf16 v[88:91], v[160:163], v[192:195], v[88:91]
	v_mfma_f32_16x16x32_bf16 v[80:83], v[168:171], v[192:195], v[80:83]
	v_mfma_f32_16x16x32_bf16 v[64:67], v[160:163], v[200:203], v[64:67]
	v_mfma_f32_16x16x32_bf16 v[48:51], v[168:171], v[200:203], v[48:51]
	v_mfma_f32_16x16x32_bf16 v[124:127], v[164:167], v[180:183], v[124:127]
	v_mfma_f32_16x16x32_bf16 v[120:123], v[172:175], v[180:183], v[120:123]
	v_mfma_f32_16x16x32_bf16 v[104:107], v[164:167], v[188:191], v[104:107]
	v_mfma_f32_16x16x32_bf16 v[96:99], v[172:175], v[188:191], v[96:99]
	v_mfma_f32_16x16x32_bf16 v[88:91], v[164:167], v[196:199], v[88:91]
	v_mfma_f32_16x16x32_bf16 v[80:83], v[172:175], v[196:199], v[80:83]
	v_mfma_f32_16x16x32_bf16 v[64:67], v[164:167], v[204:207], v[64:67]
	v_mfma_f32_16x16x32_bf16 v[48:51], v[172:175], v[204:207], v[48:51]
	s_setprio 0
	s_barrier
	ds_read_b128 v[176:179], v145 offset:49152
	ds_read_b128 v[180:183], v145 offset:50176
	ds_read_b128 v[184:187], v145 offset:51200
	ds_read_b128 v[188:191], v145 offset:52224
	ds_read_b128 v[192:195], v145 offset:53248
	ds_read_b128 v[196:199], v145 offset:54272
	ds_read_b128 v[200:203], v145 offset:55296
	ds_read_b128 v[204:207], v145 offset:56320
	s_add_i32 m0, s2, 0x18000
	s_nop 0
	global_load_lds_dwordx4 v140, s[38:39]
	s_nop 0
	s_add_i32 m0, s2, 0x1a000
	s_nop 0
	global_load_lds_dwordx4 v142, s[38:39]
	s_add_u32 s36, s36, 0x80080
	s_addc_u32 s37, s37, 0
	s_add_i32 m0, s2, 0x1c000
	s_nop 0
	global_load_lds_dwordx4 v140, s[36:37]
	s_nop 0
	s_add_i32 m0, s2, 0x1e000
	s_nop 0
	global_load_lds_dwordx4 v142, s[36:37]
	s_nop 0
	s_add_i32 m0, s2, 0x8000
	s_nop 0
	global_load_lds_dwordx4 v139, s[34:35]
	s_nop 0
	s_add_i32 m0, s2, 0xa000
	s_nop 0
	global_load_lds_dwordx4 v141, s[34:35]
	s_waitcnt vmcnt(8)
	s_waitcnt lgkmcnt(0)
	s_barrier
	s_setprio 1
	v_mfma_f32_16x16x32_bf16 v[76:79], v[132:135], v[176:179], v[76:79]
	v_mfma_f32_16x16x32_bf16 v[60:63], v[152:155], v[176:179], v[60:63]
	v_mfma_f32_16x16x32_bf16 v[44:47], v[132:135], v[184:187], v[44:47]
	v_mfma_f32_16x16x32_bf16 v[36:39], v[152:155], v[184:187], v[36:39]
	v_mfma_f32_16x16x32_bf16 v[28:31], v[132:135], v[192:195], v[28:31]
	v_mfma_f32_16x16x32_bf16 v[20:23], v[152:155], v[192:195], v[20:23]
	v_mfma_f32_16x16x32_bf16 v[12:15], v[132:135], v[200:203], v[12:15]
	v_mfma_f32_16x16x32_bf16 v[4:7], v[152:155], v[200:203], v[4:7]
	v_mfma_f32_16x16x32_bf16 v[76:79], v[148:151], v[180:183], v[76:79]
	v_mfma_f32_16x16x32_bf16 v[60:63], v[156:159], v[180:183], v[60:63]
	v_mfma_f32_16x16x32_bf16 v[44:47], v[148:151], v[188:191], v[44:47]
	v_mfma_f32_16x16x32_bf16 v[36:39], v[156:159], v[188:191], v[36:39]
	v_mfma_f32_16x16x32_bf16 v[28:31], v[148:151], v[196:199], v[28:31]
	v_mfma_f32_16x16x32_bf16 v[20:23], v[156:159], v[196:199], v[20:23]
	v_mfma_f32_16x16x32_bf16 v[12:15], v[148:151], v[204:207], v[12:15]
	v_mfma_f32_16x16x32_bf16 v[4:7], v[156:159], v[204:207], v[4:7]
	v_mfma_f32_16x16x32_bf16 v[68:71], v[160:163], v[176:179], v[68:71]
	v_mfma_f32_16x16x32_bf16 v[52:55], v[168:171], v[176:179], v[52:55]
	v_mfma_f32_16x16x32_bf16 v[40:43], v[160:163], v[184:187], v[40:43]
	v_mfma_f32_16x16x32_bf16 v[32:35], v[168:171], v[184:187], v[32:35]
	v_mfma_f32_16x16x32_bf16 v[24:27], v[160:163], v[192:195], v[24:27]
	v_mfma_f32_16x16x32_bf16 v[16:19], v[168:171], v[192:195], v[16:19]
	v_mfma_f32_16x16x32_bf16 v[8:11], v[160:163], v[200:203], v[8:11]
	v_mfma_f32_16x16x32_bf16 v[0:3], v[168:171], v[200:203], v[0:3]
	v_mfma_f32_16x16x32_bf16 v[68:71], v[164:167], v[180:183], v[68:71]
	v_mfma_f32_16x16x32_bf16 v[52:55], v[172:175], v[180:183], v[52:55]
	v_mfma_f32_16x16x32_bf16 v[40:43], v[164:167], v[188:191], v[40:43]
	v_mfma_f32_16x16x32_bf16 v[32:35], v[172:175], v[188:191], v[32:35]
	v_mfma_f32_16x16x32_bf16 v[24:27], v[164:167], v[196:199], v[24:27]
	v_mfma_f32_16x16x32_bf16 v[16:19], v[172:175], v[196:199], v[16:19]
	v_mfma_f32_16x16x32_bf16 v[8:11], v[164:167], v[204:207], v[8:11]
	v_mfma_f32_16x16x32_bf16 v[0:3], v[172:175], v[204:207], v[0:3]
	s_setprio 0
	s_barrier
	s_add_i32 s57, s57, 2
	s_add_u32 s53, s53, 0x100
	s_addc_u32 s54, s54, 0
	s_add_u32 s55, s55, 0x100
	s_addc_u32 s56, s56, 0
	s_add_u32 s30, s30, 0x100
	s_addc_u32 s31, s31, 0
	s_cmp_gt_u32 s57, 29
	s_cbranch_scc0 .LBB0_1109
	s_and_b64 vcc, exec, s[10:11]
	s_cbranch_vccz .LBB0_1112
	s_barrier

.LBB0_1410:
	ds_read_b128 v[0:3], v138
	ds_read_b128 v[4:7], v138 offset:1024
	ds_read_b128 v[8:11], v138 offset:2048
	ds_read_b128 v[12:15], v138 offset:3072
	ds_read_b128 v[16:19], v139
	ds_read_b128 v[20:23], v139 offset:1024
	ds_read_b128 v[24:27], v139 offset:2048
	ds_read_b128 v[28:31], v139 offset:3072
	s_lshl_b64 s[20:21], s[16:17], 19
	s_add_u32 s20, s39, s20
	s_addc_u32 s21, s40, s21
	s_and_b64 s[6:7], exec, s[6:7]
	s_cselect_b32 s2, s21, s29
	s_cselect_b32 s15, s20, s28
	s_add_u32 s6, s28, 0x100
	s_addc_u32 s7, s29, 0
	s_add_u32 s36, s26, 0x100
	s_addc_u32 s37, s27, 0
	s_add_u32 s30, s28, 0x180
	s_addc_u32 s31, s29, 0
	ds_read_b128 v[32:35], v140
	ds_read_b128 v[36:39], v140 offset:1024
	ds_read_b128 v[40:43], v140 offset:2048
	ds_read_b128 v[44:47], v140 offset:3072
	ds_read_b128 v[48:51], v140 offset:4096
	ds_read_b128 v[52:55], v140 offset:5120
	ds_read_b128 v[56:59], v140 offset:6144
	ds_read_b128 v[60:63], v140 offset:7168
	s_add_u32 s34, s26, 0x180
	s_addc_u32 s35, s27, 0
	s_add_u32 s54, s28, 0x40080
	s_addc_u32 s55, s29, 0
	s_add_i32 m0, s47, 0xc000
	s_nop 0
	global_load_lds_dwordx4 v134, s[54:55]
	s_nop 0
	s_add_i32 m0, s47, 0xe000
	s_nop 0
	global_load_lds_dwordx4 v136, s[54:55]
	s_waitcnt vmcnt(8)
	s_waitcnt lgkmcnt(0)
	s_barrier
	s_setprio 1
	v_mfma_f32_16x16x128_f8f6f4 v[64:67], v[0:7], v[32:39], 0
	v_mfma_f32_16x16x128_f8f6f4 v[68:71], v[8:15], v[32:39], 0
	v_mfma_f32_16x16x128_f8f6f4 v[72:75], v[0:7], v[40:47], 0
	v_mfma_f32_16x16x128_f8f6f4 v[76:79], v[8:15], v[40:47], 0
	v_mfma_f32_16x16x128_f8f6f4 v[80:83], v[0:7], v[48:55], 0
	v_mfma_f32_16x16x128_f8f6f4 v[88:91], v[8:15], v[48:55], 0
	v_mfma_f32_16x16x128_f8f6f4 v[92:95], v[0:7], v[56:63], 0
	v_mfma_f32_16x16x128_f8f6f4 v[104:107], v[8:15], v[56:63], 0
	v_mfma_f32_16x16x128_f8f6f4 v[108:111], v[16:23], v[32:39], 0
	v_mfma_f32_16x16x128_f8f6f4 v[124:127], v[24:31], v[32:39], 0
	v_mfma_f32_16x16x128_f8f6f4 v[162:165], v[16:23], v[40:47], 0
	v_mfma_f32_16x16x128_f8f6f4 v[166:169], v[24:31], v[40:47], 0
	v_mfma_f32_16x16x128_f8f6f4 v[170:173], v[16:23], v[48:55], 0
	v_mfma_f32_16x16x128_f8f6f4 v[174:177], v[24:31], v[48:55], 0
	v_mfma_f32_16x16x128_f8f6f4 v[178:181], v[16:23], v[56:63], 0
	v_mfma_f32_16x16x128_f8f6f4 v[182:185], v[24:31], v[56:63], 0
	s_setprio 0
	s_barrier
	ds_read_b128 v[32:35], v140 offset:16384
	ds_read_b128 v[36:39], v140 offset:17408
	ds_read_b128 v[40:43], v140 offset:18432
	ds_read_b128 v[44:47], v140 offset:19456
	ds_read_b128 v[48:51], v140 offset:20480
	ds_read_b128 v[52:55], v140 offset:21504
	ds_read_b128 v[56:59], v140 offset:22528
	ds_read_b128 v[60:63], v140 offset:23552
	s_add_i32 m0, s47, 0x10000
	s_nop 0
	global_load_lds_dwordx4 v135, s[36:37]
	s_nop 0
	s_add_i32 m0, s47, 0x12000
	s_nop 0
	global_load_lds_dwordx4 v137, s[36:37]
	s_add_u32 s36, s26, 0x40100
	s_addc_u32 s37, s27, 0
	s_add_i32 m0, s47, 0x14000
	s_nop 0
	global_load_lds_dwordx4 v135, s[36:37]
	s_nop 0
	s_add_i32 m0, s47, 0x16000
	s_nop 0
	global_load_lds_dwordx4 v137, s[36:37]
	s_nop 0
	s_add_i32 m0, s47, 0
	s_nop 0
	global_load_lds_dwordx4 v134, s[6:7]
	s_nop 0
	s_add_i32 m0, s47, 0x2000
	s_nop 0
	global_load_lds_dwordx4 v136, s[6:7]
	s_waitcnt vmcnt(8)
	s_waitcnt lgkmcnt(0)
	s_barrier
	s_setprio 1
	v_mfma_f32_16x16x128_f8f6f4 v[186:189], v[0:7], v[32:39], 0
	v_mfma_f32_16x16x128_f8f6f4 v[190:193], v[8:15], v[32:39], 0
	v_mfma_f32_16x16x128_f8f6f4 v[194:197], v[0:7], v[40:47], 0
	v_mfma_f32_16x16x128_f8f6f4 v[198:201], v[8:15], v[40:47], 0
	v_mfma_f32_16x16x128_f8f6f4 v[202:205], v[0:7], v[48:55], 0
	v_mfma_f32_16x16x128_f8f6f4 v[206:209], v[8:15], v[48:55], 0
	v_mfma_f32_16x16x128_f8f6f4 v[210:213], v[0:7], v[56:63], 0
	v_mfma_f32_16x16x128_f8f6f4 v[214:217], v[8:15], v[56:63], 0
	v_mfma_f32_16x16x128_f8f6f4 v[218:221], v[16:23], v[32:39], 0
	v_mfma_f32_16x16x128_f8f6f4 v[222:225], v[24:31], v[32:39], 0
	v_mfma_f32_16x16x128_f8f6f4 v[226:229], v[16:23], v[40:47], 0
	v_mfma_f32_16x16x128_f8f6f4 v[230:233], v[24:31], v[40:47], 0
	v_mfma_f32_16x16x128_f8f6f4 v[234:237], v[16:23], v[48:55], 0
	v_mfma_f32_16x16x128_f8f6f4 v[238:241], v[24:31], v[48:55], 0
	v_mfma_f32_16x16x128_f8f6f4 v[242:245], v[16:23], v[56:63], 0
	v_mfma_f32_16x16x128_f8f6f4 v[246:249], v[24:31], v[56:63], 0
	s_setprio 0
	s_barrier
	ds_read_b128 v[0:3], v141
	ds_read_b128 v[4:7], v141 offset:1024
	ds_read_b128 v[8:11], v141 offset:2048
	ds_read_b128 v[12:15], v141 offset:3072
	ds_read_b128 v[146:149], v142
	ds_read_b128 v[150:153], v142 offset:1024
	ds_read_b128 v[154:157], v142 offset:2048
	ds_read_b128 v[158:161], v142 offset:3072
	ds_read_b128 v[16:19], v140 offset:32768
	ds_read_b128 v[20:23], v140 offset:33792
	ds_read_b128 v[24:27], v140 offset:34816
	ds_read_b128 v[28:31], v140 offset:35840
	ds_read_b128 v[32:35], v140 offset:36864
	ds_read_b128 v[36:39], v140 offset:37888
	ds_read_b128 v[40:43], v140 offset:38912
	ds_read_b128 v[44:47], v140 offset:39936
	s_add_u32 s28, s28, 0x40100
	s_addc_u32 s29, s29, 0
	s_add_i32 m0, s47, 0x4000
	s_nop 0
	global_load_lds_dwordx4 v134, s[28:29]
	s_nop 0
	s_add_i32 m0, s47, 0x6000
	s_nop 0
	global_load_lds_dwordx4 v136, s[28:29]
	s_waitcnt vmcnt(8)
	s_waitcnt lgkmcnt(0)
	s_barrier
	s_setprio 1
	v_mfma_f32_16x16x128_f8f6f4 v[112:115], v[0:7], v[16:23], v[64:67]
	v_mfma_f32_16x16x128_f8f6f4 v[116:119], v[8:15], v[16:23], v[68:71]
	v_mfma_f32_16x16x128_f8f6f4 v[100:103], v[0:7], v[24:31], v[72:75]
	v_mfma_f32_16x16x128_f8f6f4 v[96:99], v[8:15], v[24:31], v[76:79]
	v_mfma_f32_16x16x128_f8f6f4 v[84:87], v[0:7], v[32:39], v[80:83]
	v_mfma_f32_16x16x128_f8f6f4 v[80:83], v[8:15], v[32:39], v[88:91]
	v_mfma_f32_16x16x128_f8f6f4 v[60:63], v[0:7], v[40:47], v[92:95]
	v_mfma_f32_16x16x128_f8f6f4 v[56:59], v[8:15], v[40:47], v[104:107]
	v_mfma_f32_16x16x128_f8f6f4 v[120:123], v[146:153], v[16:23], v[108:111]
	v_mfma_f32_16x16x128_f8f6f4 v[124:127], v[154:161], v[16:23], v[124:127]
	v_mfma_f32_16x16x128_f8f6f4 v[108:111], v[146:153], v[24:31], v[162:165]
	v_mfma_f32_16x16x128_f8f6f4 v[104:107], v[154:161], v[24:31], v[166:169]
	v_mfma_f32_16x16x128_f8f6f4 v[92:95], v[146:153], v[32:39], v[170:173]
	v_mfma_f32_16x16x128_f8f6f4 v[88:91], v[154:161], v[32:39], v[174:177]
	v_mfma_f32_16x16x128_f8f6f4 v[76:79], v[146:153], v[40:47], v[178:181]
	v_mfma_f32_16x16x128_f8f6f4 v[72:75], v[154:161], v[40:47], v[182:185]
	s_setprio 0
	s_barrier
	ds_read_b128 v[24:27], v140 offset:49152
	ds_read_b128 v[28:31], v140 offset:50176
	ds_read_b128 v[162:165], v140 offset:51200
	ds_read_b128 v[166:169], v140 offset:52224
	ds_read_b128 v[170:173], v140 offset:53248
	ds_read_b128 v[174:177], v140 offset:54272
	ds_read_b128 v[178:181], v140 offset:55296
	ds_read_b128 v[182:185], v140 offset:56320
	s_add_i32 m0, s47, 0x18000
	s_nop 0
	global_load_lds_dwordx4 v135, s[34:35]
	s_nop 0
	s_add_i32 m0, s47, 0x1a000
	s_nop 0
	global_load_lds_dwordx4 v137, s[34:35]
	s_add_u32 s28, s26, 0x40180
	s_addc_u32 s29, s27, 0
	s_add_i32 m0, s47, 0x1c000
	s_nop 0
	global_load_lds_dwordx4 v135, s[28:29]
	s_nop 0
	s_add_i32 m0, s47, 0x1e000
	s_nop 0
	global_load_lds_dwordx4 v137, s[28:29]
	s_nop 0
	s_add_i32 m0, s47, 0x8000
	s_nop 0
	global_load_lds_dwordx4 v134, s[30:31]
	s_nop 0
	s_add_i32 m0, s47, 0xa000
	s_nop 0
	global_load_lds_dwordx4 v136, s[30:31]
	s_waitcnt vmcnt(8)
	s_waitcnt lgkmcnt(0)
	s_barrier
	s_setprio 1
	v_mfma_f32_16x16x128_f8f6f4 v[52:55], v[0:7], v[24:31], v[186:189]
	v_mfma_f32_16x16x128_f8f6f4 v[48:51], v[8:15], v[24:31], v[190:193]
	v_mfma_f32_16x16x128_f8f6f4 v[36:39], v[0:7], v[162:169], v[194:197]
	v_mfma_f32_16x16x128_f8f6f4 v[32:35], v[8:15], v[162:169], v[198:201]
	v_mfma_f32_16x16x128_f8f6f4 v[20:23], v[0:7], v[170:177], v[202:205]
	v_mfma_f32_16x16x128_f8f6f4 v[16:19], v[8:15], v[170:177], v[206:209]
	v_mfma_f32_16x16x128_f8f6f4 v[4:7], v[0:7], v[178:185], v[210:213]
	v_mfma_f32_16x16x128_f8f6f4 v[0:3], v[8:15], v[178:185], v[214:217]
	v_mfma_f32_16x16x128_f8f6f4 v[68:71], v[146:153], v[24:31], v[218:221]
	v_mfma_f32_16x16x128_f8f6f4 v[64:67], v[154:161], v[24:31], v[222:225]
	v_mfma_f32_16x16x128_f8f6f4 v[44:47], v[146:153], v[162:169], v[226:229]
	v_mfma_f32_16x16x128_f8f6f4 v[40:43], v[154:161], v[162:169], v[230:233]
	v_mfma_f32_16x16x128_f8f6f4 v[28:31], v[146:153], v[170:177], v[234:237]
	v_mfma_f32_16x16x128_f8f6f4 v[24:27], v[154:161], v[170:177], v[238:241]
	v_mfma_f32_16x16x128_f8f6f4 v[12:15], v[146:153], v[178:185], v[242:245]
	v_mfma_f32_16x16x128_f8f6f4 v[8:11], v[154:161], v[178:185], v[246:249]
	s_setprio 0
	s_barrier
	s_add_u32 s17, s26, 0x200
	s_addc_u32 s54, s27, 0
	s_mov_b32 s55, 0
.LBB0_1411:
	ds_read_b128 v[146:149], v138
	ds_read_b128 v[150:153], v138 offset:1024
	ds_read_b128 v[154:157], v138 offset:2048
	ds_read_b128 v[158:161], v138 offset:3072
	ds_read_b128 v[162:165], v139
	ds_read_b128 v[166:169], v139 offset:1024
	ds_read_b128 v[170:173], v139 offset:2048
	ds_read_b128 v[174:177], v139 offset:3072
	s_add_u32 s26, s6, 0x100
	s_addc_u32 s27, s7, 0
	s_cmp_eq_u32 s55, 12
	s_cselect_b32 s36, s15, s26
	s_cselect_b32 s37, s2, s27
	s_cselect_b32 s30, s18, s17
	s_cselect_b32 s31, s19, s54
	s_add_u32 s28, s36, 0x80
	s_addc_u32 s29, s37, 0
	ds_read_b128 v[178:181], v140
	ds_read_b128 v[182:185], v140 offset:1024
	ds_read_b128 v[186:189], v140 offset:2048
	ds_read_b128 v[190:193], v140 offset:3072
	ds_read_b128 v[194:197], v140 offset:4096
	ds_read_b128 v[198:201], v140 offset:5120
	ds_read_b128 v[202:205], v140 offset:6144
	ds_read_b128 v[206:209], v140 offset:7168
	s_add_u32 s34, s30, 0x80
	s_addc_u32 s35, s31, 0
	s_add_u32 s6, s6, 0x40080
	s_addc_u32 s7, s7, 0
	s_add_i32 m0, s47, 0xc000
	s_nop 0
	global_load_lds_dwordx4 v134, s[6:7]
	s_nop 0
	s_add_i32 m0, s47, 0xe000
	s_nop 0
	global_load_lds_dwordx4 v136, s[6:7]
	s_waitcnt vmcnt(8)
	s_waitcnt lgkmcnt(0)
	s_barrier
	s_setprio 1
	v_mfma_f32_16x16x128_f8f6f4 v[112:115], v[146:153], v[178:185], v[112:115]
	v_mfma_f32_16x16x128_f8f6f4 v[116:119], v[154:161], v[178:185], v[116:119]
	v_mfma_f32_16x16x128_f8f6f4 v[100:103], v[146:153], v[186:193], v[100:103]
	v_mfma_f32_16x16x128_f8f6f4 v[96:99], v[154:161], v[186:193], v[96:99]
	v_mfma_f32_16x16x128_f8f6f4 v[210:213], v[146:153], v[194:201], v[84:87]
	v_mfma_f32_16x16x128_f8f6f4 v[214:217], v[154:161], v[194:201], v[80:83]
	v_mfma_f32_16x16x128_f8f6f4 v[218:221], v[146:153], v[202:209], v[60:63]
	v_mfma_f32_16x16x128_f8f6f4 v[222:225], v[154:161], v[202:209], v[56:59]
	v_mfma_f32_16x16x128_f8f6f4 v[120:123], v[162:169], v[178:185], v[120:123]
	v_mfma_f32_16x16x128_f8f6f4 v[124:127], v[170:177], v[178:185], v[124:127]
	v_mfma_f32_16x16x128_f8f6f4 v[108:111], v[162:169], v[186:193], v[108:111]
	v_mfma_f32_16x16x128_f8f6f4 v[104:107], v[170:177], v[186:193], v[104:107]
	v_mfma_f32_16x16x128_f8f6f4 v[178:181], v[162:169], v[194:201], v[92:95]
	v_mfma_f32_16x16x128_f8f6f4 v[182:185], v[170:177], v[194:201], v[88:91]
	v_mfma_f32_16x16x128_f8f6f4 v[186:189], v[162:169], v[202:209], v[76:79]
	v_mfma_f32_16x16x128_f8f6f4 v[190:193], v[170:177], v[202:209], v[72:75]
	s_setprio 0
	s_barrier
	ds_read_b128 v[56:59], v140 offset:16384
	ds_read_b128 v[60:63], v140 offset:17408
	s_nop 2
	ds_read_b128 v[72:75], v140 offset:18432
	ds_read_b128 v[76:79], v140 offset:19456
	ds_read_b128 v[80:83], v140 offset:20480
	ds_read_b128 v[84:87], v140 offset:21504
	ds_read_b128 v[88:91], v140 offset:22528
	ds_read_b128 v[92:95], v140 offset:23552
	s_add_i32 m0, s47, 0x10000
	s_nop 0
	global_load_lds_dwordx4 v135, s[30:31]
	s_nop 0
	s_add_i32 m0, s47, 0x12000
	s_nop 0
	global_load_lds_dwordx4 v137, s[30:31]
	s_add_u32 s6, s30, 0x40000
	s_addc_u32 s7, s31, 0
	s_add_i32 m0, s47, 0x14000
	s_nop 0
	global_load_lds_dwordx4 v135, s[6:7]
	s_nop 0
	s_add_i32 m0, s47, 0x16000
	s_nop 0
	global_load_lds_dwordx4 v137, s[6:7]
	s_nop 0
	s_add_i32 m0, s47, 0
	s_nop 0
	global_load_lds_dwordx4 v134, s[36:37]
	s_nop 0
	s_add_i32 m0, s47, 0x2000
	s_nop 0
	global_load_lds_dwordx4 v136, s[36:37]
	s_waitcnt vmcnt(8)
	s_waitcnt lgkmcnt(0)
	s_barrier
	s_setprio 1
	v_mfma_f32_16x16x128_f8f6f4 v[52:55], v[146:153], v[56:63], v[52:55]
	v_mfma_f32_16x16x128_f8f6f4 v[48:51], v[154:161], v[56:63], v[48:51]
	v_mfma_f32_16x16x128_f8f6f4 v[194:197], v[146:153], v[72:79], v[36:39]
	v_mfma_f32_16x16x128_f8f6f4 v[198:201], v[154:161], v[72:79], v[32:35]
	v_mfma_f32_16x16x128_f8f6f4 v[202:205], v[146:153], v[80:87], v[20:23]
	v_mfma_f32_16x16x128_f8f6f4 v[206:209], v[154:161], v[80:87], v[16:19]
	v_mfma_f32_16x16x128_f8f6f4 v[226:229], v[146:153], v[88:95], v[4:7]
	v_mfma_f32_16x16x128_f8f6f4 v[230:233], v[154:161], v[88:95], v[0:3]
	v_mfma_f32_16x16x128_f8f6f4 v[68:71], v[162:169], v[56:63], v[68:71]
	v_mfma_f32_16x16x128_f8f6f4 v[64:67], v[170:177], v[56:63], v[64:67]
	v_mfma_f32_16x16x128_f8f6f4 v[234:237], v[162:169], v[72:79], v[44:47]
	v_mfma_f32_16x16x128_f8f6f4 v[238:241], v[170:177], v[72:79], v[40:43]
	v_mfma_f32_16x16x128_f8f6f4 v[242:245], v[162:169], v[80:87], v[28:31]
	v_mfma_f32_16x16x128_f8f6f4 v[246:249], v[170:177], v[80:87], v[24:27]
	v_mfma_f32_16x16x128_f8f6f4 v[250:253], v[162:169], v[88:95], v[12:15]
	v_mfma_f32_16x16x128_f8f6f4 v[130:133], v[170:177], v[88:95], v[8:11]
	s_setprio 0
	s_barrier
	ds_read_b128 v[0:3], v141
	ds_read_b128 v[4:7], v141 offset:1024
	s_nop 2
	ds_read_b128 v[8:11], v141 offset:2048
	ds_read_b128 v[12:15], v141 offset:3072
	ds_read_b128 v[146:149], v142
	ds_read_b128 v[150:153], v142 offset:1024
	ds_read_b128 v[154:157], v142 offset:2048
	ds_read_b128 v[158:161], v142 offset:3072
	ds_read_b128 v[16:19], v140 offset:32768
	ds_read_b128 v[20:23], v140 offset:33792
	ds_read_b128 v[24:27], v140 offset:34816
	ds_read_b128 v[28:31], v140 offset:35840
	ds_read_b128 v[32:35], v140 offset:36864
	ds_read_b128 v[36:39], v140 offset:37888
	ds_read_b128 v[40:43], v140 offset:38912
	ds_read_b128 v[44:47], v140 offset:39936
	s_add_u32 s6, s36, 0x40000
	s_addc_u32 s7, s37, 0
	s_add_i32 m0, s47, 0x4000
	s_nop 0
	global_load_lds_dwordx4 v134, s[6:7]
	s_nop 0
	s_add_i32 m0, s47, 0x6000
	s_nop 0
	global_load_lds_dwordx4 v136, s[6:7]
	s_waitcnt vmcnt(8)
	s_waitcnt lgkmcnt(0)
	s_barrier
	s_setprio 1
	v_mfma_f32_16x16x128_f8f6f4 v[112:115], v[0:7], v[16:23], v[112:115]
	v_mfma_f32_16x16x128_f8f6f4 v[116:119], v[8:15], v[16:23], v[116:119]
	v_mfma_f32_16x16x128_f8f6f4 v[100:103], v[0:7], v[24:31], v[100:103]
	v_mfma_f32_16x16x128_f8f6f4 v[96:99], v[8:15], v[24:31], v[96:99]
	v_mfma_f32_16x16x128_f8f6f4 v[84:87], v[0:7], v[32:39], v[210:213]
	v_mfma_f32_16x16x128_f8f6f4 v[80:83], v[8:15], v[32:39], v[214:217]
	v_mfma_f32_16x16x128_f8f6f4 v[60:63], v[0:7], v[40:47], v[218:221]
	v_mfma_f32_16x16x128_f8f6f4 v[56:59], v[8:15], v[40:47], v[222:225]
	v_mfma_f32_16x16x128_f8f6f4 v[120:123], v[146:153], v[16:23], v[120:123]
	v_mfma_f32_16x16x128_f8f6f4 v[124:127], v[154:161], v[16:23], v[124:127]
	v_mfma_f32_16x16x128_f8f6f4 v[108:111], v[146:153], v[24:31], v[108:111]
	v_mfma_f32_16x16x128_f8f6f4 v[104:107], v[154:161], v[24:31], v[104:107]
	v_mfma_f32_16x16x128_f8f6f4 v[92:95], v[146:153], v[32:39], v[178:181]
	v_mfma_f32_16x16x128_f8f6f4 v[88:91], v[154:161], v[32:39], v[182:185]
	v_mfma_f32_16x16x128_f8f6f4 v[76:79], v[146:153], v[40:47], v[186:189]
	v_mfma_f32_16x16x128_f8f6f4 v[72:75], v[154:161], v[40:47], v[190:193]
	s_setprio 0
	s_barrier
	ds_read_b128 v[24:27], v140 offset:49152
	ds_read_b128 v[28:31], v140 offset:50176
	ds_read_b128 v[162:165], v140 offset:51200
	ds_read_b128 v[166:169], v140 offset:52224
	ds_read_b128 v[170:173], v140 offset:53248
	ds_read_b128 v[174:177], v140 offset:54272
	ds_read_b128 v[178:181], v140 offset:55296
	ds_read_b128 v[182:185], v140 offset:56320
	s_add_i32 m0, s47, 0x18000
	s_nop 0
	global_load_lds_dwordx4 v135, s[34:35]
	s_nop 0
	s_add_i32 m0, s47, 0x1a000
	s_nop 0
	global_load_lds_dwordx4 v137, s[34:35]
	s_add_u32 s6, s30, 0x40080
	s_addc_u32 s7, s31, 0
	s_add_i32 m0, s47, 0x1c000
	s_nop 0
	global_load_lds_dwordx4 v135, s[6:7]
	s_nop 0
	s_add_i32 m0, s47, 0x1e000
	s_nop 0
	global_load_lds_dwordx4 v137, s[6:7]
	s_nop 0
	s_add_i32 m0, s47, 0x8000
	s_nop 0
	global_load_lds_dwordx4 v134, s[28:29]
	s_nop 0
	s_add_i32 m0, s47, 0xa000
	s_nop 0
	global_load_lds_dwordx4 v136, s[28:29]
	s_waitcnt vmcnt(8)
	s_waitcnt lgkmcnt(0)
	s_barrier
	s_setprio 1
	v_mfma_f32_16x16x128_f8f6f4 v[52:55], v[0:7], v[24:31], v[52:55]
	v_mfma_f32_16x16x128_f8f6f4 v[48:51], v[8:15], v[24:31], v[48:51]
	v_mfma_f32_16x16x128_f8f6f4 v[36:39], v[0:7], v[162:169], v[194:197]
	v_mfma_f32_16x16x128_f8f6f4 v[32:35], v[8:15], v[162:169], v[198:201]
	v_mfma_f32_16x16x128_f8f6f4 v[20:23], v[0:7], v[170:177], v[202:205]
	v_mfma_f32_16x16x128_f8f6f4 v[16:19], v[8:15], v[170:177], v[206:209]
	v_mfma_f32_16x16x128_f8f6f4 v[4:7], v[0:7], v[178:185], v[226:229]
	v_mfma_f32_16x16x128_f8f6f4 v[0:3], v[8:15], v[178:185], v[230:233]
	v_mfma_f32_16x16x128_f8f6f4 v[68:71], v[146:153], v[24:31], v[68:71]
	v_mfma_f32_16x16x128_f8f6f4 v[64:67], v[154:161], v[24:31], v[64:67]
	v_mfma_f32_16x16x128_f8f6f4 v[44:47], v[146:153], v[162:169], v[234:237]
	v_mfma_f32_16x16x128_f8f6f4 v[40:43], v[154:161], v[162:169], v[238:241]
	v_mfma_f32_16x16x128_f8f6f4 v[28:31], v[146:153], v[170:177], v[242:245]
	v_mfma_f32_16x16x128_f8f6f4 v[24:27], v[154:161], v[170:177], v[246:249]
	v_mfma_f32_16x16x128_f8f6f4 v[12:15], v[146:153], v[178:185], v[250:253]
	v_mfma_f32_16x16x128_f8f6f4 v[8:11], v[154:161], v[178:185], v[130:133]
	s_setprio 0
	s_barrier
	s_add_i32 s55, s55, 2
	s_add_u32 s17, s17, 0x100
	s_addc_u32 s54, s54, 0
	s_cmp_gt_u32 s55, 13
	s_mov_b64 s[6:7], s[26:27]
	s_cbranch_scc0 .LBB0_1411
	s_and_b64 vcc, exec, s[12:13]
	s_cbranch_vccz .LBB0_1414
	s_barrier

.LBB0_1487:
	ds_read_b128 v[0:3], v153
	ds_read_b128 v[4:7], v153 offset:1024
	ds_read_b128 v[8:11], v153 offset:2048
	ds_read_b128 v[12:15], v153 offset:3072
	ds_read_b128 v[16:19], v154
	ds_read_b128 v[20:23], v154 offset:1024
	ds_read_b128 v[24:27], v154 offset:2048
	ds_read_b128 v[28:31], v154 offset:3072
	s_add_u32 s26, s28, 0x100
	s_addc_u32 s27, s29, 0
	s_add_u32 s36, s24, 0x100
	s_addc_u32 s37, s25, 0
	s_add_u32 s30, s28, 0x180
	s_addc_u32 s31, s29, 0
	ds_read_b128 v[32:35], v155
	ds_read_b128 v[36:39], v155 offset:1024
	ds_read_b128 v[40:43], v155 offset:2048
	ds_read_b128 v[44:47], v155 offset:3072
	ds_read_b128 v[48:51], v155 offset:4096
	ds_read_b128 v[52:55], v155 offset:5120
	ds_read_b128 v[56:59], v155 offset:6144
	ds_read_b128 v[60:63], v155 offset:7168
	s_add_u32 s34, s24, 0x180
	s_addc_u32 s35, s25, 0
	s_add_u32 s52, s28, 0xe0080
	s_addc_u32 s53, s29, 0
	s_add_i32 m0, s44, 0xc000
	s_nop 0
	global_load_lds_dwordx4 v149, s[52:53]
	s_nop 0
	s_add_i32 m0, s44, 0xe000
	s_nop 0
	global_load_lds_dwordx4 v151, s[52:53]
	s_waitcnt vmcnt(8)
	s_waitcnt lgkmcnt(0)
	s_barrier
	s_setprio 1
	v_mfma_f32_16x16x128_f8f6f4 v[64:67], v[0:7], v[32:39], 0
	v_mfma_f32_16x16x128_f8f6f4 v[68:71], v[8:15], v[32:39], 0
	v_mfma_f32_16x16x128_f8f6f4 v[72:75], v[0:7], v[40:47], 0
	v_mfma_f32_16x16x128_f8f6f4 v[76:79], v[8:15], v[40:47], 0
	v_mfma_f32_16x16x128_f8f6f4 v[80:83], v[0:7], v[48:55], 0
	v_mfma_f32_16x16x128_f8f6f4 v[88:91], v[8:15], v[48:55], 0
	v_mfma_f32_16x16x128_f8f6f4 v[92:95], v[0:7], v[56:63], 0
	v_mfma_f32_16x16x128_f8f6f4 v[104:107], v[8:15], v[56:63], 0
	v_mfma_f32_16x16x128_f8f6f4 v[108:111], v[16:23], v[32:39], 0
	v_mfma_f32_16x16x128_f8f6f4 v[124:127], v[24:31], v[32:39], 0
	v_mfma_f32_16x16x128_f8f6f4 v[158:161], v[16:23], v[40:47], 0
	v_mfma_f32_16x16x128_f8f6f4 v[162:165], v[24:31], v[40:47], 0
	v_mfma_f32_16x16x128_f8f6f4 v[166:169], v[16:23], v[48:55], 0
	v_mfma_f32_16x16x128_f8f6f4 v[170:173], v[24:31], v[48:55], 0
	v_mfma_f32_16x16x128_f8f6f4 v[174:177], v[16:23], v[56:63], 0
	v_mfma_f32_16x16x128_f8f6f4 v[178:181], v[24:31], v[56:63], 0
	s_setprio 0
	s_barrier
	ds_read_b128 v[32:35], v155 offset:16384
	ds_read_b128 v[36:39], v155 offset:17408
	ds_read_b128 v[40:43], v155 offset:18432
	ds_read_b128 v[44:47], v155 offset:19456
	ds_read_b128 v[48:51], v155 offset:20480
	ds_read_b128 v[52:55], v155 offset:21504
	ds_read_b128 v[56:59], v155 offset:22528
	ds_read_b128 v[60:63], v155 offset:23552
	s_add_i32 m0, s44, 0x10000
	s_nop 0
	global_load_lds_dwordx4 v150, s[36:37]
	s_nop 0
	s_add_i32 m0, s44, 0x12000
	s_nop 0
	global_load_lds_dwordx4 v152, s[36:37]
	s_add_u32 s36, s24, 0xe0100
	s_addc_u32 s37, s25, 0
	s_add_i32 m0, s44, 0x14000
	s_nop 0
	global_load_lds_dwordx4 v150, s[36:37]
	s_nop 0
	s_add_i32 m0, s44, 0x16000
	s_nop 0
	global_load_lds_dwordx4 v152, s[36:37]
	s_nop 0
	s_add_i32 m0, s44, 0
	s_nop 0
	global_load_lds_dwordx4 v149, s[26:27]
	s_nop 0
	s_add_i32 m0, s44, 0x2000
	s_nop 0
	global_load_lds_dwordx4 v151, s[26:27]
	s_waitcnt vmcnt(8)
	s_waitcnt lgkmcnt(0)
	s_barrier
	s_setprio 1
	v_mfma_f32_16x16x128_f8f6f4 v[190:193], v[0:7], v[32:39], 0
	v_mfma_f32_16x16x128_f8f6f4 v[194:197], v[8:15], v[32:39], 0
	v_mfma_f32_16x16x128_f8f6f4 v[198:201], v[0:7], v[40:47], 0
	v_mfma_f32_16x16x128_f8f6f4 v[202:205], v[8:15], v[40:47], 0
	v_mfma_f32_16x16x128_f8f6f4 v[206:209], v[0:7], v[48:55], 0
	v_mfma_f32_16x16x128_f8f6f4 v[210:213], v[8:15], v[48:55], 0
	v_mfma_f32_16x16x128_f8f6f4 v[214:217], v[0:7], v[56:63], 0
	v_mfma_f32_16x16x128_f8f6f4 v[218:221], v[8:15], v[56:63], 0
	v_mfma_f32_16x16x128_f8f6f4 v[222:225], v[16:23], v[32:39], 0
	v_mfma_f32_16x16x128_f8f6f4 v[226:229], v[24:31], v[32:39], 0
	v_mfma_f32_16x16x128_f8f6f4 v[230:233], v[16:23], v[40:47], 0
	v_mfma_f32_16x16x128_f8f6f4 v[234:237], v[24:31], v[40:47], 0
	v_mfma_f32_16x16x128_f8f6f4 v[238:241], v[16:23], v[48:55], 0
	v_mfma_f32_16x16x128_f8f6f4 v[242:245], v[24:31], v[48:55], 0
	v_mfma_f32_16x16x128_f8f6f4 v[246:249], v[16:23], v[56:63], 0
	v_mfma_f32_16x16x128_f8f6f4 v[250:253], v[24:31], v[56:63], 0
	s_setprio 0
	s_barrier
	ds_read_b128 v[0:3], v156
	ds_read_b128 v[4:7], v156 offset:1024
	ds_read_b128 v[16:19], v156 offset:2048
	ds_read_b128 v[20:23], v156 offset:3072
	ds_read_b128 v[132:135], v157
	ds_read_b128 v[136:139], v157 offset:1024
	ds_read_b128 v[140:143], v157 offset:2048
	ds_read_b128 v[144:147], v157 offset:3072
	ds_read_b128 v[8:11], v155 offset:32768
	ds_read_b128 v[12:15], v155 offset:33792
	ds_read_b128 v[24:27], v155 offset:34816
	ds_read_b128 v[28:31], v155 offset:35840
	ds_read_b128 v[32:35], v155 offset:36864
	ds_read_b128 v[36:39], v155 offset:37888
	ds_read_b128 v[40:43], v155 offset:38912
	ds_read_b128 v[44:47], v155 offset:39936
	s_add_u32 s28, s28, 0xe0100
	s_addc_u32 s29, s29, 0
	s_add_i32 m0, s44, 0x4000
	s_nop 0
	global_load_lds_dwordx4 v149, s[28:29]
	s_nop 0
	s_add_i32 m0, s44, 0x6000
	s_nop 0
	global_load_lds_dwordx4 v151, s[28:29]
	s_waitcnt vmcnt(8)
	s_waitcnt lgkmcnt(0)
	s_barrier
	s_setprio 1
	v_mfma_f32_16x16x128_f8f6f4 v[112:115], v[0:7], v[8:15], v[64:67]
	v_mfma_f32_16x16x128_f8f6f4 v[116:119], v[16:23], v[8:15], v[68:71]
	v_mfma_f32_16x16x128_f8f6f4 v[100:103], v[0:7], v[24:31], v[72:75]
	v_mfma_f32_16x16x128_f8f6f4 v[96:99], v[16:23], v[24:31], v[76:79]
	v_mfma_f32_16x16x128_f8f6f4 v[84:87], v[0:7], v[32:39], v[80:83]
	v_mfma_f32_16x16x128_f8f6f4 v[80:83], v[16:23], v[32:39], v[88:91]
	v_mfma_f32_16x16x128_f8f6f4 v[60:63], v[0:7], v[40:47], v[92:95]
	v_mfma_f32_16x16x128_f8f6f4 v[52:55], v[16:23], v[40:47], v[104:107]
	v_mfma_f32_16x16x128_f8f6f4 v[120:123], v[132:139], v[8:15], v[108:111]
	v_mfma_f32_16x16x128_f8f6f4 v[124:127], v[140:147], v[8:15], v[124:127]
	v_mfma_f32_16x16x128_f8f6f4 v[108:111], v[132:139], v[24:31], v[158:161]
	v_mfma_f32_16x16x128_f8f6f4 v[104:107], v[140:147], v[24:31], v[162:165]
	v_mfma_f32_16x16x128_f8f6f4 v[92:95], v[132:139], v[32:39], v[166:169]
	v_mfma_f32_16x16x128_f8f6f4 v[88:91], v[140:147], v[32:39], v[170:173]
	v_mfma_f32_16x16x128_f8f6f4 v[56:59], v[132:139], v[40:47], v[174:177]
	v_mfma_f32_16x16x128_f8f6f4 v[48:51], v[140:147], v[40:47], v[178:181]
	s_setprio 0
	s_barrier
	ds_read_b128 v[158:161], v155 offset:49152
	ds_read_b128 v[162:165], v155 offset:50176
	ds_read_b128 v[166:169], v155 offset:51200
	ds_read_b128 v[170:173], v155 offset:52224
	ds_read_b128 v[174:177], v155 offset:53248
	ds_read_b128 v[178:181], v155 offset:54272
	ds_read_b128 v[182:185], v155 offset:55296
	ds_read_b128 v[186:189], v155 offset:56320
	s_add_i32 m0, s44, 0x18000
	s_nop 0
	global_load_lds_dwordx4 v150, s[34:35]
	s_nop 0
	s_add_i32 m0, s44, 0x1a000
	s_nop 0
	global_load_lds_dwordx4 v152, s[34:35]
	s_add_u32 s28, s24, 0xe0180
	s_addc_u32 s29, s25, 0
	s_add_i32 m0, s44, 0x1c000
	s_nop 0
	global_load_lds_dwordx4 v150, s[28:29]
	s_nop 0
	s_add_i32 m0, s44, 0x1e000
	s_nop 0
	global_load_lds_dwordx4 v152, s[28:29]
	s_nop 0
	s_add_i32 m0, s44, 0x8000
	s_nop 0
	global_load_lds_dwordx4 v149, s[30:31]
	s_nop 0
	s_add_i32 m0, s44, 0xa000
	s_nop 0
	global_load_lds_dwordx4 v151, s[30:31]
	s_waitcnt vmcnt(8)
	s_waitcnt lgkmcnt(0)
	s_barrier
	s_setprio 1
	v_mfma_f32_16x16x128_f8f6f4 v[68:71], v[0:7], v[158:165], v[190:193]
	v_mfma_f32_16x16x128_f8f6f4 v[64:67], v[16:23], v[158:165], v[194:197]
	v_mfma_f32_16x16x128_f8f6f4 v[44:47], v[0:7], v[166:173], v[198:201]
	v_mfma_f32_16x16x128_f8f6f4 v[36:39], v[16:23], v[166:173], v[202:205]
	v_mfma_f32_16x16x128_f8f6f4 v[28:31], v[0:7], v[174:181], v[206:209]
	v_mfma_f32_16x16x128_f8f6f4 v[24:27], v[16:23], v[174:181], v[210:213]
	v_mfma_f32_16x16x128_f8f6f4 v[12:15], v[0:7], v[182:189], v[214:217]
	v_mfma_f32_16x16x128_f8f6f4 v[8:11], v[16:23], v[182:189], v[218:221]
	v_mfma_f32_16x16x128_f8f6f4 v[76:79], v[132:139], v[158:165], v[222:225]
	v_mfma_f32_16x16x128_f8f6f4 v[72:75], v[140:147], v[158:165], v[226:229]
	v_mfma_f32_16x16x128_f8f6f4 v[40:43], v[132:139], v[166:173], v[230:233]
	v_mfma_f32_16x16x128_f8f6f4 v[32:35], v[140:147], v[166:173], v[234:237]
	v_mfma_f32_16x16x128_f8f6f4 v[20:23], v[132:139], v[174:181], v[238:241]
	v_mfma_f32_16x16x128_f8f6f4 v[16:19], v[140:147], v[174:181], v[242:245]
	v_mfma_f32_16x16x128_f8f6f4 v[4:7], v[132:139], v[182:189], v[246:249]
	v_mfma_f32_16x16x128_f8f6f4 v[0:3], v[140:147], v[182:189], v[250:253]
	s_setprio 0
	s_barrier
	s_add_u32 s23, s24, 0x200
	s_addc_u32 s51, s25, 0
	s_mov_b32 s52, 0
.LBB0_1488:
	ds_read_b128 v[132:135], v153
	ds_read_b128 v[136:139], v153 offset:1024
	ds_read_b128 v[140:143], v153 offset:2048
	ds_read_b128 v[144:147], v153 offset:3072
	ds_read_b128 v[158:161], v154
	ds_read_b128 v[162:165], v154 offset:1024
	ds_read_b128 v[166:169], v154 offset:2048
	ds_read_b128 v[170:173], v154 offset:3072
	s_add_u32 s24, s26, 0x100
	s_addc_u32 s25, s27, 0
	s_cmp_eq_u32 s52, 52
	s_cselect_b32 s36, s6, s24
	s_cselect_b32 s37, s7, s25
	s_cselect_b32 s30, s20, s23
	s_cselect_b32 s31, s21, s51
	s_add_u32 s28, s36, 0x80
	s_addc_u32 s29, s37, 0
	ds_read_b128 v[174:177], v155
	ds_read_b128 v[178:181], v155 offset:1024
	ds_read_b128 v[182:185], v155 offset:2048
	ds_read_b128 v[186:189], v155 offset:3072
	ds_read_b128 v[190:193], v155 offset:4096
	ds_read_b128 v[194:197], v155 offset:5120
	ds_read_b128 v[198:201], v155 offset:6144
	ds_read_b128 v[202:205], v155 offset:7168
	s_add_u32 s34, s30, 0x80
	s_addc_u32 s35, s31, 0
	s_add_u32 s26, s26, 0xe0080
	s_addc_u32 s27, s27, 0
	s_add_i32 m0, s44, 0xc000
	s_nop 0
	global_load_lds_dwordx4 v149, s[26:27]
	s_nop 0
	s_add_i32 m0, s44, 0xe000
	s_nop 0
	global_load_lds_dwordx4 v151, s[26:27]
	s_waitcnt vmcnt(8)
	s_waitcnt lgkmcnt(0)
	s_barrier
	s_setprio 1
	v_mfma_f32_16x16x128_f8f6f4 v[112:115], v[132:139], v[174:181], v[112:115]
	v_mfma_f32_16x16x128_f8f6f4 v[116:119], v[140:147], v[174:181], v[116:119]
	v_mfma_f32_16x16x128_f8f6f4 v[100:103], v[132:139], v[182:189], v[100:103]
	v_mfma_f32_16x16x128_f8f6f4 v[96:99], v[140:147], v[182:189], v[96:99]
	v_mfma_f32_16x16x128_f8f6f4 v[206:209], v[132:139], v[190:197], v[84:87]
	v_mfma_f32_16x16x128_f8f6f4 v[210:213], v[140:147], v[190:197], v[80:83]
	v_mfma_f32_16x16x128_f8f6f4 v[214:217], v[132:139], v[198:205], v[60:63]
	v_mfma_f32_16x16x128_f8f6f4 v[218:221], v[140:147], v[198:205], v[52:55]
	v_mfma_f32_16x16x128_f8f6f4 v[120:123], v[158:165], v[174:181], v[120:123]
	v_mfma_f32_16x16x128_f8f6f4 v[124:127], v[166:173], v[174:181], v[124:127]
	v_mfma_f32_16x16x128_f8f6f4 v[108:111], v[158:165], v[182:189], v[108:111]
	v_mfma_f32_16x16x128_f8f6f4 v[104:107], v[166:173], v[182:189], v[104:107]
	v_mfma_f32_16x16x128_f8f6f4 v[174:177], v[158:165], v[190:197], v[92:95]
	v_mfma_f32_16x16x128_f8f6f4 v[178:181], v[166:173], v[190:197], v[88:91]
	v_mfma_f32_16x16x128_f8f6f4 v[182:185], v[158:165], v[198:205], v[56:59]
	v_mfma_f32_16x16x128_f8f6f4 v[186:189], v[166:173], v[198:205], v[48:51]
	s_setprio 0
	s_barrier
	s_nop 4
	ds_read_b128 v[48:51], v155 offset:16384
	ds_read_b128 v[52:55], v155 offset:17408
	ds_read_b128 v[56:59], v155 offset:18432
	ds_read_b128 v[60:63], v155 offset:19456
	ds_read_b128 v[80:83], v155 offset:20480
	ds_read_b128 v[84:87], v155 offset:21504
	ds_read_b128 v[88:91], v155 offset:22528
	ds_read_b128 v[92:95], v155 offset:23552
	s_add_i32 m0, s44, 0x10000
	s_nop 0
	global_load_lds_dwordx4 v150, s[30:31]
	s_nop 0
	s_add_i32 m0, s44, 0x12000
	s_nop 0
	global_load_lds_dwordx4 v152, s[30:31]
	s_add_u32 s26, s30, 0xe0000
	s_addc_u32 s27, s31, 0
	s_add_i32 m0, s44, 0x14000
	s_nop 0
	global_load_lds_dwordx4 v150, s[26:27]
	s_nop 0
	s_add_i32 m0, s44, 0x16000
	s_nop 0
	global_load_lds_dwordx4 v152, s[26:27]
	s_nop 0
	s_add_i32 m0, s44, 0
	s_nop 0
	global_load_lds_dwordx4 v149, s[36:37]
	s_nop 0
	s_add_i32 m0, s44, 0x2000
	s_nop 0
	global_load_lds_dwordx4 v151, s[36:37]
	s_waitcnt vmcnt(8)
	s_waitcnt lgkmcnt(0)
	s_barrier
	s_setprio 1
	v_mfma_f32_16x16x128_f8f6f4 v[68:71], v[132:139], v[48:55], v[68:71]
	v_mfma_f32_16x16x128_f8f6f4 v[64:67], v[140:147], v[48:55], v[64:67]
	v_mfma_f32_16x16x128_f8f6f4 v[190:193], v[132:139], v[56:63], v[44:47]
	v_mfma_f32_16x16x128_f8f6f4 v[194:197], v[140:147], v[56:63], v[36:39]
	v_mfma_f32_16x16x128_f8f6f4 v[198:201], v[132:139], v[80:87], v[28:31]
	v_mfma_f32_16x16x128_f8f6f4 v[202:205], v[140:147], v[80:87], v[24:27]
	v_mfma_f32_16x16x128_f8f6f4 v[222:225], v[132:139], v[88:95], v[12:15]
	v_mfma_f32_16x16x128_f8f6f4 v[226:229], v[140:147], v[88:95], v[8:11]
	v_mfma_f32_16x16x128_f8f6f4 v[76:79], v[158:165], v[48:55], v[76:79]
	v_mfma_f32_16x16x128_f8f6f4 v[72:75], v[166:173], v[48:55], v[72:75]
	v_mfma_f32_16x16x128_f8f6f4 v[230:233], v[158:165], v[56:63], v[40:43]
	v_mfma_f32_16x16x128_f8f6f4 v[234:237], v[166:173], v[56:63], v[32:35]
	v_mfma_f32_16x16x128_f8f6f4 v[238:241], v[158:165], v[80:87], v[20:23]
	v_mfma_f32_16x16x128_f8f6f4 v[242:245], v[166:173], v[80:87], v[16:19]
	v_mfma_f32_16x16x128_f8f6f4 v[246:249], v[158:165], v[88:95], v[4:7]
	v_mfma_f32_16x16x128_f8f6f4 v[250:253], v[166:173], v[88:95], v[0:3]
	s_setprio 0
	s_barrier
	s_nop 4
	ds_read_b128 v[0:3], v156
	ds_read_b128 v[4:7], v156 offset:1024
	ds_read_b128 v[16:19], v156 offset:2048
	ds_read_b128 v[20:23], v156 offset:3072
	ds_read_b128 v[132:135], v157
	ds_read_b128 v[136:139], v157 offset:1024
	ds_read_b128 v[140:143], v157 offset:2048
	ds_read_b128 v[144:147], v157 offset:3072
	ds_read_b128 v[8:11], v155 offset:32768
	ds_read_b128 v[12:15], v155 offset:33792
	ds_read_b128 v[24:27], v155 offset:34816
	ds_read_b128 v[28:31], v155 offset:35840
	ds_read_b128 v[32:35], v155 offset:36864
	ds_read_b128 v[36:39], v155 offset:37888
	ds_read_b128 v[40:43], v155 offset:38912
	ds_read_b128 v[44:47], v155 offset:39936
	s_add_u32 s26, s36, 0xe0000
	s_addc_u32 s27, s37, 0
	s_add_i32 m0, s44, 0x4000
	s_nop 0
	global_load_lds_dwordx4 v149, s[26:27]
	s_nop 0
	s_add_i32 m0, s44, 0x6000
	s_nop 0
	global_load_lds_dwordx4 v151, s[26:27]
	s_waitcnt vmcnt(8)
	s_waitcnt lgkmcnt(0)
	s_barrier
	s_setprio 1
	v_mfma_f32_16x16x128_f8f6f4 v[112:115], v[0:7], v[8:15], v[112:115]
	v_mfma_f32_16x16x128_f8f6f4 v[116:119], v[16:23], v[8:15], v[116:119]
	v_mfma_f32_16x16x128_f8f6f4 v[100:103], v[0:7], v[24:31], v[100:103]
	v_mfma_f32_16x16x128_f8f6f4 v[96:99], v[16:23], v[24:31], v[96:99]
	v_mfma_f32_16x16x128_f8f6f4 v[84:87], v[0:7], v[32:39], v[206:209]
	v_mfma_f32_16x16x128_f8f6f4 v[80:83], v[16:23], v[32:39], v[210:213]
	v_mfma_f32_16x16x128_f8f6f4 v[60:63], v[0:7], v[40:47], v[214:217]
	v_mfma_f32_16x16x128_f8f6f4 v[52:55], v[16:23], v[40:47], v[218:221]
	v_mfma_f32_16x16x128_f8f6f4 v[120:123], v[132:139], v[8:15], v[120:123]
	v_mfma_f32_16x16x128_f8f6f4 v[124:127], v[140:147], v[8:15], v[124:127]
	v_mfma_f32_16x16x128_f8f6f4 v[108:111], v[132:139], v[24:31], v[108:111]
	v_mfma_f32_16x16x128_f8f6f4 v[104:107], v[140:147], v[24:31], v[104:107]
	v_mfma_f32_16x16x128_f8f6f4 v[92:95], v[132:139], v[32:39], v[174:177]
	v_mfma_f32_16x16x128_f8f6f4 v[88:91], v[140:147], v[32:39], v[178:181]
	v_mfma_f32_16x16x128_f8f6f4 v[56:59], v[132:139], v[40:47], v[182:185]
	v_mfma_f32_16x16x128_f8f6f4 v[48:51], v[140:147], v[40:47], v[186:189]
	s_setprio 0
	s_barrier
	ds_read_b128 v[158:161], v155 offset:49152
	ds_read_b128 v[162:165], v155 offset:50176
	ds_read_b128 v[166:169], v155 offset:51200
	ds_read_b128 v[170:173], v155 offset:52224
	ds_read_b128 v[174:177], v155 offset:53248
	ds_read_b128 v[178:181], v155 offset:54272
	ds_read_b128 v[182:185], v155 offset:55296
	ds_read_b128 v[186:189], v155 offset:56320
	s_add_i32 m0, s44, 0x18000
	s_nop 0
	global_load_lds_dwordx4 v150, s[34:35]
	s_nop 0
	s_add_i32 m0, s44, 0x1a000
	s_nop 0
	global_load_lds_dwordx4 v152, s[34:35]
	s_add_u32 s26, s30, 0xe0080
	s_addc_u32 s27, s31, 0
	s_add_i32 m0, s44, 0x1c000
	s_nop 0
	global_load_lds_dwordx4 v150, s[26:27]
	s_nop 0
	s_add_i32 m0, s44, 0x1e000
	s_nop 0
	global_load_lds_dwordx4 v152, s[26:27]
	s_nop 0
	s_add_i32 m0, s44, 0x8000
	s_nop 0
	global_load_lds_dwordx4 v149, s[28:29]
	s_nop 0
	s_add_i32 m0, s44, 0xa000
	s_nop 0
	global_load_lds_dwordx4 v151, s[28:29]
	s_waitcnt vmcnt(8)
	s_waitcnt lgkmcnt(0)
	s_barrier
	s_setprio 1
	v_mfma_f32_16x16x128_f8f6f4 v[68:71], v[0:7], v[158:165], v[68:71]
	v_mfma_f32_16x16x128_f8f6f4 v[64:67], v[16:23], v[158:165], v[64:67]
	v_mfma_f32_16x16x128_f8f6f4 v[44:47], v[0:7], v[166:173], v[190:193]
	v_mfma_f32_16x16x128_f8f6f4 v[36:39], v[16:23], v[166:173], v[194:197]
	v_mfma_f32_16x16x128_f8f6f4 v[28:31], v[0:7], v[174:181], v[198:201]
	v_mfma_f32_16x16x128_f8f6f4 v[24:27], v[16:23], v[174:181], v[202:205]
	v_mfma_f32_16x16x128_f8f6f4 v[12:15], v[0:7], v[182:189], v[222:225]
	v_mfma_f32_16x16x128_f8f6f4 v[8:11], v[16:23], v[182:189], v[226:229]
	v_mfma_f32_16x16x128_f8f6f4 v[76:79], v[132:139], v[158:165], v[76:79]
	v_mfma_f32_16x16x128_f8f6f4 v[72:75], v[140:147], v[158:165], v[72:75]
	v_mfma_f32_16x16x128_f8f6f4 v[40:43], v[132:139], v[166:173], v[230:233]
	v_mfma_f32_16x16x128_f8f6f4 v[32:35], v[140:147], v[166:173], v[234:237]
	v_mfma_f32_16x16x128_f8f6f4 v[20:23], v[132:139], v[174:181], v[238:241]
	v_mfma_f32_16x16x128_f8f6f4 v[16:19], v[140:147], v[174:181], v[242:245]
	v_mfma_f32_16x16x128_f8f6f4 v[4:7], v[132:139], v[182:189], v[246:249]
	v_mfma_f32_16x16x128_f8f6f4 v[0:3], v[140:147], v[182:189], v[250:253]
	s_setprio 0
	s_barrier
	s_add_i32 s52, s52, 2
	s_add_u32 s23, s23, 0x100
	s_addc_u32 s51, s51, 0
	s_cmp_gt_u32 s52, 53
	s_mov_b64 s[26:27], s[24:25]
	s_cbranch_scc0 .LBB0_1488
	s_and_b64 vcc, exec, s[16:17]
	s_cbranch_vccz .LBB0_1491
	s_barrier
